# baseline (speedup 1.0000x reference)
_Z9convert_wPKfP15HIP_vector_typeIjLj4EEPjPy:
	s_load_dwordx4 s[4:7], s[0:1], 0x0
	s_load_dwordx2 s[8:9], s[0:1], 0x10
	v_lshl_or_b32 v1, s2, 8, v0
	v_lshlrev_b32_e32 v2, 5, v1
	v_lshlrev_b32_e32 v3, 4, v1
	v_mov_b32_e32 v4, 0
	v_mov_b32_e32 v5, 0
	v_mov_b32_e32 v6, 0
	v_mov_b32_e32 v7, 0
	s_waitcnt lgkmcnt(0)
	global_load_dwordx4 v[8:11], v2, s[4:5]
	global_load_dwordx4 v[12:15], v2, s[4:5] offset:16
	global_store_dwordx4 v3, v[4:7], s[8:9]
	v_lshrrev_b32_e32 v16, 7, v1
	v_and_b32_e32 v17, 0x7f, v1
	v_lshrrev_b32_e32 v18, 7, v16
	v_bfe_u32 v19, v16, 5, 2
	v_lshl_add_u32 v18, v18, 2, v19
	v_lshlrev_b32_e32 v18, 12, v18
	v_lshrrev_b32_e32 v19, 1, v17
	v_lshl_add_u32 v18, v19, 6, v18
	v_and_b32_e32 v19, 1, v17
	v_lshl_add_u32 v18, v19, 5, v18
	v_and_b32_e32 v19, 31, v16
	v_add_lshl_u32 v18, v18, v19, 4
	s_waitcnt vmcnt(1)
	v_cvt_pk_f16_f32 v20, v8, v9
	v_cvt_pk_f16_f32 v21, v10, v11
	v_cvt_pk_f16_f32 v22, v12, v13
	v_cvt_pk_f16_f32 v23, v14, v15
	global_store_dwordx4 v18, v[20:23], s[6:7]
	s_endpgm

	.amdhsa_kernel _Z9convert_wPKfP15HIP_vector_typeIjLj4EEPjPy
		.amdhsa_group_segment_fixed_size 0
		.amdhsa_private_segment_fixed_size 0
		.amdhsa_kernarg_size 32
		.amdhsa_user_sgpr_count 2
		.amdhsa_user_sgpr_dispatch_ptr 0
		.amdhsa_user_sgpr_queue_ptr 0
		.amdhsa_user_sgpr_kernarg_segment_ptr 1
		.amdhsa_user_sgpr_dispatch_id 0
		.amdhsa_user_sgpr_kernarg_preload_length 0
		.amdhsa_user_sgpr_kernarg_preload_offset 0
		.amdhsa_user_sgpr_private_segment_size 0
		.amdhsa_uses_dynamic_stack 0
		.amdhsa_enable_private_segment 0
		.amdhsa_system_sgpr_workgroup_id_x 1
		.amdhsa_system_sgpr_workgroup_id_y 0
		.amdhsa_system_sgpr_workgroup_id_z 0
		.amdhsa_system_sgpr_workgroup_info 0
		.amdhsa_system_vgpr_workitem_id 0
		.amdhsa_next_free_vgpr 24
		.amdhsa_next_free_sgpr 12
		.amdhsa_accum_offset 24
		.amdhsa_reserve_vcc 1
		.amdhsa_float_round_mode_32 0
		.amdhsa_float_round_mode_16_64 0
		.amdhsa_float_denorm_mode_32 3
		.amdhsa_float_denorm_mode_16_64 3
		.amdhsa_dx10_clamp 1
		.amdhsa_ieee_mode 1
		.amdhsa_fp16_overflow 0
		.amdhsa_tg_split 0
		.amdhsa_exception_fp_ieee_invalid_op 0
		.amdhsa_exception_fp_denorm_src 0
		.amdhsa_exception_fp_ieee_div_zero 0
		.amdhsa_exception_fp_ieee_overflow 0
		.amdhsa_exception_fp_ieee_underflow 0
		.amdhsa_exception_fp_ieee_inexact 0
		.amdhsa_exception_int_div_zero 0
	.end_amdhsa_kernel

_Z9fused_oscPKfS0_PK15HIP_vector_typeIjLj4EEPfPyPj:
	s_load_dwordx4 s[4:7], s[0:1], 0x0
	s_load_dwordx4 s[8:11], s[0:1], 0x10
	s_load_dwordx4 s[12:15], s[0:1], 0x20
	v_and_b32_e32 v210, 63, v0
	v_lshrrev_b32_e32 v1, 6, v0
	v_and_b32_e32 v211, 31, v0
	v_bfe_u32 v212, v0, 5, 1
	s_nop 0
	v_readfirstlane_b32 s3, v1
	v_cmp_eq_u32_e32 vcc, 0, v0
	s_and_saveexec_b64 s[16:17], vcc
	s_cbranch_execz .Ltk_skip
	v_mov_b32_e32 v1, 0
	v_mov_b32_e32 v2, 1
	s_waitcnt lgkmcnt(0)
	global_atomic_add v3, v1, v2, s[14:15] sc0
	v_mov_b32_e32 v1, 0x20400
	s_waitcnt vmcnt(0)
	ds_write_b32 v1, v3
	s_waitcnt lgkmcnt(0)
.Ltk_skip:
	s_or_b64 exec, exec, s[16:17]
	s_waitcnt lgkmcnt(0)
	s_barrier
	v_mov_b32_e32 v1, 0x20400
	ds_read_b32 v2, v1
	s_waitcnt lgkmcnt(0)
	v_readfirstlane_b32 s16, v2
	s_and_b32 s17, s16, 3
	s_lshr_b32 s18, s16, 2
	s_lshl_b32 s19, s17, 12
	s_lshl_b32 s20, s18, 6
	s_add_u32 s19, s19, s20
	s_lshl_b32 s20, s19, 12
	s_add_u32 s22, s4, s20
	s_addc_u32 s23, s5, 0
	s_add_u32 s24, s22, 0x10000
	s_addc_u32 s25, s23, 0
	s_add_u32 s26, s24, 0x10000
	s_addc_u32 s27, s25, 0
	s_add_u32 s28, s26, 0x10000
	s_addc_u32 s29, s27, 0
	s_add_u32 s30, s10, s20
	s_addc_u32 s31, s11, 0
	s_add_u32 s32, s30, 0x4000000
	s_addc_u32 s33, s31, 0
	s_add_u32 s34, s32, 0x4000000
	s_addc_u32 s35, s33, 0
	s_lshl_b32 s20, s3, 18
	s_add_u32 s36, s8, s20
	s_addc_u32 s37, s9, 0
	s_mul_i32 s20, s17, 63
	s_lshl_b32 s20, s20, 13
	s_add_u32 s20, s20, 0x8000
	s_add_u32 s38, s14, s20
	s_addc_u32 s39, s15, 0
	s_lshl_b32 s20, s18, 13
	s_add_u32 s48, s38, s20
	s_addc_u32 s49, s39, 0
	s_add_u32 s52, s14, 0x1000
	s_addc_u32 s53, s15, 0
	s_cmp_eq_u32 s18, 63
	s_cselect_b32 s48, s52, s48
	s_cselect_b32 s49, s53, s49
	s_add_u32 s50, s38, 0x20000
	s_addc_u32 s51, s39, 0
	s_mov_b32 s42, 0x41a00000
	s_mov_b32 s62, 0x3dcccccd
	v_and_b32_e32 v1, 1, v0
	v_cmp_eq_u32_e64 s[54:55], 0, v1
	v_cmp_ne_u32_e64 s[56:57], 0, v1
	v_and_b32_e32 v1, 2, v0
	v_cmp_eq_u32_e64 s[58:59], 0, v1
	v_cmp_ne_u32_e64 s[60:61], 0, v1
	v_mov_b32_e32 v1, s3
	v_lshl_or_b32 v223, v1, 7, v211
	v_lshlrev_b32_e32 v223, 2, v223
	v_bfe_u32 v1, v211, 2, 1
	v_and_b32_e32 v2, 3, v211
	v_lshrrev_b32_e32 v3, 3, v211
	v_lshl_add_u32 v2, v3, 2, v2
	v_lshl_add_u32 v1, v1, 5, v2
	v_mul_u32_u24_e32 v1, 0x810, v1
	v_lshl_add_u32 v213, v212, 4, v1
	v_lshlrev_b32_e32 v214, 4, v210
	v_and_b32_e32 v1, 3, v210
	v_lshl_add_u32 v1, v212, 5, v1
	v_lshlrev_b32_e32 v1, 12, v1
	v_lshrrev_b32_e32 v2, 2, v211
	v_lshl_add_u32 v1, v2, 4, v1
	s_lshl_b32 s20, s3, 7
	v_add_u32_e32 v253, s20, v1
	v_xor_b32_e32 v224, 32, v210
	v_lshlrev_b32_e32 v224, 2, v224
	v_cmp_ne_u32_e64 s[46:47], 0, v212
	v_lshlrev_b32_e32 v1, 5, v212
	v_sub_u32_e32 v1, s18, v1
	v_max_i32_e32 v225, 0, v1
	v_bfm_b32 v1, v225, 0
	v_mov_b32_e32 v2, -1
	v_cmp_lt_u32_e32 vcc, 31, v225
	s_nop 1
	v_cndmask_b32_e32 v1, v1, v2, vcc
	v_and_b32_e32 v226, 0xffff, v1
	v_lshrrev_b32_e32 v227, 16, v1
	global_load_dword v216, v223, s[6:7]
	global_load_dword v217, v223, s[6:7] offset:128
	global_load_dword v218, v223, s[6:7] offset:256
	global_load_dword v219, v223, s[6:7] offset:384
	v_lshrrev_b32_e32 v1, 5, v0
	v_and_b32_e32 v2, 31, v0
	v_lshlrev_b32_e32 v3, 12, v1
	v_lshl_add_u32 v245, v2, 4, v3
	v_mul_u32_u24_e32 v3, 0x810, v1
	v_lshl_add_u32 v246, v2, 3, v3
	v_add_u32_e32 v247, 0x10200, v246
	global_load_dwordx4 v[34:37], v245, s[22:23]
	global_load_dwordx4 v[38:41], v245, s[24:25]
	global_load_dwordx4 v[42:45], v245, s[26:27]
	global_load_dwordx4 v[46:49], v245, s[28:29]
	global_load_dwordx4 v[50:53], v245, s[22:23] offset:512
	global_load_dwordx4 v[54:57], v245, s[24:25] offset:512
	global_load_dwordx4 v[58:61], v245, s[26:27] offset:512
	global_load_dwordx4 v[62:65], v245, s[28:29] offset:512
	global_load_dwordx4 v[66:69], v245, s[22:23] offset:1024
	global_load_dwordx4 v[70:73], v245, s[24:25] offset:1024
	global_load_dwordx4 v[74:77], v245, s[26:27] offset:1024
	global_load_dwordx4 v[78:81], v245, s[28:29] offset:1024
	global_load_dwordx4 v[82:85], v245, s[22:23] offset:1536
	global_load_dwordx4 v[86:89], v245, s[24:25] offset:1536
	global_load_dwordx4 v[90:93], v245, s[26:27] offset:1536
	global_load_dwordx4 v[94:97], v245, s[28:29] offset:1536
	global_load_dwordx4 v[114:117], v245, s[22:23] offset:2048
	global_load_dwordx4 v[118:121], v245, s[24:25] offset:2048
	global_load_dwordx4 v[122:125], v245, s[26:27] offset:2048
	global_load_dwordx4 v[126:129], v245, s[28:29] offset:2048
	global_load_dwordx4 v[130:133], v245, s[22:23] offset:2560
	global_load_dwordx4 v[134:137], v245, s[24:25] offset:2560
	global_load_dwordx4 v[138:141], v245, s[26:27] offset:2560
	global_load_dwordx4 v[142:145], v245, s[28:29] offset:2560
	global_load_dwordx4 v[146:149], v214, s[36:37]
	global_load_dwordx4 v[150:153], v214, s[36:37] offset:1024
	global_load_dwordx4 v[154:157], v214, s[36:37] offset:2048
	global_load_dwordx4 v[158:161], v214, s[36:37] offset:3072
	v_add_u32_e32 v214, 0x1000, v214
	global_load_dwordx4 v[162:165], v214, s[36:37]
	global_load_dwordx4 v[166:169], v214, s[36:37] offset:1024
	global_load_dwordx4 v[170:173], v214, s[36:37] offset:2048
	global_load_dwordx4 v[174:177], v214, s[36:37] offset:3072
	v_add_u32_e32 v214, 0x1000, v214
	global_load_dwordx4 v[178:181], v214, s[36:37]
	global_load_dwordx4 v[182:185], v214, s[36:37] offset:1024
	global_load_dwordx4 v[186:189], v214, s[36:37] offset:2048
	global_load_dwordx4 v[190:193], v214, s[36:37] offset:3072
	v_add_u32_e32 v214, 0x1000, v214
	global_load_dwordx4 v[194:197], v214, s[36:37]
	global_load_dwordx4 v[198:201], v214, s[36:37] offset:1024
	global_load_dwordx4 v[202:205], v214, s[36:37] offset:2048
	global_load_dwordx4 v[206:209], v214, s[36:37] offset:3072
	v_add_u32_e32 v214, 0x1000, v214
	s_waitcnt vmcnt(40)
	s_mov_b32 s45, 0
.Lsp_loop:
	v_mov_b32_e32 v229, v216
	v_cmp_nlt_f32_e32 vcc, s42, v229
	s_and_saveexec_b64 s[40:41], vcc
	s_cbranch_execz .Lsp_skip
	v_mul_f32_e32 v228, 0x3fb8aa3b, v229
	s_mov_b32 s43, 0x3fb8aa3b
	v_rndne_f32_e32 v230, v228
	v_sub_f32_e32 v231, v228, v230
	v_fma_f32 v228, v229, s43, -v228
	v_fmamk_f32 v228, v229, 0x32a5705f, v228
	v_add_f32_e32 v228, v231, v228
	v_exp_f32_e32 v228, v228
	v_cvt_i32_f32_e32 v230, v230
	s_mov_b32 s43, 0xc2ce8ed0
	v_cmp_ngt_f32_e32 vcc, s43, v229
	s_mov_b32 s43, 0x42b17218
	v_ldexp_f32 v228, v228, v230
	v_cndmask_b32_e32 v228, 0, v228, vcc
	v_mov_b32_e32 v242, 0x7f800000
	v_cmp_nlt_f32_e32 vcc, s43, v229
	s_mov_b32 s43, 0x3f2aaaab
	s_mov_b32 s44, 0x7f800000
	v_cndmask_b32_e32 v243, v242, v228, vcc
	v_add_f32_e32 v230, 1.0, v243
	v_add_f32_e32 v228, -1.0, v230
	v_sub_f32_e32 v229, v228, v230
	v_add_f32_e32 v229, 1.0, v229
	v_sub_f32_e32 v228, v243, v228
	v_add_f32_e32 v231, v228, v229
	v_frexp_mant_f32_e32 v232, v230
	v_cvt_f64_f32_e32 v[228:229], v230
	v_frexp_exp_i32_f64_e32 v228, v[228:229]
	v_cmp_gt_f32_e32 vcc, s43, v232
	s_mov_b32 s43, 0x3f317218
	s_nop 0
	v_subbrev_co_u32_e32 v236, vcc, 0, v228, vcc
	v_sub_u32_e32 v228, 0, v236
	v_ldexp_f32 v229, v230, v228
	v_add_f32_e32 v230, -1.0, v229
	v_add_f32_e32 v232, 1.0, v229
	v_ldexp_f32 v228, v231, v228
	v_add_f32_e32 v231, 1.0, v230
	v_add_f32_e32 v233, -1.0, v232
	v_sub_f32_e32 v231, v229, v231
	v_sub_f32_e32 v229, v229, v233
	v_add_f32_e32 v231, v228, v231
	v_add_f32_e32 v228, v228, v229
	v_add_f32_e32 v237, v232, v228
	v_rcp_f32_e32 v239, v237
	v_sub_f32_e32 v229, v232, v237
	v_add_f32_e32 v238, v228, v229
	v_add_f32_e32 v229, v230, v231
	v_mul_f32_e32 v241, v229, v239
	v_sub_f32_e32 v228, v230, v229
	v_mul_f32_e32 v230, v237, v241
	v_fma_f32 v232, v241, v237, -v230
	v_fmac_f32_e32 v232, v241, v238
	v_add_f32_e32 v240, v231, v228
	v_add_f32_e32 v228, v230, v232
	v_sub_f32_e32 v231, v229, v228
	v_pk_add_f32 v[234:235], v[228:229], v[230:231] neg_lo:[0,1] neg_hi:[0,1]
	v_mov_b32_e32 v233, v228
	v_pk_add_f32 v[228:229], v[234:235], v[232:233] neg_lo:[0,1] neg_hi:[0,1]
	v_cmp_neq_f32_e32 vcc, s44, v243
	v_add_f32_e32 v229, v240, v229
	v_add_f32_e32 v228, v228, v229
	v_add_f32_e32 v229, v231, v228
	v_mul_f32_e32 v240, v239, v229
	v_mul_f32_e32 v230, v237, v240
	v_fma_f32 v232, v240, v237, -v230
	v_fmac_f32_e32 v232, v240, v238
	v_sub_f32_e32 v231, v231, v229
	v_add_f32_e32 v237, v228, v231
	v_add_f32_e32 v228, v230, v232
	v_sub_f32_e32 v231, v229, v228
	v_pk_add_f32 v[234:235], v[228:229], v[230:231] neg_lo:[0,1] neg_hi:[0,1]
	v_mov_b32_e32 v233, v228
	v_pk_add_f32 v[228:229], v[234:235], v[232:233] neg_lo:[0,1] neg_hi:[0,1]
	v_cvt_f32_i32_e32 v230, v236
	v_add_f32_e32 v229, v237, v229
	v_add_f32_e32 v228, v228, v229
	v_add_f32_e32 v228, v231, v228
	v_add_f32_e32 v231, v241, v240
	v_sub_f32_e32 v229, v231, v241
	v_mul_f32_e32 v228, v239, v228
	v_sub_f32_e32 v229, v240, v229
	v_add_f32_e32 v228, v229, v228
	v_add_f32_e32 v232, v231, v228
	v_mul_f32_e32 v234, v232, v232
	v_mov_b32_e32 v229, 0x3ecc95a3
	v_sub_f32_e32 v231, v232, v231
	v_fmac_f32_e32 v229, 0x3e9b6dac, v234
	v_sub_f32_e32 v228, v228, v231
	v_fmaak_f32 v229, v234, v229, 0x3f2aaada
	v_ldexp_f32 v235, v228, 1
	v_mul_f32_e32 v231, v232, v234
	v_mov_b32_e32 v228, 0x3f317218
	v_pk_mul_f32 v[228:229], v[230:231], v[228:229]
	v_ldexp_f32 v233, v232, 1
	v_fma_f32 v231, v230, s43, -v228
	v_fmamk_f32 v232, v230, 0xb102e308, v231
	v_pk_add_f32 v[230:231], v[228:229], v[232:233]
	v_mov_b32_e32 v234, v228
	v_sub_f32_e32 v233, v231, v233
	v_sub_f32_e32 v233, v229, v233
	v_add_f32_e32 v235, v235, v233
	v_pk_add_f32 v[228:229], v[230:231], v[228:229] neg_lo:[0,1] neg_hi:[0,1]
	v_pk_add_f32 v[236:237], v[230:231], v[234:235]
	v_mov_b32_e32 v233, v230
	v_mov_b32_e32 v229, v237
	v_pk_add_f32 v[238:239], v[232:233], v[228:229] neg_lo:[0,1] neg_hi:[0,1]
	v_pk_add_f32 v[228:229], v[232:233], v[228:229]
	v_mov_b32_e32 v234, v235
	v_pk_add_f32 v[232:233], v[228:229], v[230:231] op_sel:[1,0] op_sel_hi:[0,1] neg_lo:[0,1] neg_hi:[0,1]
	v_pk_add_f32 v[240:241], v[236:237], v[232:233] op_sel_hi:[1,0] neg_lo:[0,1] neg_hi:[0,1]
	v_mov_b32_e32 v236, v237
	v_mov_b32_e32 v237, v229
	v_pk_mov_b32 v[232:233], v[230:231], v[232:233] op_sel:[1,0]
	v_mov_b32_e32 v235, v230
	v_pk_add_f32 v[232:233], v[236:237], v[232:233] neg_lo:[0,1] neg_hi:[0,1]
	v_mov_b32_e32 v240, v238
	v_pk_add_f32 v[230:231], v[234:235], v[232:233] neg_lo:[0,1] neg_hi:[0,1]
	v_mov_b32_e32 v239, v229
	v_pk_add_f32 v[232:233], v[240:241], v[230:231]
	s_mov_b32 s43, 0x33800000
	v_pk_add_f32 v[234:235], v[232:233], v[232:233] op_sel:[0,1] op_sel_hi:[1,0]
	s_nop 0
	v_pk_add_f32 v[228:229], v[228:229], v[234:235] op_sel:[1,0] op_sel_hi:[0,1]
	v_mov_b32_e32 v233, v228
	v_pk_add_f32 v[236:237], v[232:233], v[238:239] neg_lo:[0,1] neg_hi:[0,1]
	v_mov_b32_e32 v231, v234
	v_sub_f32_e32 v229, v232, v236
	v_pk_add_f32 v[230:231], v[230:231], v[236:237] neg_lo:[0,1] neg_hi:[0,1]
	v_sub_f32_e32 v229, v238, v229
	v_add_f32_e32 v229, v230, v229
	v_add_f32_e32 v229, v229, v231
	v_add_f32_e32 v228, v228, v229
	v_cndmask_b32_e32 v228, v242, v228, vcc
	v_cmp_lt_f32_e64 vcc, |v243|, s43
	s_nop 1
	v_cndmask_b32_e32 v229, v228, v243, vcc
.Lsp_skip:
	s_or_b64 exec, exec, s[40:41]
	v_mov_b32_e32 v216, v217
	v_mov_b32_e32 v217, v218
	v_mov_b32_e32 v218, v219
	v_mov_b32_e32 v219, v229
	s_add_u32 s45, s45, 1
	s_cmp_lt_u32 s45, 4
	s_cbranch_scc1 .Lsp_loop
	s_waitcnt vmcnt(39)
	v_cvt_pk_f16_f32 v34, v34, v35
	v_cvt_pk_f16_f32 v35, v36, v37
	ds_write_b64 v246, v[34:35]
	s_waitcnt vmcnt(38)
	v_cvt_pk_f16_f32 v38, v38, v39
	v_cvt_pk_f16_f32 v39, v40, v41
	ds_write_b64 v246, v[38:39] offset:33024
	s_waitcnt vmcnt(37)
	v_cvt_pk_f16_f32 v42, v42, v43
	v_cvt_pk_f16_f32 v43, v44, v45
	ds_write_b64 v247, v[42:43]
	s_waitcnt vmcnt(36)
	v_cvt_pk_f16_f32 v46, v46, v47
	v_cvt_pk_f16_f32 v47, v48, v49
	ds_write_b64 v247, v[46:47] offset:33024
	global_load_dwordx4 v[34:37], v245, s[22:23] offset:3072
	global_load_dwordx4 v[38:41], v245, s[24:25] offset:3072
	global_load_dwordx4 v[42:45], v245, s[26:27] offset:3072
	global_load_dwordx4 v[46:49], v245, s[28:29] offset:3072
	s_waitcnt lgkmcnt(0)
	s_barrier
	ds_read_b128 v[98:101], v213
	ds_read_b128 v[102:105], v213 offset:33024
	ds_read_b128 v[106:109], v213 offset:32
	ds_read_b128 v[110:113], v213 offset:33056
	s_waitcnt vmcnt(19) lgkmcnt(2)
	v_mfma_f32_32x32x16_f16 v[2:17], v[98:101], v[146:149], 0
	v_mfma_f32_32x32x16_f16 v[18:33], v[102:105], v[146:149], 0
	global_load_dwordx4 v[146:149], v214, s[36:37]
	ds_read_b128 v[98:101], v213 offset:64
	ds_read_b128 v[102:105], v213 offset:33088
	s_waitcnt vmcnt(19) lgkmcnt(2)
	v_mfma_f32_32x32x16_f16 v[2:17], v[106:109], v[150:153], v[2:17]
	v_mfma_f32_32x32x16_f16 v[18:33], v[110:113], v[150:153], v[18:33]
	global_load_dwordx4 v[150:153], v214, s[36:37] offset:1024
	ds_read_b128 v[106:109], v213 offset:96
	ds_read_b128 v[110:113], v213 offset:33120
	s_waitcnt vmcnt(19) lgkmcnt(2)
	v_mfma_f32_32x32x16_f16 v[2:17], v[98:101], v[154:157], v[2:17]
	v_mfma_f32_32x32x16_f16 v[18:33], v[102:105], v[154:157], v[18:33]
	global_load_dwordx4 v[154:157], v214, s[36:37] offset:2048
	ds_read_b128 v[98:101], v213 offset:128
	ds_read_b128 v[102:105], v213 offset:33152
	s_waitcnt vmcnt(19) lgkmcnt(2)
	v_mfma_f32_32x32x16_f16 v[2:17], v[106:109], v[158:161], v[2:17]
	v_mfma_f32_32x32x16_f16 v[18:33], v[110:113], v[158:161], v[18:33]
	global_load_dwordx4 v[158:161], v214, s[36:37] offset:3072
	v_add_u32_e32 v214, 0x1000, v214
	ds_read_b128 v[106:109], v213 offset:160
	ds_read_b128 v[110:113], v213 offset:33184
	s_waitcnt vmcnt(19) lgkmcnt(2)
	v_mfma_f32_32x32x16_f16 v[2:17], v[98:101], v[162:165], v[2:17]
	v_mfma_f32_32x32x16_f16 v[18:33], v[102:105], v[162:165], v[18:33]
	global_load_dwordx4 v[162:165], v214, s[36:37]
	ds_read_b128 v[98:101], v213 offset:192
	ds_read_b128 v[102:105], v213 offset:33216
	s_waitcnt vmcnt(19) lgkmcnt(2)
	v_mfma_f32_32x32x16_f16 v[2:17], v[106:109], v[166:169], v[2:17]
	v_mfma_f32_32x32x16_f16 v[18:33], v[110:113], v[166:169], v[18:33]
	global_load_dwordx4 v[166:169], v214, s[36:37] offset:1024
	ds_read_b128 v[106:109], v213 offset:224
	ds_read_b128 v[110:113], v213 offset:33248
	s_waitcnt vmcnt(19) lgkmcnt(2)
	v_mfma_f32_32x32x16_f16 v[2:17], v[98:101], v[170:173], v[2:17]
	v_mfma_f32_32x32x16_f16 v[18:33], v[102:105], v[170:173], v[18:33]
	global_load_dwordx4 v[170:173], v214, s[36:37] offset:2048
	s_waitcnt vmcnt(19) lgkmcnt(0)
	v_mfma_f32_32x32x16_f16 v[2:17], v[106:109], v[174:177], v[2:17]
	v_mfma_f32_32x32x16_f16 v[18:33], v[110:113], v[174:177], v[18:33]
	global_load_dwordx4 v[174:177], v214, s[36:37] offset:3072
	v_add_u32_e32 v214, 0x1000, v214
	s_waitcnt vmcnt(47)
	v_cvt_pk_f16_f32 v50, v50, v51
	v_cvt_pk_f16_f32 v51, v52, v53
	ds_write_b64 v246, v[50:51] offset:256
	s_waitcnt vmcnt(46)
	v_cvt_pk_f16_f32 v54, v54, v55
	v_cvt_pk_f16_f32 v55, v56, v57
	ds_write_b64 v246, v[54:55] offset:33280
	s_waitcnt vmcnt(45)
	v_cvt_pk_f16_f32 v58, v58, v59
	v_cvt_pk_f16_f32 v59, v60, v61
	ds_write_b64 v247, v[58:59] offset:256
	s_waitcnt vmcnt(44)
	v_cvt_pk_f16_f32 v62, v62, v63
	v_cvt_pk_f16_f32 v63, v64, v65
	ds_write_b64 v247, v[62:63] offset:33280
	global_load_dwordx4 v[50:53], v245, s[22:23] offset:3584
	global_load_dwordx4 v[54:57], v245, s[24:25] offset:3584
	global_load_dwordx4 v[58:61], v245, s[26:27] offset:3584
	global_load_dwordx4 v[62:65], v245, s[28:29] offset:3584
	s_waitcnt lgkmcnt(0)
	s_barrier
	ds_read_b128 v[98:101], v213 offset:256
	ds_read_b128 v[102:105], v213 offset:33280
	ds_read_b128 v[106:109], v213 offset:288
	ds_read_b128 v[110:113], v213 offset:33312
	s_waitcnt vmcnt(23) lgkmcnt(2)
	v_mfma_f32_32x32x16_f16 v[2:17], v[98:101], v[178:181], v[2:17]
	v_mfma_f32_32x32x16_f16 v[18:33], v[102:105], v[178:181], v[18:33]
	global_load_dwordx4 v[178:181], v214, s[36:37]
	ds_read_b128 v[98:101], v213 offset:320
	ds_read_b128 v[102:105], v213 offset:33344
	s_waitcnt vmcnt(23) lgkmcnt(2)
	v_mfma_f32_32x32x16_f16 v[2:17], v[106:109], v[182:185], v[2:17]
	v_mfma_f32_32x32x16_f16 v[18:33], v[110:113], v[182:185], v[18:33]
	global_load_dwordx4 v[182:185], v214, s[36:37] offset:1024
	ds_read_b128 v[106:109], v213 offset:352
	ds_read_b128 v[110:113], v213 offset:33376
	s_waitcnt vmcnt(23) lgkmcnt(2)
	v_mfma_f32_32x32x16_f16 v[2:17], v[98:101], v[186:189], v[2:17]
	v_mfma_f32_32x32x16_f16 v[18:33], v[102:105], v[186:189], v[18:33]
	global_load_dwordx4 v[186:189], v214, s[36:37] offset:2048
	ds_read_b128 v[98:101], v213 offset:384
	ds_read_b128 v[102:105], v213 offset:33408
	s_waitcnt vmcnt(23) lgkmcnt(2)
	v_mfma_f32_32x32x16_f16 v[2:17], v[106:109], v[190:193], v[2:17]
	v_mfma_f32_32x32x16_f16 v[18:33], v[110:113], v[190:193], v[18:33]
	global_load_dwordx4 v[190:193], v214, s[36:37] offset:3072
	v_add_u32_e32 v214, 0x1000, v214
	ds_read_b128 v[106:109], v213 offset:416
	ds_read_b128 v[110:113], v213 offset:33440
	s_waitcnt vmcnt(23) lgkmcnt(2)
	v_mfma_f32_32x32x16_f16 v[2:17], v[98:101], v[194:197], v[2:17]
	v_mfma_f32_32x32x16_f16 v[18:33], v[102:105], v[194:197], v[18:33]
	global_load_dwordx4 v[194:197], v214, s[36:37]
	ds_read_b128 v[98:101], v213 offset:448
	ds_read_b128 v[102:105], v213 offset:33472
	s_waitcnt vmcnt(23) lgkmcnt(2)
	v_mfma_f32_32x32x16_f16 v[2:17], v[106:109], v[198:201], v[2:17]
	v_mfma_f32_32x32x16_f16 v[18:33], v[110:113], v[198:201], v[18:33]
	global_load_dwordx4 v[198:201], v214, s[36:37] offset:1024
	ds_read_b128 v[106:109], v213 offset:480
	ds_read_b128 v[110:113], v213 offset:33504
	s_waitcnt vmcnt(23) lgkmcnt(2)
	v_mfma_f32_32x32x16_f16 v[2:17], v[98:101], v[202:205], v[2:17]
	v_mfma_f32_32x32x16_f16 v[18:33], v[102:105], v[202:205], v[18:33]
	global_load_dwordx4 v[202:205], v214, s[36:37] offset:2048
	s_waitcnt vmcnt(23) lgkmcnt(0)
	v_mfma_f32_32x32x16_f16 v[2:17], v[106:109], v[206:209], v[2:17]
	v_mfma_f32_32x32x16_f16 v[18:33], v[110:113], v[206:209], v[18:33]
	global_load_dwordx4 v[206:209], v214, s[36:37] offset:3072
	v_add_u32_e32 v214, 0x1000, v214
	s_waitcnt vmcnt(55)
	v_cvt_pk_f16_f32 v66, v66, v67
	v_cvt_pk_f16_f32 v67, v68, v69
	ds_write_b64 v246, v[66:67] offset:512
	s_waitcnt vmcnt(54)
	v_cvt_pk_f16_f32 v70, v70, v71
	v_cvt_pk_f16_f32 v71, v72, v73
	ds_write_b64 v246, v[70:71] offset:33536
	s_waitcnt vmcnt(53)
	v_cvt_pk_f16_f32 v74, v74, v75
	v_cvt_pk_f16_f32 v75, v76, v77
	ds_write_b64 v247, v[74:75] offset:512
	s_waitcnt vmcnt(52)
	v_cvt_pk_f16_f32 v78, v78, v79
	v_cvt_pk_f16_f32 v79, v80, v81
	ds_write_b64 v247, v[78:79] offset:33536
	s_waitcnt lgkmcnt(0)
	s_barrier
	ds_read_b128 v[98:101], v213 offset:512
	ds_read_b128 v[102:105], v213 offset:33536
	ds_read_b128 v[106:109], v213 offset:544
	ds_read_b128 v[110:113], v213 offset:33568
	s_waitcnt vmcnt(19) lgkmcnt(2)
	v_mfma_f32_32x32x16_f16 v[2:17], v[98:101], v[146:149], v[2:17]
	v_mfma_f32_32x32x16_f16 v[18:33], v[102:105], v[146:149], v[18:33]
	global_load_dwordx4 v[146:149], v214, s[36:37]
	ds_read_b128 v[98:101], v213 offset:576
	ds_read_b128 v[102:105], v213 offset:33600
	s_waitcnt vmcnt(19) lgkmcnt(2)
	v_mfma_f32_32x32x16_f16 v[2:17], v[106:109], v[150:153], v[2:17]
	v_mfma_f32_32x32x16_f16 v[18:33], v[110:113], v[150:153], v[18:33]
	global_load_dwordx4 v[150:153], v214, s[36:37] offset:1024
	ds_read_b128 v[106:109], v213 offset:608
	ds_read_b128 v[110:113], v213 offset:33632
	s_waitcnt vmcnt(19) lgkmcnt(2)
	v_mfma_f32_32x32x16_f16 v[2:17], v[98:101], v[154:157], v[2:17]
	v_mfma_f32_32x32x16_f16 v[18:33], v[102:105], v[154:157], v[18:33]
	global_load_dwordx4 v[154:157], v214, s[36:37] offset:2048
	ds_read_b128 v[98:101], v213 offset:640
	ds_read_b128 v[102:105], v213 offset:33664
	s_waitcnt vmcnt(19) lgkmcnt(2)
	v_mfma_f32_32x32x16_f16 v[2:17], v[106:109], v[158:161], v[2:17]
	v_mfma_f32_32x32x16_f16 v[18:33], v[110:113], v[158:161], v[18:33]
	global_load_dwordx4 v[158:161], v214, s[36:37] offset:3072
	v_add_u32_e32 v214, 0x1000, v214
	ds_read_b128 v[106:109], v213 offset:672
	ds_read_b128 v[110:113], v213 offset:33696
	s_waitcnt vmcnt(19) lgkmcnt(2)
	v_mfma_f32_32x32x16_f16 v[2:17], v[98:101], v[162:165], v[2:17]
	v_mfma_f32_32x32x16_f16 v[18:33], v[102:105], v[162:165], v[18:33]
	global_load_dwordx4 v[162:165], v214, s[36:37]
	ds_read_b128 v[98:101], v213 offset:704
	ds_read_b128 v[102:105], v213 offset:33728
	s_waitcnt vmcnt(19) lgkmcnt(2)
	v_mfma_f32_32x32x16_f16 v[2:17], v[106:109], v[166:169], v[2:17]
	v_mfma_f32_32x32x16_f16 v[18:33], v[110:113], v[166:169], v[18:33]
	global_load_dwordx4 v[166:169], v214, s[36:37] offset:1024
	ds_read_b128 v[106:109], v213 offset:736
	ds_read_b128 v[110:113], v213 offset:33760
	s_waitcnt vmcnt(19) lgkmcnt(2)
	v_mfma_f32_32x32x16_f16 v[2:17], v[98:101], v[170:173], v[2:17]
	v_mfma_f32_32x32x16_f16 v[18:33], v[102:105], v[170:173], v[18:33]
	global_load_dwordx4 v[170:173], v214, s[36:37] offset:2048
	s_waitcnt vmcnt(19) lgkmcnt(0)
	v_mfma_f32_32x32x16_f16 v[2:17], v[106:109], v[174:177], v[2:17]
	v_mfma_f32_32x32x16_f16 v[18:33], v[110:113], v[174:177], v[18:33]
	global_load_dwordx4 v[174:177], v214, s[36:37] offset:3072
	v_add_u32_e32 v214, 0x1000, v214
	s_waitcnt vmcnt(59)
	v_cvt_pk_f16_f32 v82, v82, v83
	v_cvt_pk_f16_f32 v83, v84, v85
	ds_write_b64 v246, v[82:83] offset:768
	s_waitcnt vmcnt(58)
	v_cvt_pk_f16_f32 v86, v86, v87
	v_cvt_pk_f16_f32 v87, v88, v89
	ds_write_b64 v246, v[86:87] offset:33792
	s_waitcnt vmcnt(57)
	v_cvt_pk_f16_f32 v90, v90, v91
	v_cvt_pk_f16_f32 v91, v92, v93
	ds_write_b64 v247, v[90:91] offset:768
	s_waitcnt vmcnt(56)
	v_cvt_pk_f16_f32 v94, v94, v95
	v_cvt_pk_f16_f32 v95, v96, v97
	ds_write_b64 v247, v[94:95] offset:33792
	s_waitcnt lgkmcnt(0)
	s_barrier
	ds_read_b128 v[98:101], v213 offset:768
	ds_read_b128 v[102:105], v213 offset:33792
	ds_read_b128 v[106:109], v213 offset:800
	ds_read_b128 v[110:113], v213 offset:33824
	s_waitcnt vmcnt(15) lgkmcnt(2)
	v_mfma_f32_32x32x16_f16 v[2:17], v[98:101], v[178:181], v[2:17]
	v_mfma_f32_32x32x16_f16 v[18:33], v[102:105], v[178:181], v[18:33]
	global_load_dwordx4 v[178:181], v214, s[36:37]
	ds_read_b128 v[98:101], v213 offset:832
	ds_read_b128 v[102:105], v213 offset:33856
	s_waitcnt vmcnt(15) lgkmcnt(2)
	v_mfma_f32_32x32x16_f16 v[2:17], v[106:109], v[182:185], v[2:17]
	v_mfma_f32_32x32x16_f16 v[18:33], v[110:113], v[182:185], v[18:33]
	global_load_dwordx4 v[182:185], v214, s[36:37] offset:1024
	ds_read_b128 v[106:109], v213 offset:864
	ds_read_b128 v[110:113], v213 offset:33888
	s_waitcnt vmcnt(15) lgkmcnt(2)
	v_mfma_f32_32x32x16_f16 v[2:17], v[98:101], v[186:189], v[2:17]
	v_mfma_f32_32x32x16_f16 v[18:33], v[102:105], v[186:189], v[18:33]
	global_load_dwordx4 v[186:189], v214, s[36:37] offset:2048
	ds_read_b128 v[98:101], v213 offset:896
	ds_read_b128 v[102:105], v213 offset:33920
	s_waitcnt vmcnt(15) lgkmcnt(2)
	v_mfma_f32_32x32x16_f16 v[2:17], v[106:109], v[190:193], v[2:17]
	v_mfma_f32_32x32x16_f16 v[18:33], v[110:113], v[190:193], v[18:33]
	global_load_dwordx4 v[190:193], v214, s[36:37] offset:3072
	v_add_u32_e32 v214, 0x1000, v214
	ds_read_b128 v[106:109], v213 offset:928
	ds_read_b128 v[110:113], v213 offset:33952
	s_waitcnt vmcnt(15) lgkmcnt(2)
	v_mfma_f32_32x32x16_f16 v[2:17], v[98:101], v[194:197], v[2:17]
	v_mfma_f32_32x32x16_f16 v[18:33], v[102:105], v[194:197], v[18:33]
	global_load_dwordx4 v[194:197], v214, s[36:37]
	ds_read_b128 v[98:101], v213 offset:960
	ds_read_b128 v[102:105], v213 offset:33984
	s_waitcnt vmcnt(15) lgkmcnt(2)
	v_mfma_f32_32x32x16_f16 v[2:17], v[106:109], v[198:201], v[2:17]
	v_mfma_f32_32x32x16_f16 v[18:33], v[110:113], v[198:201], v[18:33]
	global_load_dwordx4 v[198:201], v214, s[36:37] offset:1024
	ds_read_b128 v[106:109], v213 offset:992
	ds_read_b128 v[110:113], v213 offset:34016
	s_waitcnt vmcnt(15) lgkmcnt(2)
	v_mfma_f32_32x32x16_f16 v[2:17], v[98:101], v[202:205], v[2:17]
	v_mfma_f32_32x32x16_f16 v[18:33], v[102:105], v[202:205], v[18:33]
	global_load_dwordx4 v[202:205], v214, s[36:37] offset:2048
	s_waitcnt vmcnt(15) lgkmcnt(0)
	v_mfma_f32_32x32x16_f16 v[2:17], v[106:109], v[206:209], v[2:17]
	v_mfma_f32_32x32x16_f16 v[18:33], v[110:113], v[206:209], v[18:33]
	global_load_dwordx4 v[206:209], v214, s[36:37] offset:3072
	v_add_u32_e32 v214, 0x1000, v214
	s_waitcnt vmcnt(63)
	v_cvt_pk_f16_f32 v114, v114, v115
	v_cvt_pk_f16_f32 v115, v116, v117
	ds_write_b64 v246, v[114:115] offset:1024
	s_waitcnt vmcnt(62)
	v_cvt_pk_f16_f32 v118, v118, v119
	v_cvt_pk_f16_f32 v119, v120, v121
	ds_write_b64 v246, v[118:119] offset:34048
	s_waitcnt vmcnt(61)
	v_cvt_pk_f16_f32 v122, v122, v123
	v_cvt_pk_f16_f32 v123, v124, v125
	ds_write_b64 v247, v[122:123] offset:1024
	s_waitcnt vmcnt(60)
	v_cvt_pk_f16_f32 v126, v126, v127
	v_cvt_pk_f16_f32 v127, v128, v129
	ds_write_b64 v247, v[126:127] offset:34048
	s_waitcnt lgkmcnt(0)
	s_barrier
	ds_read_b128 v[98:101], v213 offset:1024
	ds_read_b128 v[102:105], v213 offset:34048
	ds_read_b128 v[106:109], v213 offset:1056
	ds_read_b128 v[110:113], v213 offset:34080
	s_waitcnt vmcnt(15) lgkmcnt(2)
	v_mfma_f32_32x32x16_f16 v[2:17], v[98:101], v[146:149], v[2:17]
	v_mfma_f32_32x32x16_f16 v[18:33], v[102:105], v[146:149], v[18:33]
	global_load_dwordx4 v[146:149], v214, s[36:37]
	ds_read_b128 v[98:101], v213 offset:1088
	ds_read_b128 v[102:105], v213 offset:34112
	s_waitcnt vmcnt(15) lgkmcnt(2)
	v_mfma_f32_32x32x16_f16 v[2:17], v[106:109], v[150:153], v[2:17]
	v_mfma_f32_32x32x16_f16 v[18:33], v[110:113], v[150:153], v[18:33]
	global_load_dwordx4 v[150:153], v214, s[36:37] offset:1024
	ds_read_b128 v[106:109], v213 offset:1120
	ds_read_b128 v[110:113], v213 offset:34144
	s_waitcnt vmcnt(15) lgkmcnt(2)
	v_mfma_f32_32x32x16_f16 v[2:17], v[98:101], v[154:157], v[2:17]
	v_mfma_f32_32x32x16_f16 v[18:33], v[102:105], v[154:157], v[18:33]
	global_load_dwordx4 v[154:157], v214, s[36:37] offset:2048
	ds_read_b128 v[98:101], v213 offset:1152
	ds_read_b128 v[102:105], v213 offset:34176
	s_waitcnt vmcnt(15) lgkmcnt(2)
	v_mfma_f32_32x32x16_f16 v[2:17], v[106:109], v[158:161], v[2:17]
	v_mfma_f32_32x32x16_f16 v[18:33], v[110:113], v[158:161], v[18:33]
	global_load_dwordx4 v[158:161], v214, s[36:37] offset:3072
	v_add_u32_e32 v214, 0x1000, v214
	ds_read_b128 v[106:109], v213 offset:1184
	ds_read_b128 v[110:113], v213 offset:34208
	s_waitcnt vmcnt(15) lgkmcnt(2)
	v_mfma_f32_32x32x16_f16 v[2:17], v[98:101], v[162:165], v[2:17]
	v_mfma_f32_32x32x16_f16 v[18:33], v[102:105], v[162:165], v[18:33]
	global_load_dwordx4 v[162:165], v214, s[36:37]
	ds_read_b128 v[98:101], v213 offset:1216
	ds_read_b128 v[102:105], v213 offset:34240
	s_waitcnt vmcnt(15) lgkmcnt(2)
	v_mfma_f32_32x32x16_f16 v[2:17], v[106:109], v[166:169], v[2:17]
	v_mfma_f32_32x32x16_f16 v[18:33], v[110:113], v[166:169], v[18:33]
	global_load_dwordx4 v[166:169], v214, s[36:37] offset:1024
	ds_read_b128 v[106:109], v213 offset:1248
	ds_read_b128 v[110:113], v213 offset:34272
	s_waitcnt vmcnt(15) lgkmcnt(2)
	v_mfma_f32_32x32x16_f16 v[2:17], v[98:101], v[170:173], v[2:17]
	v_mfma_f32_32x32x16_f16 v[18:33], v[102:105], v[170:173], v[18:33]
	global_load_dwordx4 v[170:173], v214, s[36:37] offset:2048
	s_waitcnt vmcnt(15) lgkmcnt(0)
	v_mfma_f32_32x32x16_f16 v[2:17], v[106:109], v[174:177], v[2:17]
	v_mfma_f32_32x32x16_f16 v[18:33], v[110:113], v[174:177], v[18:33]
	global_load_dwordx4 v[174:177], v214, s[36:37] offset:3072
	v_add_u32_e32 v214, 0x1000, v214
	s_waitcnt vmcnt(63)
	v_cvt_pk_f16_f32 v130, v130, v131
	v_cvt_pk_f16_f32 v131, v132, v133
	ds_write_b64 v246, v[130:131] offset:1280
	s_waitcnt vmcnt(63)
	v_cvt_pk_f16_f32 v134, v134, v135
	v_cvt_pk_f16_f32 v135, v136, v137
	ds_write_b64 v246, v[134:135] offset:34304
	s_waitcnt vmcnt(63)
	v_cvt_pk_f16_f32 v138, v138, v139
	v_cvt_pk_f16_f32 v139, v140, v141
	ds_write_b64 v247, v[138:139] offset:1280
	s_waitcnt vmcnt(63)
	v_cvt_pk_f16_f32 v142, v142, v143
	v_cvt_pk_f16_f32 v143, v144, v145
	ds_write_b64 v247, v[142:143] offset:34304
	s_waitcnt lgkmcnt(0)
	s_barrier
	ds_read_b128 v[98:101], v213 offset:1280
	ds_read_b128 v[102:105], v213 offset:34304
	ds_read_b128 v[106:109], v213 offset:1312
	ds_read_b128 v[110:113], v213 offset:34336
	s_waitcnt vmcnt(15) lgkmcnt(2)
	v_mfma_f32_32x32x16_f16 v[2:17], v[98:101], v[178:181], v[2:17]
	v_mfma_f32_32x32x16_f16 v[18:33], v[102:105], v[178:181], v[18:33]
	global_load_dwordx4 v[178:181], v214, s[36:37]
	ds_read_b128 v[98:101], v213 offset:1344
	ds_read_b128 v[102:105], v213 offset:34368
	s_waitcnt vmcnt(15) lgkmcnt(2)
	v_mfma_f32_32x32x16_f16 v[2:17], v[106:109], v[182:185], v[2:17]
	v_mfma_f32_32x32x16_f16 v[18:33], v[110:113], v[182:185], v[18:33]
	global_load_dwordx4 v[182:185], v214, s[36:37] offset:1024
	ds_read_b128 v[106:109], v213 offset:1376
	ds_read_b128 v[110:113], v213 offset:34400
	s_waitcnt vmcnt(15) lgkmcnt(2)
	v_mfma_f32_32x32x16_f16 v[2:17], v[98:101], v[186:189], v[2:17]
	v_mfma_f32_32x32x16_f16 v[18:33], v[102:105], v[186:189], v[18:33]
	global_load_dwordx4 v[186:189], v214, s[36:37] offset:2048
	ds_read_b128 v[98:101], v213 offset:1408
	ds_read_b128 v[102:105], v213 offset:34432
	s_waitcnt vmcnt(15) lgkmcnt(2)
	v_mfma_f32_32x32x16_f16 v[2:17], v[106:109], v[190:193], v[2:17]
	v_mfma_f32_32x32x16_f16 v[18:33], v[110:113], v[190:193], v[18:33]
	global_load_dwordx4 v[190:193], v214, s[36:37] offset:3072
	v_add_u32_e32 v214, 0x1000, v214
	ds_read_b128 v[106:109], v213 offset:1440
	ds_read_b128 v[110:113], v213 offset:34464
	s_waitcnt vmcnt(15) lgkmcnt(2)
	v_mfma_f32_32x32x16_f16 v[2:17], v[98:101], v[194:197], v[2:17]
	v_mfma_f32_32x32x16_f16 v[18:33], v[102:105], v[194:197], v[18:33]
	global_load_dwordx4 v[194:197], v214, s[36:37]
	ds_read_b128 v[98:101], v213 offset:1472
	ds_read_b128 v[102:105], v213 offset:34496
	s_waitcnt vmcnt(15) lgkmcnt(2)
	v_mfma_f32_32x32x16_f16 v[2:17], v[106:109], v[198:201], v[2:17]
	v_mfma_f32_32x32x16_f16 v[18:33], v[110:113], v[198:201], v[18:33]
	global_load_dwordx4 v[198:201], v214, s[36:37] offset:1024
	ds_read_b128 v[106:109], v213 offset:1504
	ds_read_b128 v[110:113], v213 offset:34528
	s_waitcnt vmcnt(15) lgkmcnt(2)
	v_mfma_f32_32x32x16_f16 v[2:17], v[98:101], v[202:205], v[2:17]
	v_mfma_f32_32x32x16_f16 v[18:33], v[102:105], v[202:205], v[18:33]
	global_load_dwordx4 v[202:205], v214, s[36:37] offset:2048
	s_waitcnt vmcnt(15) lgkmcnt(0)
	v_mfma_f32_32x32x16_f16 v[2:17], v[106:109], v[206:209], v[2:17]
	v_mfma_f32_32x32x16_f16 v[18:33], v[110:113], v[206:209], v[18:33]
	global_load_dwordx4 v[206:209], v214, s[36:37] offset:3072
	v_add_u32_e32 v214, 0x1000, v214
	s_waitcnt vmcnt(55)
	v_cvt_pk_f16_f32 v34, v34, v35
	v_cvt_pk_f16_f32 v35, v36, v37
	ds_write_b64 v246, v[34:35] offset:1536
	s_waitcnt vmcnt(54)
	v_cvt_pk_f16_f32 v38, v38, v39
	v_cvt_pk_f16_f32 v39, v40, v41
	ds_write_b64 v246, v[38:39] offset:34560
	s_waitcnt vmcnt(53)
	v_cvt_pk_f16_f32 v42, v42, v43
	v_cvt_pk_f16_f32 v43, v44, v45
	ds_write_b64 v247, v[42:43] offset:1536
	s_waitcnt vmcnt(52)
	v_cvt_pk_f16_f32 v46, v46, v47
	v_cvt_pk_f16_f32 v47, v48, v49
	ds_write_b64 v247, v[46:47] offset:34560
	s_waitcnt lgkmcnt(0)
	s_barrier
	ds_read_b128 v[98:101], v213 offset:1536
	ds_read_b128 v[102:105], v213 offset:34560
	ds_read_b128 v[106:109], v213 offset:1568
	ds_read_b128 v[110:113], v213 offset:34592
	s_waitcnt vmcnt(15) lgkmcnt(2)
	v_mfma_f32_32x32x16_f16 v[2:17], v[98:101], v[146:149], v[2:17]
	v_mfma_f32_32x32x16_f16 v[18:33], v[102:105], v[146:149], v[18:33]
	global_load_dwordx4 v[146:149], v214, s[36:37]
	ds_read_b128 v[98:101], v213 offset:1600
	ds_read_b128 v[102:105], v213 offset:34624
	s_waitcnt vmcnt(15) lgkmcnt(2)
	v_mfma_f32_32x32x16_f16 v[2:17], v[106:109], v[150:153], v[2:17]
	v_mfma_f32_32x32x16_f16 v[18:33], v[110:113], v[150:153], v[18:33]
	global_load_dwordx4 v[150:153], v214, s[36:37] offset:1024
	ds_read_b128 v[106:109], v213 offset:1632
	ds_read_b128 v[110:113], v213 offset:34656
	s_waitcnt vmcnt(15) lgkmcnt(2)
	v_mfma_f32_32x32x16_f16 v[2:17], v[98:101], v[154:157], v[2:17]
	v_mfma_f32_32x32x16_f16 v[18:33], v[102:105], v[154:157], v[18:33]
	global_load_dwordx4 v[154:157], v214, s[36:37] offset:2048
	ds_read_b128 v[98:101], v213 offset:1664
	ds_read_b128 v[102:105], v213 offset:34688
	s_waitcnt vmcnt(15) lgkmcnt(2)
	v_mfma_f32_32x32x16_f16 v[2:17], v[106:109], v[158:161], v[2:17]
	v_mfma_f32_32x32x16_f16 v[18:33], v[110:113], v[158:161], v[18:33]
	global_load_dwordx4 v[158:161], v214, s[36:37] offset:3072
	v_add_u32_e32 v214, 0x1000, v214
	ds_read_b128 v[106:109], v213 offset:1696
	ds_read_b128 v[110:113], v213 offset:34720
	s_waitcnt vmcnt(15) lgkmcnt(2)
	v_mfma_f32_32x32x16_f16 v[2:17], v[98:101], v[162:165], v[2:17]
	v_mfma_f32_32x32x16_f16 v[18:33], v[102:105], v[162:165], v[18:33]
	global_load_dwordx4 v[162:165], v214, s[36:37]
	ds_read_b128 v[98:101], v213 offset:1728
	ds_read_b128 v[102:105], v213 offset:34752
	s_waitcnt vmcnt(15) lgkmcnt(2)
	v_mfma_f32_32x32x16_f16 v[2:17], v[106:109], v[166:169], v[2:17]
	v_mfma_f32_32x32x16_f16 v[18:33], v[110:113], v[166:169], v[18:33]
	global_load_dwordx4 v[166:169], v214, s[36:37] offset:1024
	ds_read_b128 v[106:109], v213 offset:1760
	ds_read_b128 v[110:113], v213 offset:34784
	s_waitcnt vmcnt(15) lgkmcnt(2)
	v_mfma_f32_32x32x16_f16 v[2:17], v[98:101], v[170:173], v[2:17]
	v_mfma_f32_32x32x16_f16 v[18:33], v[102:105], v[170:173], v[18:33]
	global_load_dwordx4 v[170:173], v214, s[36:37] offset:2048
	s_waitcnt vmcnt(15) lgkmcnt(0)
	v_mfma_f32_32x32x16_f16 v[2:17], v[106:109], v[174:177], v[2:17]
	v_mfma_f32_32x32x16_f16 v[18:33], v[110:113], v[174:177], v[18:33]
	global_load_dwordx4 v[174:177], v214, s[36:37] offset:3072
	v_add_u32_e32 v214, 0x1000, v214
	s_waitcnt vmcnt(51)
	v_cvt_pk_f16_f32 v50, v50, v51
	v_cvt_pk_f16_f32 v51, v52, v53
	ds_write_b64 v246, v[50:51] offset:1792
	s_waitcnt vmcnt(50)
	v_cvt_pk_f16_f32 v54, v54, v55
	v_cvt_pk_f16_f32 v55, v56, v57
	ds_write_b64 v246, v[54:55] offset:34816
	s_waitcnt vmcnt(49)
	v_cvt_pk_f16_f32 v58, v58, v59
	v_cvt_pk_f16_f32 v59, v60, v61
	ds_write_b64 v247, v[58:59] offset:1792
	s_waitcnt vmcnt(48)
	v_cvt_pk_f16_f32 v62, v62, v63
	v_cvt_pk_f16_f32 v63, v64, v65
	ds_write_b64 v247, v[62:63] offset:34816
	s_waitcnt lgkmcnt(0)
	s_barrier
	ds_read_b128 v[98:101], v213 offset:1792
	ds_read_b128 v[102:105], v213 offset:34816
	ds_read_b128 v[106:109], v213 offset:1824
	ds_read_b128 v[110:113], v213 offset:34848
	s_waitcnt vmcnt(15) lgkmcnt(2)
	v_mfma_f32_32x32x16_f16 v[2:17], v[98:101], v[178:181], v[2:17]
	v_mfma_f32_32x32x16_f16 v[18:33], v[102:105], v[178:181], v[18:33]
	global_load_dwordx4 v[178:181], v214, s[36:37]
	ds_read_b128 v[98:101], v213 offset:1856
	ds_read_b128 v[102:105], v213 offset:34880
	s_waitcnt vmcnt(15) lgkmcnt(2)
	v_mfma_f32_32x32x16_f16 v[2:17], v[106:109], v[182:185], v[2:17]
	v_mfma_f32_32x32x16_f16 v[18:33], v[110:113], v[182:185], v[18:33]
	global_load_dwordx4 v[182:185], v214, s[36:37] offset:1024
	ds_read_b128 v[106:109], v213 offset:1888
	ds_read_b128 v[110:113], v213 offset:34912
	s_waitcnt vmcnt(15) lgkmcnt(2)
	v_mfma_f32_32x32x16_f16 v[2:17], v[98:101], v[186:189], v[2:17]
	v_mfma_f32_32x32x16_f16 v[18:33], v[102:105], v[186:189], v[18:33]
	global_load_dwordx4 v[186:189], v214, s[36:37] offset:2048
	ds_read_b128 v[98:101], v213 offset:1920
	ds_read_b128 v[102:105], v213 offset:34944
	s_waitcnt vmcnt(15) lgkmcnt(2)
	v_mfma_f32_32x32x16_f16 v[2:17], v[106:109], v[190:193], v[2:17]
	v_mfma_f32_32x32x16_f16 v[18:33], v[110:113], v[190:193], v[18:33]
	global_load_dwordx4 v[190:193], v214, s[36:37] offset:3072
	v_add_u32_e32 v214, 0x1000, v214
	ds_read_b128 v[106:109], v213 offset:1952
	ds_read_b128 v[110:113], v213 offset:34976
	s_waitcnt vmcnt(15) lgkmcnt(2)
	v_mfma_f32_32x32x16_f16 v[2:17], v[98:101], v[194:197], v[2:17]
	v_mfma_f32_32x32x16_f16 v[18:33], v[102:105], v[194:197], v[18:33]
	global_load_dwordx4 v[194:197], v214, s[36:37]
	ds_read_b128 v[98:101], v213 offset:1984
	ds_read_b128 v[102:105], v213 offset:35008
	s_waitcnt vmcnt(15) lgkmcnt(2)
	v_mfma_f32_32x32x16_f16 v[2:17], v[106:109], v[198:201], v[2:17]
	v_mfma_f32_32x32x16_f16 v[18:33], v[110:113], v[198:201], v[18:33]
	global_load_dwordx4 v[198:201], v214, s[36:37] offset:1024
	ds_read_b128 v[106:109], v213 offset:2016
	ds_read_b128 v[110:113], v213 offset:35040
	s_waitcnt vmcnt(15) lgkmcnt(2)
	v_mfma_f32_32x32x16_f16 v[2:17], v[98:101], v[202:205], v[2:17]
	v_mfma_f32_32x32x16_f16 v[18:33], v[102:105], v[202:205], v[18:33]
	global_load_dwordx4 v[202:205], v214, s[36:37] offset:2048
	s_waitcnt vmcnt(15) lgkmcnt(0)
	v_mfma_f32_32x32x16_f16 v[2:17], v[106:109], v[206:209], v[2:17]
	v_mfma_f32_32x32x16_f16 v[18:33], v[110:113], v[206:209], v[18:33]
	global_load_dwordx4 v[206:209], v214, s[36:37] offset:3072
	v_add_u32_e32 v214, 0x1000, v214
	s_nop 15
	v_mov_b32_e32 v254, 0
	v_mov_b32_e32 v255, 0
	v_fma_f32 v241, -v255, v216, v2
	v_fmac_f32_e32 v254, 0x3dcccccd, v241
	v_fmac_f32_e32 v255, 0x3dcccccd, v254
	v_fma_f32 v241, -v255, v216, v3
	v_fmac_f32_e32 v254, 0x3dcccccd, v241
	v_fmac_f32_e32 v255, 0x3dcccccd, v254
	v_fma_f32 v241, -v255, v216, v4
	v_fmac_f32_e32 v254, 0x3dcccccd, v241
	v_fmac_f32_e32 v255, 0x3dcccccd, v254
	v_fma_f32 v241, -v255, v216, v5
	v_fmac_f32_e32 v254, 0x3dcccccd, v241
	v_fmac_f32_e32 v255, 0x3dcccccd, v254
	v_fma_f32 v241, -v255, v216, v6
	v_fmac_f32_e32 v254, 0x3dcccccd, v241
	v_fmac_f32_e32 v255, 0x3dcccccd, v254
	v_fma_f32 v241, -v255, v216, v7
	v_fmac_f32_e32 v254, 0x3dcccccd, v241
	v_fmac_f32_e32 v255, 0x3dcccccd, v254
	v_fma_f32 v241, -v255, v216, v8
	v_fmac_f32_e32 v254, 0x3dcccccd, v241
	v_fmac_f32_e32 v255, 0x3dcccccd, v254
	v_fma_f32 v241, -v255, v216, v9
	v_fmac_f32_e32 v254, 0x3dcccccd, v241
	v_fmac_f32_e32 v255, 0x3dcccccd, v254
	v_fma_f32 v241, -v255, v216, v10
	v_fmac_f32_e32 v254, 0x3dcccccd, v241
	v_fmac_f32_e32 v255, 0x3dcccccd, v254
	v_fma_f32 v241, -v255, v216, v11
	v_fmac_f32_e32 v254, 0x3dcccccd, v241
	v_fmac_f32_e32 v255, 0x3dcccccd, v254
	v_fma_f32 v241, -v255, v216, v12
	v_fmac_f32_e32 v254, 0x3dcccccd, v241
	v_fmac_f32_e32 v255, 0x3dcccccd, v254
	v_fma_f32 v241, -v255, v216, v13
	v_fmac_f32_e32 v254, 0x3dcccccd, v241
	v_fmac_f32_e32 v255, 0x3dcccccd, v254
	v_fma_f32 v241, -v255, v216, v14
	v_fmac_f32_e32 v254, 0x3dcccccd, v241
	v_fmac_f32_e32 v255, 0x3dcccccd, v254
	v_fma_f32 v241, -v255, v216, v15
	v_fmac_f32_e32 v254, 0x3dcccccd, v241
	v_fmac_f32_e32 v255, 0x3dcccccd, v254
	v_fma_f32 v241, -v255, v216, v16
	v_fmac_f32_e32 v254, 0x3dcccccd, v241
	v_fmac_f32_e32 v255, 0x3dcccccd, v254
	v_fma_f32 v241, -v255, v216, v17
	v_fmac_f32_e32 v254, 0x3dcccccd, v241
	v_fmac_f32_e32 v255, 0x3dcccccd, v254
	v_fma_f32 v241, -v255, v216, v18
	v_fmac_f32_e32 v254, 0x3dcccccd, v241
	v_fmac_f32_e32 v255, 0x3dcccccd, v254
	v_fma_f32 v241, -v255, v216, v19
	v_fmac_f32_e32 v254, 0x3dcccccd, v241
	v_fmac_f32_e32 v255, 0x3dcccccd, v254
	v_fma_f32 v241, -v255, v216, v20
	v_fmac_f32_e32 v254, 0x3dcccccd, v241
	v_fmac_f32_e32 v255, 0x3dcccccd, v254
	v_fma_f32 v241, -v255, v216, v21
	v_fmac_f32_e32 v254, 0x3dcccccd, v241
	v_fmac_f32_e32 v255, 0x3dcccccd, v254
	v_fma_f32 v241, -v255, v216, v22
	v_fmac_f32_e32 v254, 0x3dcccccd, v241
	v_fmac_f32_e32 v255, 0x3dcccccd, v254
	v_fma_f32 v241, -v255, v216, v23
	v_fmac_f32_e32 v254, 0x3dcccccd, v241
	v_fmac_f32_e32 v255, 0x3dcccccd, v254
	v_fma_f32 v241, -v255, v216, v24
	v_fmac_f32_e32 v254, 0x3dcccccd, v241
	v_fmac_f32_e32 v255, 0x3dcccccd, v254
	v_fma_f32 v241, -v255, v216, v25
	v_fmac_f32_e32 v254, 0x3dcccccd, v241
	v_fmac_f32_e32 v255, 0x3dcccccd, v254
	v_fma_f32 v241, -v255, v216, v26
	v_fmac_f32_e32 v254, 0x3dcccccd, v241
	v_fmac_f32_e32 v255, 0x3dcccccd, v254
	v_fma_f32 v241, -v255, v216, v27
	v_fmac_f32_e32 v254, 0x3dcccccd, v241
	v_fmac_f32_e32 v255, 0x3dcccccd, v254
	v_fma_f32 v241, -v255, v216, v28
	v_fmac_f32_e32 v254, 0x3dcccccd, v241
	v_fmac_f32_e32 v255, 0x3dcccccd, v254
	v_fma_f32 v241, -v255, v216, v29
	v_fmac_f32_e32 v254, 0x3dcccccd, v241
	v_fmac_f32_e32 v255, 0x3dcccccd, v254
	v_fma_f32 v241, -v255, v216, v30
	v_fmac_f32_e32 v254, 0x3dcccccd, v241
	v_fmac_f32_e32 v255, 0x3dcccccd, v254
	v_fma_f32 v241, -v255, v216, v31
	v_fmac_f32_e32 v254, 0x3dcccccd, v241
	v_fmac_f32_e32 v255, 0x3dcccccd, v254
	v_fma_f32 v241, -v255, v216, v32
	v_fmac_f32_e32 v254, 0x3dcccccd, v241
	v_fmac_f32_e32 v255, 0x3dcccccd, v254
	v_fma_f32 v241, -v255, v216, v33
	v_fmac_f32_e32 v254, 0x3dcccccd, v241
	v_fmac_f32_e32 v255, 0x3dcccccd, v254
	v_mov_b32_e32 v228, 1.0
	v_mul_f32_e32 v229, 0xbdcccccd, v216
	v_mov_b32_e32 v230, 0x3dcccccd
	v_fma_f32 v231, v229, v230, 1.0
	v_mul_f32_e32 v244, v228, v228
	v_fmac_f32_e32 v244, v229, v230
	v_mul_f32_e32 v245, v228, v229
	v_fmac_f32_e32 v245, v229, v231
	v_mul_f32_e32 v246, v230, v228
	v_fmac_f32_e32 v246, v231, v230
	v_mul_f32_e32 v247, v230, v229
	v_fmac_f32_e32 v247, v231, v231
	v_mov_b32_e32 v228, v244
	v_mov_b32_e32 v229, v245
	v_mov_b32_e32 v230, v246
	v_mov_b32_e32 v231, v247
	v_mul_f32_e32 v244, v228, v228
	v_fmac_f32_e32 v244, v229, v230
	v_mul_f32_e32 v245, v228, v229
	v_fmac_f32_e32 v245, v229, v231
	v_mul_f32_e32 v246, v230, v228
	v_fmac_f32_e32 v246, v231, v230
	v_mul_f32_e32 v247, v230, v229
	v_fmac_f32_e32 v247, v231, v231
	v_mov_b32_e32 v228, v244
	v_mov_b32_e32 v229, v245
	v_mov_b32_e32 v230, v246
	v_mov_b32_e32 v231, v247
	v_mul_f32_e32 v244, v228, v228
	v_fmac_f32_e32 v244, v229, v230
	v_mul_f32_e32 v245, v228, v229
	v_fmac_f32_e32 v245, v229, v231
	v_mul_f32_e32 v246, v230, v228
	v_fmac_f32_e32 v246, v231, v230
	v_mul_f32_e32 v247, v230, v229
	v_fmac_f32_e32 v247, v231, v231
	v_mov_b32_e32 v228, v244
	v_mov_b32_e32 v229, v245
	v_mov_b32_e32 v230, v246
	v_mov_b32_e32 v231, v247
	v_mul_f32_e32 v244, v228, v228
	v_fmac_f32_e32 v244, v229, v230
	v_mul_f32_e32 v245, v228, v229
	v_fmac_f32_e32 v245, v229, v231
	v_mul_f32_e32 v246, v230, v228
	v_fmac_f32_e32 v246, v231, v230
	v_mul_f32_e32 v247, v230, v229
	v_fmac_f32_e32 v247, v231, v231
	v_mov_b32_e32 v228, v244
	v_mov_b32_e32 v229, v245
	v_mov_b32_e32 v230, v246
	v_mov_b32_e32 v231, v247
	v_mul_f32_e32 v244, v228, v228
	v_fmac_f32_e32 v244, v229, v230
	v_mul_f32_e32 v245, v228, v229
	v_fmac_f32_e32 v245, v229, v231
	v_mul_f32_e32 v246, v230, v228
	v_fmac_f32_e32 v246, v231, v230
	v_mul_f32_e32 v247, v230, v229
	v_fmac_f32_e32 v247, v231, v231
	v_mov_b32_e32 v228, v244
	v_mov_b32_e32 v229, v245
	v_mov_b32_e32 v230, v246
	v_mov_b32_e32 v231, v247
	v_mul_f32_e32 v232, v228, v228
	v_fmac_f32_e32 v232, v229, v230
	v_mul_f32_e32 v233, v228, v229
	v_fmac_f32_e32 v233, v229, v231
	v_mul_f32_e32 v234, v230, v228
	v_fmac_f32_e32 v234, v231, v230
	v_mul_f32_e32 v235, v230, v229
	v_fmac_f32_e32 v235, v231, v231
	ds_bpermute_b32 v248, v224, v254
	ds_bpermute_b32 v249, v224, v255
	s_waitcnt lgkmcnt(0)
	v_cndmask_b32_e64 v236, v254, v248, s[46:47]
	v_cndmask_b32_e64 v237, v255, v249, s[46:47]
	v_cndmask_b32_e64 v241, v248, v254, s[46:47]
	v_cndmask_b32_e64 v242, v249, v255, s[46:47]
	v_fma_f32 v250, v228, v236, v241
	v_fma_f32 v251, v230, v236, v242
	v_fmac_f32_e32 v250, v229, v237
	v_fmac_f32_e32 v251, v231, v237
	v_or_b32_e32 v250, 1, v250
	v_or_b32_e32 v251, 1, v251
	v_lshlrev_b32_e32 v240, 1, v223
	s_mov_b64 s[52:53], exec
	s_andn2_b64 exec, exec, s[46:47]
	global_store_dwordx2 v240, v[250:251], s[48:49] sc1
	s_mov_b64 exec, s[52:53]
	v_lshl_add_u32 v240, v212, 18, v240
	ds_read_b128 v[98:101], v213
	ds_read_b128 v[102:105], v213 offset:33024
	ds_read_b128 v[106:109], v213 offset:32
	ds_read_b128 v[110:113], v213 offset:33056
	s_waitcnt vmcnt(16) lgkmcnt(2)
	v_mfma_f32_32x32x16_f16 v[34:49], v[98:101], v[146:149], 0
	v_mfma_f32_32x32x16_f16 v[50:65], v[102:105], v[146:149], 0
	global_load_dwordx4 v[146:149], v214, s[36:37]
	ds_read_b128 v[98:101], v213 offset:64
	ds_read_b128 v[102:105], v213 offset:33088
	s_waitcnt vmcnt(16) lgkmcnt(2)
	v_mfma_f32_32x32x16_f16 v[34:49], v[106:109], v[150:153], v[34:49]
	v_mfma_f32_32x32x16_f16 v[50:65], v[110:113], v[150:153], v[50:65]
	global_load_dwordx4 v[150:153], v214, s[36:37] offset:1024
	ds_read_b128 v[106:109], v213 offset:96
	ds_read_b128 v[110:113], v213 offset:33120
	s_waitcnt vmcnt(16) lgkmcnt(2)
	v_mfma_f32_32x32x16_f16 v[34:49], v[98:101], v[154:157], v[34:49]
	v_mfma_f32_32x32x16_f16 v[50:65], v[102:105], v[154:157], v[50:65]
	global_load_dwordx4 v[154:157], v214, s[36:37] offset:2048
	ds_read_b128 v[98:101], v213 offset:128
	ds_read_b128 v[102:105], v213 offset:33152
	s_waitcnt vmcnt(16) lgkmcnt(2)
	v_mfma_f32_32x32x16_f16 v[34:49], v[106:109], v[158:161], v[34:49]
	v_mfma_f32_32x32x16_f16 v[50:65], v[110:113], v[158:161], v[50:65]
	global_load_dwordx4 v[158:161], v214, s[36:37] offset:3072
	v_add_u32_e32 v214, 0x1000, v214
	ds_read_b128 v[106:109], v213 offset:160
	ds_read_b128 v[110:113], v213 offset:33184
	s_waitcnt vmcnt(16) lgkmcnt(2)
	v_mfma_f32_32x32x16_f16 v[34:49], v[98:101], v[162:165], v[34:49]
	v_mfma_f32_32x32x16_f16 v[50:65], v[102:105], v[162:165], v[50:65]
	global_load_dwordx4 v[162:165], v214, s[36:37]
	ds_read_b128 v[98:101], v213 offset:192
	ds_read_b128 v[102:105], v213 offset:33216
	s_waitcnt vmcnt(16) lgkmcnt(2)
	v_mfma_f32_32x32x16_f16 v[34:49], v[106:109], v[166:169], v[34:49]
	v_mfma_f32_32x32x16_f16 v[50:65], v[110:113], v[166:169], v[50:65]
	global_load_dwordx4 v[166:169], v214, s[36:37] offset:1024
	ds_read_b128 v[106:109], v213 offset:224
	ds_read_b128 v[110:113], v213 offset:33248
	s_waitcnt vmcnt(16) lgkmcnt(2)
	v_mfma_f32_32x32x16_f16 v[34:49], v[98:101], v[170:173], v[34:49]
	v_mfma_f32_32x32x16_f16 v[50:65], v[102:105], v[170:173], v[50:65]
	global_load_dwordx4 v[170:173], v214, s[36:37] offset:2048
	ds_read_b128 v[98:101], v213 offset:256
	ds_read_b128 v[102:105], v213 offset:33280
	s_waitcnt vmcnt(16) lgkmcnt(2)
	v_mfma_f32_32x32x16_f16 v[34:49], v[106:109], v[174:177], v[34:49]
	v_mfma_f32_32x32x16_f16 v[50:65], v[110:113], v[174:177], v[50:65]
	global_load_dwordx4 v[174:177], v214, s[36:37] offset:3072
	v_add_u32_e32 v214, 0x1000, v214
	s_mov_b64 s[40:41], s[38:39]
	global_load_dwordx2 v[114:115], v240, s[40:41] sc1
	s_add_u32 s40, s40, 0x2000
	s_addc_u32 s41, s41, 0
	global_load_dwordx2 v[116:117], v240, s[40:41] sc1
	s_add_u32 s40, s40, 0x2000
	s_addc_u32 s41, s41, 0
	global_load_dwordx2 v[118:119], v240, s[40:41] sc1
	s_add_u32 s40, s40, 0x2000
	s_addc_u32 s41, s41, 0
	global_load_dwordx2 v[120:121], v240, s[40:41] sc1
	s_add_u32 s40, s40, 0x2000
	s_addc_u32 s41, s41, 0
	global_load_dwordx2 v[122:123], v240, s[40:41] sc1
	s_add_u32 s40, s40, 0x2000
	s_addc_u32 s41, s41, 0
	global_load_dwordx2 v[124:125], v240, s[40:41] sc1
	s_add_u32 s40, s40, 0x2000
	s_addc_u32 s41, s41, 0
	global_load_dwordx2 v[126:127], v240, s[40:41] sc1
	s_add_u32 s40, s40, 0x2000
	s_addc_u32 s41, s41, 0
	global_load_dwordx2 v[128:129], v240, s[40:41] sc1
	s_add_u32 s40, s40, 0x2000
	s_addc_u32 s41, s41, 0
	global_load_dwordx2 v[130:131], v240, s[40:41] sc1
	s_add_u32 s40, s40, 0x2000
	s_addc_u32 s41, s41, 0
	global_load_dwordx2 v[132:133], v240, s[40:41] sc1
	s_add_u32 s40, s40, 0x2000
	s_addc_u32 s41, s41, 0
	global_load_dwordx2 v[134:135], v240, s[40:41] sc1
	s_add_u32 s40, s40, 0x2000
	s_addc_u32 s41, s41, 0
	global_load_dwordx2 v[136:137], v240, s[40:41] sc1
	s_add_u32 s40, s40, 0x2000
	s_addc_u32 s41, s41, 0
	global_load_dwordx2 v[138:139], v240, s[40:41] sc1
	s_add_u32 s40, s40, 0x2000
	s_addc_u32 s41, s41, 0
	global_load_dwordx2 v[140:141], v240, s[40:41] sc1
	s_add_u32 s40, s40, 0x2000
	s_addc_u32 s41, s41, 0
	global_load_dwordx2 v[142:143], v240, s[40:41] sc1
	s_add_u32 s40, s40, 0x2000
	s_addc_u32 s41, s41, 0
	global_load_dwordx2 v[144:145], v240, s[40:41] sc1
	ds_read_b128 v[106:109], v213 offset:288
	ds_read_b128 v[110:113], v213 offset:33312
	s_waitcnt vmcnt(32) lgkmcnt(2)
	v_mfma_f32_32x32x16_f16 v[34:49], v[98:101], v[178:181], v[34:49]
	v_mfma_f32_32x32x16_f16 v[50:65], v[102:105], v[178:181], v[50:65]
	global_load_dwordx4 v[178:181], v214, s[36:37]
	ds_read_b128 v[98:101], v213 offset:320
	ds_read_b128 v[102:105], v213 offset:33344
	s_waitcnt vmcnt(32) lgkmcnt(2)
	v_mfma_f32_32x32x16_f16 v[34:49], v[106:109], v[182:185], v[34:49]
	v_mfma_f32_32x32x16_f16 v[50:65], v[110:113], v[182:185], v[50:65]
	global_load_dwordx4 v[182:185], v214, s[36:37] offset:1024
	ds_read_b128 v[106:109], v213 offset:352
	ds_read_b128 v[110:113], v213 offset:33376
	s_waitcnt vmcnt(32) lgkmcnt(2)
	v_mfma_f32_32x32x16_f16 v[34:49], v[98:101], v[186:189], v[34:49]
	v_mfma_f32_32x32x16_f16 v[50:65], v[102:105], v[186:189], v[50:65]
	global_load_dwordx4 v[186:189], v214, s[36:37] offset:2048
	ds_read_b128 v[98:101], v213 offset:384
	ds_read_b128 v[102:105], v213 offset:33408
	s_waitcnt vmcnt(32) lgkmcnt(2)
	v_mfma_f32_32x32x16_f16 v[34:49], v[106:109], v[190:193], v[34:49]
	v_mfma_f32_32x32x16_f16 v[50:65], v[110:113], v[190:193], v[50:65]
	global_load_dwordx4 v[190:193], v214, s[36:37] offset:3072
	v_add_u32_e32 v214, 0x1000, v214
	ds_read_b128 v[106:109], v213 offset:416
	ds_read_b128 v[110:113], v213 offset:33440
	s_waitcnt vmcnt(32) lgkmcnt(2)
	v_mfma_f32_32x32x16_f16 v[34:49], v[98:101], v[194:197], v[34:49]
	v_mfma_f32_32x32x16_f16 v[50:65], v[102:105], v[194:197], v[50:65]
	global_load_dwordx4 v[194:197], v214, s[36:37]
	ds_read_b128 v[98:101], v213 offset:448
	ds_read_b128 v[102:105], v213 offset:33472
	s_waitcnt vmcnt(32) lgkmcnt(2)
	v_mfma_f32_32x32x16_f16 v[34:49], v[106:109], v[198:201], v[34:49]
	v_mfma_f32_32x32x16_f16 v[50:65], v[110:113], v[198:201], v[50:65]
	global_load_dwordx4 v[198:201], v214, s[36:37] offset:1024
	ds_read_b128 v[106:109], v213 offset:480
	ds_read_b128 v[110:113], v213 offset:33504
	s_waitcnt vmcnt(32) lgkmcnt(2)
	v_mfma_f32_32x32x16_f16 v[34:49], v[98:101], v[202:205], v[34:49]
	v_mfma_f32_32x32x16_f16 v[50:65], v[102:105], v[202:205], v[50:65]
	global_load_dwordx4 v[202:205], v214, s[36:37] offset:2048
	ds_read_b128 v[98:101], v213 offset:512
	ds_read_b128 v[102:105], v213 offset:33536
	s_waitcnt vmcnt(32) lgkmcnt(2)
	v_mfma_f32_32x32x16_f16 v[34:49], v[106:109], v[206:209], v[34:49]
	v_mfma_f32_32x32x16_f16 v[50:65], v[110:113], v[206:209], v[50:65]
	global_load_dwordx4 v[206:209], v214, s[36:37] offset:3072
	v_add_u32_e32 v214, 0x1000, v214
	ds_read_b128 v[106:109], v213 offset:544
	ds_read_b128 v[110:113], v213 offset:33568
	s_waitcnt vmcnt(31) lgkmcnt(2)
	v_mfma_f32_32x32x16_f16 v[34:49], v[98:101], v[146:149], v[34:49]
	v_mfma_f32_32x32x16_f16 v[50:65], v[102:105], v[146:149], v[50:65]
	global_load_dwordx4 v[146:149], v214, s[36:37]
	ds_read_b128 v[98:101], v213 offset:576
	ds_read_b128 v[102:105], v213 offset:33600
	s_waitcnt vmcnt(31) lgkmcnt(2)
	v_mfma_f32_32x32x16_f16 v[34:49], v[106:109], v[150:153], v[34:49]
	v_mfma_f32_32x32x16_f16 v[50:65], v[110:113], v[150:153], v[50:65]
	global_load_dwordx4 v[150:153], v214, s[36:37] offset:1024
	v_mov_b32_e32 v238, 0
	v_mov_b32_e32 v239, 0
	s_waitcnt vmcnt(10)
	s_branch .Llb_chk_0_0
.Llb_retry_0_0:
	s_sleep 2
	s_mov_b64 s[40:41], s[38:39]
	global_load_dwordx2 v[114:115], v240, s[40:41] sc1
	s_add_u32 s40, s40, 0x2000
	s_addc_u32 s41, s41, 0
	global_load_dwordx2 v[116:117], v240, s[40:41] sc1
	s_add_u32 s40, s40, 0x2000
	s_addc_u32 s41, s41, 0
	global_load_dwordx2 v[118:119], v240, s[40:41] sc1
	s_add_u32 s40, s40, 0x2000
	s_addc_u32 s41, s41, 0
	global_load_dwordx2 v[120:121], v240, s[40:41] sc1
	s_add_u32 s40, s40, 0x2000
	s_addc_u32 s41, s41, 0
	global_load_dwordx2 v[122:123], v240, s[40:41] sc1
	s_add_u32 s40, s40, 0x2000
	s_addc_u32 s41, s41, 0
	global_load_dwordx2 v[124:125], v240, s[40:41] sc1
	s_add_u32 s40, s40, 0x2000
	s_addc_u32 s41, s41, 0
	global_load_dwordx2 v[126:127], v240, s[40:41] sc1
	s_add_u32 s40, s40, 0x2000
	s_addc_u32 s41, s41, 0
	global_load_dwordx2 v[128:129], v240, s[40:41] sc1
	s_add_u32 s40, s40, 0x2000
	s_addc_u32 s41, s41, 0
	global_load_dwordx2 v[130:131], v240, s[40:41] sc1
	s_add_u32 s40, s40, 0x2000
	s_addc_u32 s41, s41, 0
	global_load_dwordx2 v[132:133], v240, s[40:41] sc1
	s_add_u32 s40, s40, 0x2000
	s_addc_u32 s41, s41, 0
	global_load_dwordx2 v[134:135], v240, s[40:41] sc1
	s_add_u32 s40, s40, 0x2000
	s_addc_u32 s41, s41, 0
	global_load_dwordx2 v[136:137], v240, s[40:41] sc1
	s_add_u32 s40, s40, 0x2000
	s_addc_u32 s41, s41, 0
	global_load_dwordx2 v[138:139], v240, s[40:41] sc1
	s_add_u32 s40, s40, 0x2000
	s_addc_u32 s41, s41, 0
	global_load_dwordx2 v[140:141], v240, s[40:41] sc1
	s_add_u32 s40, s40, 0x2000
	s_addc_u32 s41, s41, 0
	global_load_dwordx2 v[142:143], v240, s[40:41] sc1
	s_add_u32 s40, s40, 0x2000
	s_addc_u32 s41, s41, 0
	global_load_dwordx2 v[144:145], v240, s[40:41] sc1
	s_waitcnt vmcnt(0)
.Llb_chk_0_0:
	v_mov_b32_e32 v243, 0
	v_and_b32_e32 v244, v114, v115
	v_alignbit_b32 v243, v244, v243, 1
	v_and_b32_e32 v244, v116, v117
	v_alignbit_b32 v243, v244, v243, 1
	v_and_b32_e32 v244, v118, v119
	v_alignbit_b32 v243, v244, v243, 1
	v_and_b32_e32 v244, v120, v121
	v_alignbit_b32 v243, v244, v243, 1
	v_and_b32_e32 v244, v122, v123
	v_alignbit_b32 v243, v244, v243, 1
	v_and_b32_e32 v244, v124, v125
	v_alignbit_b32 v243, v244, v243, 1
	v_and_b32_e32 v244, v126, v127
	v_alignbit_b32 v243, v244, v243, 1
	v_and_b32_e32 v244, v128, v129
	v_alignbit_b32 v243, v244, v243, 1
	v_and_b32_e32 v244, v130, v131
	v_alignbit_b32 v243, v244, v243, 1
	v_and_b32_e32 v244, v132, v133
	v_alignbit_b32 v243, v244, v243, 1
	v_and_b32_e32 v244, v134, v135
	v_alignbit_b32 v243, v244, v243, 1
	v_and_b32_e32 v244, v136, v137
	v_alignbit_b32 v243, v244, v243, 1
	v_and_b32_e32 v244, v138, v139
	v_alignbit_b32 v243, v244, v243, 1
	v_and_b32_e32 v244, v140, v141
	v_alignbit_b32 v243, v244, v243, 1
	v_and_b32_e32 v244, v142, v143
	v_alignbit_b32 v243, v244, v243, 1
	v_and_b32_e32 v244, v144, v145
	v_alignbit_b32 v243, v244, v243, 1
	v_lshrrev_b32_e32 v243, 16, v243
	v_and_b32_e32 v243, v243, v226
	v_cmp_ne_u32_e32 vcc, v243, v226
	s_nop 1
	s_cmp_eq_u64 vcc, 0
	s_cbranch_scc0 .Llb_retry_0_0
	ds_read_b128 v[106:109], v213 offset:608
	ds_read_b128 v[110:113], v213 offset:33632
	s_waitcnt vmcnt(31) lgkmcnt(2)
	v_mfma_f32_32x32x16_f16 v[34:49], v[98:101], v[154:157], v[34:49]
	v_mfma_f32_32x32x16_f16 v[50:65], v[102:105], v[154:157], v[50:65]
	global_load_dwordx4 v[154:157], v214, s[36:37] offset:2048
	v_cmp_lt_u32_e32 vcc, 0, v225
	v_fma_f32 v241, v232, v238, v114
	v_fma_f32 v242, v234, v238, v115
	v_fmac_f32_e32 v241, v233, v239
	v_fmac_f32_e32 v242, v235, v239
	v_cndmask_b32_e32 v238, v238, v241, vcc
	v_cndmask_b32_e32 v239, v239, v242, vcc
	v_cmp_lt_u32_e32 vcc, 1, v225
	v_fma_f32 v241, v232, v238, v116
	v_fma_f32 v242, v234, v238, v117
	v_fmac_f32_e32 v241, v233, v239
	v_fmac_f32_e32 v242, v235, v239
	v_cndmask_b32_e32 v238, v238, v241, vcc
	v_cndmask_b32_e32 v239, v239, v242, vcc
	v_cmp_lt_u32_e32 vcc, 2, v225
	v_fma_f32 v241, v232, v238, v118
	v_fma_f32 v242, v234, v238, v119
	v_fmac_f32_e32 v241, v233, v239
	v_fmac_f32_e32 v242, v235, v239
	v_cndmask_b32_e32 v238, v238, v241, vcc
	v_cndmask_b32_e32 v239, v239, v242, vcc
	v_cmp_lt_u32_e32 vcc, 3, v225
	v_fma_f32 v241, v232, v238, v120
	v_fma_f32 v242, v234, v238, v121
	v_fmac_f32_e32 v241, v233, v239
	v_fmac_f32_e32 v242, v235, v239
	v_cndmask_b32_e32 v238, v238, v241, vcc
	v_cndmask_b32_e32 v239, v239, v242, vcc
	ds_read_b128 v[98:101], v213 offset:640
	ds_read_b128 v[102:105], v213 offset:33664
	s_waitcnt vmcnt(31) lgkmcnt(2)
	v_mfma_f32_32x32x16_f16 v[34:49], v[106:109], v[158:161], v[34:49]
	v_mfma_f32_32x32x16_f16 v[50:65], v[110:113], v[158:161], v[50:65]
	global_load_dwordx4 v[158:161], v214, s[36:37] offset:3072
	v_add_u32_e32 v214, 0x1000, v214
	v_cmp_lt_u32_e32 vcc, 4, v225
	v_fma_f32 v241, v232, v238, v122
	v_fma_f32 v242, v234, v238, v123
	v_fmac_f32_e32 v241, v233, v239
	v_fmac_f32_e32 v242, v235, v239
	v_cndmask_b32_e32 v238, v238, v241, vcc
	v_cndmask_b32_e32 v239, v239, v242, vcc
	v_cmp_lt_u32_e32 vcc, 5, v225
	v_fma_f32 v241, v232, v238, v124
	v_fma_f32 v242, v234, v238, v125
	v_fmac_f32_e32 v241, v233, v239
	v_fmac_f32_e32 v242, v235, v239
	v_cndmask_b32_e32 v238, v238, v241, vcc
	v_cndmask_b32_e32 v239, v239, v242, vcc
	v_cmp_lt_u32_e32 vcc, 6, v225
	v_fma_f32 v241, v232, v238, v126
	v_fma_f32 v242, v234, v238, v127
	v_fmac_f32_e32 v241, v233, v239
	v_fmac_f32_e32 v242, v235, v239
	v_cndmask_b32_e32 v238, v238, v241, vcc
	v_cndmask_b32_e32 v239, v239, v242, vcc
	v_cmp_lt_u32_e32 vcc, 7, v225
	v_fma_f32 v241, v232, v238, v128
	v_fma_f32 v242, v234, v238, v129
	v_fmac_f32_e32 v241, v233, v239
	v_fmac_f32_e32 v242, v235, v239
	v_cndmask_b32_e32 v238, v238, v241, vcc
	v_cndmask_b32_e32 v239, v239, v242, vcc
	ds_read_b128 v[106:109], v213 offset:672
	ds_read_b128 v[110:113], v213 offset:33696
	s_waitcnt vmcnt(31) lgkmcnt(2)
	v_mfma_f32_32x32x16_f16 v[34:49], v[98:101], v[162:165], v[34:49]
	v_mfma_f32_32x32x16_f16 v[50:65], v[102:105], v[162:165], v[50:65]
	global_load_dwordx4 v[162:165], v214, s[36:37]
	v_cmp_lt_u32_e32 vcc, 8, v225
	v_fma_f32 v241, v232, v238, v130
	v_fma_f32 v242, v234, v238, v131
	v_fmac_f32_e32 v241, v233, v239
	v_fmac_f32_e32 v242, v235, v239
	v_cndmask_b32_e32 v238, v238, v241, vcc
	v_cndmask_b32_e32 v239, v239, v242, vcc
	v_cmp_lt_u32_e32 vcc, 9, v225
	v_fma_f32 v241, v232, v238, v132
	v_fma_f32 v242, v234, v238, v133
	v_fmac_f32_e32 v241, v233, v239
	v_fmac_f32_e32 v242, v235, v239
	v_cndmask_b32_e32 v238, v238, v241, vcc
	v_cndmask_b32_e32 v239, v239, v242, vcc
	v_cmp_lt_u32_e32 vcc, 10, v225
	v_fma_f32 v241, v232, v238, v134
	v_fma_f32 v242, v234, v238, v135
	v_fmac_f32_e32 v241, v233, v239
	v_fmac_f32_e32 v242, v235, v239
	v_cndmask_b32_e32 v238, v238, v241, vcc
	v_cndmask_b32_e32 v239, v239, v242, vcc
	v_cmp_lt_u32_e32 vcc, 11, v225
	v_fma_f32 v241, v232, v238, v136
	v_fma_f32 v242, v234, v238, v137
	v_fmac_f32_e32 v241, v233, v239
	v_fmac_f32_e32 v242, v235, v239
	v_cndmask_b32_e32 v238, v238, v241, vcc
	v_cndmask_b32_e32 v239, v239, v242, vcc
	ds_read_b128 v[98:101], v213 offset:704
	ds_read_b128 v[102:105], v213 offset:33728
	s_waitcnt vmcnt(31) lgkmcnt(2)
	v_mfma_f32_32x32x16_f16 v[34:49], v[106:109], v[166:169], v[34:49]
	v_mfma_f32_32x32x16_f16 v[50:65], v[110:113], v[166:169], v[50:65]
	global_load_dwordx4 v[166:169], v214, s[36:37] offset:1024
	v_cmp_lt_u32_e32 vcc, 12, v225
	v_fma_f32 v241, v232, v238, v138
	v_fma_f32 v242, v234, v238, v139
	v_fmac_f32_e32 v241, v233, v239
	v_fmac_f32_e32 v242, v235, v239
	v_cndmask_b32_e32 v238, v238, v241, vcc
	v_cndmask_b32_e32 v239, v239, v242, vcc
	v_cmp_lt_u32_e32 vcc, 13, v225
	v_fma_f32 v241, v232, v238, v140
	v_fma_f32 v242, v234, v238, v141
	v_fmac_f32_e32 v241, v233, v239
	v_fmac_f32_e32 v242, v235, v239
	v_cndmask_b32_e32 v238, v238, v241, vcc
	v_cndmask_b32_e32 v239, v239, v242, vcc
	v_cmp_lt_u32_e32 vcc, 14, v225
	v_fma_f32 v241, v232, v238, v142
	v_fma_f32 v242, v234, v238, v143
	v_fmac_f32_e32 v241, v233, v239
	v_fmac_f32_e32 v242, v235, v239
	v_cndmask_b32_e32 v238, v238, v241, vcc
	v_cndmask_b32_e32 v239, v239, v242, vcc
	v_cmp_lt_u32_e32 vcc, 15, v225
	v_fma_f32 v241, v232, v238, v144
	v_fma_f32 v242, v234, v238, v145
	v_fmac_f32_e32 v241, v233, v239
	v_fmac_f32_e32 v242, v235, v239
	v_cndmask_b32_e32 v238, v238, v241, vcc
	v_cndmask_b32_e32 v239, v239, v242, vcc
	s_mov_b64 s[40:41], s[50:51]
	global_load_dwordx2 v[114:115], v240, s[40:41] sc1
	s_add_u32 s40, s40, 0x2000
	s_addc_u32 s41, s41, 0
	global_load_dwordx2 v[116:117], v240, s[40:41] sc1
	s_add_u32 s40, s40, 0x2000
	s_addc_u32 s41, s41, 0
	global_load_dwordx2 v[118:119], v240, s[40:41] sc1
	s_add_u32 s40, s40, 0x2000
	s_addc_u32 s41, s41, 0
	global_load_dwordx2 v[120:121], v240, s[40:41] sc1
	s_add_u32 s40, s40, 0x2000
	s_addc_u32 s41, s41, 0
	global_load_dwordx2 v[122:123], v240, s[40:41] sc1
	s_add_u32 s40, s40, 0x2000
	s_addc_u32 s41, s41, 0
	global_load_dwordx2 v[124:125], v240, s[40:41] sc1
	s_add_u32 s40, s40, 0x2000
	s_addc_u32 s41, s41, 0
	global_load_dwordx2 v[126:127], v240, s[40:41] sc1
	s_add_u32 s40, s40, 0x2000
	s_addc_u32 s41, s41, 0
	global_load_dwordx2 v[128:129], v240, s[40:41] sc1
	s_add_u32 s40, s40, 0x2000
	s_addc_u32 s41, s41, 0
	global_load_dwordx2 v[130:131], v240, s[40:41] sc1
	s_add_u32 s40, s40, 0x2000
	s_addc_u32 s41, s41, 0
	global_load_dwordx2 v[132:133], v240, s[40:41] sc1
	s_add_u32 s40, s40, 0x2000
	s_addc_u32 s41, s41, 0
	global_load_dwordx2 v[134:135], v240, s[40:41] sc1
	s_add_u32 s40, s40, 0x2000
	s_addc_u32 s41, s41, 0
	global_load_dwordx2 v[136:137], v240, s[40:41] sc1
	s_add_u32 s40, s40, 0x2000
	s_addc_u32 s41, s41, 0
	global_load_dwordx2 v[138:139], v240, s[40:41] sc1
	s_add_u32 s40, s40, 0x2000
	s_addc_u32 s41, s41, 0
	global_load_dwordx2 v[140:141], v240, s[40:41] sc1
	s_add_u32 s40, s40, 0x2000
	s_addc_u32 s41, s41, 0
	global_load_dwordx2 v[142:143], v240, s[40:41] sc1
	s_add_u32 s40, s40, 0x2000
	s_addc_u32 s41, s41, 0
	global_load_dwordx2 v[144:145], v240, s[40:41] sc1
	ds_read_b128 v[106:109], v213 offset:736
	ds_read_b128 v[110:113], v213 offset:33760
	s_waitcnt vmcnt(47) lgkmcnt(2)
	v_mfma_f32_32x32x16_f16 v[34:49], v[98:101], v[170:173], v[34:49]
	v_mfma_f32_32x32x16_f16 v[50:65], v[102:105], v[170:173], v[50:65]
	global_load_dwordx4 v[170:173], v214, s[36:37] offset:2048
	ds_read_b128 v[98:101], v213 offset:768
	ds_read_b128 v[102:105], v213 offset:33792
	s_waitcnt vmcnt(47) lgkmcnt(2)
	v_mfma_f32_32x32x16_f16 v[34:49], v[106:109], v[174:177], v[34:49]
	v_mfma_f32_32x32x16_f16 v[50:65], v[110:113], v[174:177], v[50:65]
	global_load_dwordx4 v[174:177], v214, s[36:37] offset:3072
	v_add_u32_e32 v214, 0x1000, v214
	ds_read_b128 v[106:109], v213 offset:800
	ds_read_b128 v[110:113], v213 offset:33824
	s_waitcnt vmcnt(31) lgkmcnt(2)
	v_mfma_f32_32x32x16_f16 v[34:49], v[98:101], v[178:181], v[34:49]
	v_mfma_f32_32x32x16_f16 v[50:65], v[102:105], v[178:181], v[50:65]
	global_load_dwordx4 v[178:181], v214, s[36:37]
	ds_read_b128 v[98:101], v213 offset:832
	ds_read_b128 v[102:105], v213 offset:33856
	s_waitcnt vmcnt(31) lgkmcnt(2)
	v_mfma_f32_32x32x16_f16 v[34:49], v[106:109], v[182:185], v[34:49]
	v_mfma_f32_32x32x16_f16 v[50:65], v[110:113], v[182:185], v[50:65]
	global_load_dwordx4 v[182:185], v214, s[36:37] offset:1024
	ds_read_b128 v[106:109], v213 offset:864
	ds_read_b128 v[110:113], v213 offset:33888
	s_waitcnt vmcnt(31) lgkmcnt(2)
	v_mfma_f32_32x32x16_f16 v[34:49], v[98:101], v[186:189], v[34:49]
	v_mfma_f32_32x32x16_f16 v[50:65], v[102:105], v[186:189], v[50:65]
	global_load_dwordx4 v[186:189], v214, s[36:37] offset:2048
	ds_read_b128 v[98:101], v213 offset:896
	ds_read_b128 v[102:105], v213 offset:33920
	s_waitcnt vmcnt(31) lgkmcnt(2)
	v_mfma_f32_32x32x16_f16 v[34:49], v[106:109], v[190:193], v[34:49]
	v_mfma_f32_32x32x16_f16 v[50:65], v[110:113], v[190:193], v[50:65]
	global_load_dwordx4 v[190:193], v214, s[36:37] offset:3072
	v_add_u32_e32 v214, 0x1000, v214
	ds_read_b128 v[106:109], v213 offset:928
	ds_read_b128 v[110:113], v213 offset:33952
	s_waitcnt vmcnt(31) lgkmcnt(2)
	v_mfma_f32_32x32x16_f16 v[34:49], v[98:101], v[194:197], v[34:49]
	v_mfma_f32_32x32x16_f16 v[50:65], v[102:105], v[194:197], v[50:65]
	global_load_dwordx4 v[194:197], v214, s[36:37]
	ds_read_b128 v[98:101], v213 offset:960
	ds_read_b128 v[102:105], v213 offset:33984
	s_waitcnt vmcnt(31) lgkmcnt(2)
	v_mfma_f32_32x32x16_f16 v[34:49], v[106:109], v[198:201], v[34:49]
	v_mfma_f32_32x32x16_f16 v[50:65], v[110:113], v[198:201], v[50:65]
	global_load_dwordx4 v[198:201], v214, s[36:37] offset:1024
	ds_read_b128 v[106:109], v213 offset:992
	ds_read_b128 v[110:113], v213 offset:34016
	s_waitcnt vmcnt(31) lgkmcnt(2)
	v_mfma_f32_32x32x16_f16 v[34:49], v[98:101], v[202:205], v[34:49]
	v_mfma_f32_32x32x16_f16 v[50:65], v[102:105], v[202:205], v[50:65]
	global_load_dwordx4 v[202:205], v214, s[36:37] offset:2048
	ds_read_b128 v[98:101], v213 offset:1024
	ds_read_b128 v[102:105], v213 offset:34048
	s_waitcnt vmcnt(31) lgkmcnt(2)
	v_mfma_f32_32x32x16_f16 v[34:49], v[106:109], v[206:209], v[34:49]
	v_mfma_f32_32x32x16_f16 v[50:65], v[110:113], v[206:209], v[50:65]
	global_load_dwordx4 v[206:209], v214, s[36:37] offset:3072
	v_add_u32_e32 v214, 0x1000, v214
	s_waitcnt vmcnt(10)
	s_branch .Llb_chk_0_1
.Llb_retry_0_1:
	s_sleep 2
	s_mov_b64 s[40:41], s[50:51]
	global_load_dwordx2 v[114:115], v240, s[40:41] sc1
	s_add_u32 s40, s40, 0x2000
	s_addc_u32 s41, s41, 0
	global_load_dwordx2 v[116:117], v240, s[40:41] sc1
	s_add_u32 s40, s40, 0x2000
	s_addc_u32 s41, s41, 0
	global_load_dwordx2 v[118:119], v240, s[40:41] sc1
	s_add_u32 s40, s40, 0x2000
	s_addc_u32 s41, s41, 0
	global_load_dwordx2 v[120:121], v240, s[40:41] sc1
	s_add_u32 s40, s40, 0x2000
	s_addc_u32 s41, s41, 0
	global_load_dwordx2 v[122:123], v240, s[40:41] sc1
	s_add_u32 s40, s40, 0x2000
	s_addc_u32 s41, s41, 0
	global_load_dwordx2 v[124:125], v240, s[40:41] sc1
	s_add_u32 s40, s40, 0x2000
	s_addc_u32 s41, s41, 0
	global_load_dwordx2 v[126:127], v240, s[40:41] sc1
	s_add_u32 s40, s40, 0x2000
	s_addc_u32 s41, s41, 0
	global_load_dwordx2 v[128:129], v240, s[40:41] sc1
	s_add_u32 s40, s40, 0x2000
	s_addc_u32 s41, s41, 0
	global_load_dwordx2 v[130:131], v240, s[40:41] sc1
	s_add_u32 s40, s40, 0x2000
	s_addc_u32 s41, s41, 0
	global_load_dwordx2 v[132:133], v240, s[40:41] sc1
	s_add_u32 s40, s40, 0x2000
	s_addc_u32 s41, s41, 0
	global_load_dwordx2 v[134:135], v240, s[40:41] sc1
	s_add_u32 s40, s40, 0x2000
	s_addc_u32 s41, s41, 0
	global_load_dwordx2 v[136:137], v240, s[40:41] sc1
	s_add_u32 s40, s40, 0x2000
	s_addc_u32 s41, s41, 0
	global_load_dwordx2 v[138:139], v240, s[40:41] sc1
	s_add_u32 s40, s40, 0x2000
	s_addc_u32 s41, s41, 0
	global_load_dwordx2 v[140:141], v240, s[40:41] sc1
	s_add_u32 s40, s40, 0x2000
	s_addc_u32 s41, s41, 0
	global_load_dwordx2 v[142:143], v240, s[40:41] sc1
	s_add_u32 s40, s40, 0x2000
	s_addc_u32 s41, s41, 0
	global_load_dwordx2 v[144:145], v240, s[40:41] sc1
	s_waitcnt vmcnt(0)
.Llb_chk_0_1:
	v_mov_b32_e32 v243, 0
	v_and_b32_e32 v244, v114, v115
	v_alignbit_b32 v243, v244, v243, 1
	v_and_b32_e32 v244, v116, v117
	v_alignbit_b32 v243, v244, v243, 1
	v_and_b32_e32 v244, v118, v119
	v_alignbit_b32 v243, v244, v243, 1
	v_and_b32_e32 v244, v120, v121
	v_alignbit_b32 v243, v244, v243, 1
	v_and_b32_e32 v244, v122, v123
	v_alignbit_b32 v243, v244, v243, 1
	v_and_b32_e32 v244, v124, v125
	v_alignbit_b32 v243, v244, v243, 1
	v_and_b32_e32 v244, v126, v127
	v_alignbit_b32 v243, v244, v243, 1
	v_and_b32_e32 v244, v128, v129
	v_alignbit_b32 v243, v244, v243, 1
	v_and_b32_e32 v244, v130, v131
	v_alignbit_b32 v243, v244, v243, 1
	v_and_b32_e32 v244, v132, v133
	v_alignbit_b32 v243, v244, v243, 1
	v_and_b32_e32 v244, v134, v135
	v_alignbit_b32 v243, v244, v243, 1
	v_and_b32_e32 v244, v136, v137
	v_alignbit_b32 v243, v244, v243, 1
	v_and_b32_e32 v244, v138, v139
	v_alignbit_b32 v243, v244, v243, 1
	v_and_b32_e32 v244, v140, v141
	v_alignbit_b32 v243, v244, v243, 1
	v_and_b32_e32 v244, v142, v143
	v_alignbit_b32 v243, v244, v243, 1
	v_and_b32_e32 v244, v144, v145
	v_alignbit_b32 v243, v244, v243, 1
	v_lshrrev_b32_e32 v243, 16, v243
	v_and_b32_e32 v243, v243, v227
	v_cmp_ne_u32_e32 vcc, v243, v227
	s_nop 1
	s_cmp_eq_u64 vcc, 0
	s_cbranch_scc0 .Llb_retry_0_1
	ds_read_b128 v[106:109], v213 offset:1056
	ds_read_b128 v[110:113], v213 offset:34080
	s_waitcnt vmcnt(31) lgkmcnt(2)
	v_mfma_f32_32x32x16_f16 v[34:49], v[98:101], v[146:149], v[34:49]
	v_mfma_f32_32x32x16_f16 v[50:65], v[102:105], v[146:149], v[50:65]
	global_load_dwordx4 v[146:149], v214, s[36:37]
	v_cmp_lt_u32_e32 vcc, 16, v225
	v_fma_f32 v241, v232, v238, v114
	v_fma_f32 v242, v234, v238, v115
	v_fmac_f32_e32 v241, v233, v239
	v_fmac_f32_e32 v242, v235, v239
	v_cndmask_b32_e32 v238, v238, v241, vcc
	v_cndmask_b32_e32 v239, v239, v242, vcc
	v_cmp_lt_u32_e32 vcc, 17, v225
	v_fma_f32 v241, v232, v238, v116
	v_fma_f32 v242, v234, v238, v117
	v_fmac_f32_e32 v241, v233, v239
	v_fmac_f32_e32 v242, v235, v239
	v_cndmask_b32_e32 v238, v238, v241, vcc
	v_cndmask_b32_e32 v239, v239, v242, vcc
	v_cmp_lt_u32_e32 vcc, 18, v225
	v_fma_f32 v241, v232, v238, v118
	v_fma_f32 v242, v234, v238, v119
	v_fmac_f32_e32 v241, v233, v239
	v_fmac_f32_e32 v242, v235, v239
	v_cndmask_b32_e32 v238, v238, v241, vcc
	v_cndmask_b32_e32 v239, v239, v242, vcc
	v_cmp_lt_u32_e32 vcc, 19, v225
	v_fma_f32 v241, v232, v238, v120
	v_fma_f32 v242, v234, v238, v121
	v_fmac_f32_e32 v241, v233, v239
	v_fmac_f32_e32 v242, v235, v239
	v_cndmask_b32_e32 v238, v238, v241, vcc
	v_cndmask_b32_e32 v239, v239, v242, vcc
	ds_read_b128 v[98:101], v213 offset:1088
	ds_read_b128 v[102:105], v213 offset:34112
	s_waitcnt vmcnt(31) lgkmcnt(2)
	v_mfma_f32_32x32x16_f16 v[34:49], v[106:109], v[150:153], v[34:49]
	v_mfma_f32_32x32x16_f16 v[50:65], v[110:113], v[150:153], v[50:65]
	global_load_dwordx4 v[150:153], v214, s[36:37] offset:1024
	v_cmp_lt_u32_e32 vcc, 20, v225
	v_fma_f32 v241, v232, v238, v122
	v_fma_f32 v242, v234, v238, v123
	v_fmac_f32_e32 v241, v233, v239
	v_fmac_f32_e32 v242, v235, v239
	v_cndmask_b32_e32 v238, v238, v241, vcc
	v_cndmask_b32_e32 v239, v239, v242, vcc
	v_cmp_lt_u32_e32 vcc, 21, v225
	v_fma_f32 v241, v232, v238, v124
	v_fma_f32 v242, v234, v238, v125
	v_fmac_f32_e32 v241, v233, v239
	v_fmac_f32_e32 v242, v235, v239
	v_cndmask_b32_e32 v238, v238, v241, vcc
	v_cndmask_b32_e32 v239, v239, v242, vcc
	v_cmp_lt_u32_e32 vcc, 22, v225
	v_fma_f32 v241, v232, v238, v126
	v_fma_f32 v242, v234, v238, v127
	v_fmac_f32_e32 v241, v233, v239
	v_fmac_f32_e32 v242, v235, v239
	v_cndmask_b32_e32 v238, v238, v241, vcc
	v_cndmask_b32_e32 v239, v239, v242, vcc
	v_cmp_lt_u32_e32 vcc, 23, v225
	v_fma_f32 v241, v232, v238, v128
	v_fma_f32 v242, v234, v238, v129
	v_fmac_f32_e32 v241, v233, v239
	v_fmac_f32_e32 v242, v235, v239
	v_cndmask_b32_e32 v238, v238, v241, vcc
	v_cndmask_b32_e32 v239, v239, v242, vcc
	ds_read_b128 v[106:109], v213 offset:1120
	ds_read_b128 v[110:113], v213 offset:34144
	s_waitcnt vmcnt(31) lgkmcnt(2)
	v_mfma_f32_32x32x16_f16 v[34:49], v[98:101], v[154:157], v[34:49]
	v_mfma_f32_32x32x16_f16 v[50:65], v[102:105], v[154:157], v[50:65]
	global_load_dwordx4 v[154:157], v214, s[36:37] offset:2048
	v_cmp_lt_u32_e32 vcc, 24, v225
	v_fma_f32 v241, v232, v238, v130
	v_fma_f32 v242, v234, v238, v131
	v_fmac_f32_e32 v241, v233, v239
	v_fmac_f32_e32 v242, v235, v239
	v_cndmask_b32_e32 v238, v238, v241, vcc
	v_cndmask_b32_e32 v239, v239, v242, vcc
	v_cmp_lt_u32_e32 vcc, 25, v225
	v_fma_f32 v241, v232, v238, v132
	v_fma_f32 v242, v234, v238, v133
	v_fmac_f32_e32 v241, v233, v239
	v_fmac_f32_e32 v242, v235, v239
	v_cndmask_b32_e32 v238, v238, v241, vcc
	v_cndmask_b32_e32 v239, v239, v242, vcc
	v_cmp_lt_u32_e32 vcc, 26, v225
	v_fma_f32 v241, v232, v238, v134
	v_fma_f32 v242, v234, v238, v135
	v_fmac_f32_e32 v241, v233, v239
	v_fmac_f32_e32 v242, v235, v239
	v_cndmask_b32_e32 v238, v238, v241, vcc
	v_cndmask_b32_e32 v239, v239, v242, vcc
	v_cmp_lt_u32_e32 vcc, 27, v225
	v_fma_f32 v241, v232, v238, v136
	v_fma_f32 v242, v234, v238, v137
	v_fmac_f32_e32 v241, v233, v239
	v_fmac_f32_e32 v242, v235, v239
	v_cndmask_b32_e32 v238, v238, v241, vcc
	v_cndmask_b32_e32 v239, v239, v242, vcc
	ds_read_b128 v[98:101], v213 offset:1152
	ds_read_b128 v[102:105], v213 offset:34176
	s_waitcnt vmcnt(31) lgkmcnt(2)
	v_mfma_f32_32x32x16_f16 v[34:49], v[106:109], v[158:161], v[34:49]
	v_mfma_f32_32x32x16_f16 v[50:65], v[110:113], v[158:161], v[50:65]
	global_load_dwordx4 v[158:161], v214, s[36:37] offset:3072
	v_add_u32_e32 v214, 0x1000, v214
	v_cmp_lt_u32_e32 vcc, 28, v225
	v_fma_f32 v241, v232, v238, v138
	v_fma_f32 v242, v234, v238, v139
	v_fmac_f32_e32 v241, v233, v239
	v_fmac_f32_e32 v242, v235, v239
	v_cndmask_b32_e32 v238, v238, v241, vcc
	v_cndmask_b32_e32 v239, v239, v242, vcc
	v_cmp_lt_u32_e32 vcc, 29, v225
	v_fma_f32 v241, v232, v238, v140
	v_fma_f32 v242, v234, v238, v141
	v_fmac_f32_e32 v241, v233, v239
	v_fmac_f32_e32 v242, v235, v239
	v_cndmask_b32_e32 v238, v238, v241, vcc
	v_cndmask_b32_e32 v239, v239, v242, vcc
	v_cmp_lt_u32_e32 vcc, 30, v225
	v_fma_f32 v241, v232, v238, v142
	v_fma_f32 v242, v234, v238, v143
	v_fmac_f32_e32 v241, v233, v239
	v_fmac_f32_e32 v242, v235, v239
	v_cndmask_b32_e32 v238, v238, v241, vcc
	v_cndmask_b32_e32 v239, v239, v242, vcc
	v_cmp_lt_u32_e32 vcc, 31, v225
	v_fma_f32 v241, v232, v238, v144
	v_fma_f32 v242, v234, v238, v145
	v_fmac_f32_e32 v241, v233, v239
	v_fmac_f32_e32 v242, v235, v239
	v_cndmask_b32_e32 v238, v238, v241, vcc
	v_cndmask_b32_e32 v239, v239, v242, vcc
	ds_read_b128 v[106:109], v213 offset:1184
	ds_read_b128 v[110:113], v213 offset:34208
	s_waitcnt vmcnt(31) lgkmcnt(2)
	v_mfma_f32_32x32x16_f16 v[34:49], v[98:101], v[162:165], v[34:49]
	v_mfma_f32_32x32x16_f16 v[50:65], v[102:105], v[162:165], v[50:65]
	global_load_dwordx4 v[162:165], v214, s[36:37]
	ds_bpermute_b32 v247, v224, v238
	ds_bpermute_b32 v248, v224, v239
	s_waitcnt lgkmcnt(0)
	v_cndmask_b32_e64 v249, v238, v247, s[46:47]
	v_cndmask_b32_e64 v250, v239, v248, s[46:47]
	v_cndmask_b32_e64 v251, v247, v238, s[46:47]
	v_cndmask_b32_e64 v252, v248, v239, s[46:47]
	s_sub_i32 s44, s18, 32
	s_cmp_gt_i32 s44, 0
	s_cbranch_scc0 .Llb_np_0
.Llb_pow_0:
	v_mul_f32_e32 v245, v232, v249
	v_mul_f32_e32 v246, v234, v249
	v_fmac_f32_e32 v245, v233, v250
	v_fmac_f32_e32 v246, v235, v250
	v_mov_b32_e32 v249, v245
	v_mov_b32_e32 v250, v246
	s_sub_i32 s44, s44, 1
	s_cmp_gt_i32 s44, 0
	s_cbranch_scc1 .Llb_pow_0
.Llb_np_0:
	v_add_f32_e32 v238, v249, v251
	v_add_f32_e32 v239, v250, v252
	ds_read_b128 v[98:101], v213 offset:1216
	ds_read_b128 v[102:105], v213 offset:34240
	s_waitcnt vmcnt(31) lgkmcnt(2)
	v_mfma_f32_32x32x16_f16 v[34:49], v[106:109], v[166:169], v[34:49]
	v_mfma_f32_32x32x16_f16 v[50:65], v[110:113], v[166:169], v[50:65]
	global_load_dwordx4 v[166:169], v214, s[36:37] offset:1024
	v_fma_f32 v245, v228, v238, v236
	v_fma_f32 v246, v230, v238, v237
	v_fmac_f32_e32 v245, v229, v239
	v_fmac_f32_e32 v246, v231, v239
	v_cndmask_b32_e64 v220, v238, v245, s[46:47]
	v_cndmask_b32_e64 v221, v239, v246, s[46:47]
	v_lshl_add_u32 v215, v212, 17, v223
	v_add_u32_e32 v215, 0x1000, v215
	ds_read_b128 v[106:109], v213 offset:1248
	ds_read_b128 v[110:113], v213 offset:34272
	s_waitcnt vmcnt(15) lgkmcnt(2)
	v_mfma_f32_32x32x16_f16 v[34:49], v[98:101], v[170:173], v[34:49]
	v_mfma_f32_32x32x16_f16 v[50:65], v[102:105], v[170:173], v[50:65]
	global_load_dwordx4 v[170:173], v214, s[36:37] offset:2048
	v_fma_f32 v222, -v221, v216, v2
	v_fmac_f32_e32 v220, 0x3dcccccd, v222
	v_fmac_f32_e32 v221, 0x3dcccccd, v220
	global_store_dword v215, v221, s[30:31] offset:-4096
	global_store_dword v215, v220, s[32:33] offset:-4096
	global_store_dword v215, v221, s[34:35] offset:-4096
	ds_read_b128 v[98:101], v213 offset:1280
	ds_read_b128 v[102:105], v213 offset:34304
	s_waitcnt vmcnt(18) lgkmcnt(2)
	v_mfma_f32_32x32x16_f16 v[34:49], v[106:109], v[174:177], v[34:49]
	v_mfma_f32_32x32x16_f16 v[50:65], v[110:113], v[174:177], v[50:65]
	global_load_dwordx4 v[174:177], v214, s[36:37] offset:3072
	v_add_u32_e32 v214, 0x1000, v214
	v_fma_f32 v222, -v221, v216, v3
	v_fmac_f32_e32 v220, 0x3dcccccd, v222
	v_fmac_f32_e32 v221, 0x3dcccccd, v220
	global_store_dword v215, v221, s[30:31]
	global_store_dword v215, v220, s[32:33]
	global_store_dword v215, v221, s[34:35]
	v_add_u32_e32 v215, 0x2000, v215
	ds_read_b128 v[106:109], v213 offset:1312
	ds_read_b128 v[110:113], v213 offset:34336
	s_waitcnt vmcnt(21) lgkmcnt(2)
	v_mfma_f32_32x32x16_f16 v[34:49], v[98:101], v[178:181], v[34:49]
	v_mfma_f32_32x32x16_f16 v[50:65], v[102:105], v[178:181], v[50:65]
	global_load_dwordx4 v[178:181], v214, s[36:37]
	v_fma_f32 v222, -v221, v216, v4
	v_fmac_f32_e32 v220, 0x3dcccccd, v222
	v_fmac_f32_e32 v221, 0x3dcccccd, v220
	global_store_dword v215, v221, s[30:31] offset:-4096
	global_store_dword v215, v220, s[32:33] offset:-4096
	global_store_dword v215, v221, s[34:35] offset:-4096
	ds_read_b128 v[98:101], v213 offset:1344
	ds_read_b128 v[102:105], v213 offset:34368
	s_waitcnt vmcnt(24) lgkmcnt(2)
	v_mfma_f32_32x32x16_f16 v[34:49], v[106:109], v[182:185], v[34:49]
	v_mfma_f32_32x32x16_f16 v[50:65], v[110:113], v[182:185], v[50:65]
	global_load_dwordx4 v[182:185], v214, s[36:37] offset:1024
	v_fma_f32 v222, -v221, v216, v5
	v_fmac_f32_e32 v220, 0x3dcccccd, v222
	v_fmac_f32_e32 v221, 0x3dcccccd, v220
	global_store_dword v215, v221, s[30:31]
	global_store_dword v215, v220, s[32:33]
	global_store_dword v215, v221, s[34:35]
	v_add_u32_e32 v215, 0x2000, v215
	ds_read_b128 v[106:109], v213 offset:1376
	ds_read_b128 v[110:113], v213 offset:34400
	s_waitcnt vmcnt(27) lgkmcnt(2)
	v_mfma_f32_32x32x16_f16 v[34:49], v[98:101], v[186:189], v[34:49]
	v_mfma_f32_32x32x16_f16 v[50:65], v[102:105], v[186:189], v[50:65]
	global_load_dwordx4 v[186:189], v214, s[36:37] offset:2048
	v_fma_f32 v222, -v221, v216, v6
	v_fmac_f32_e32 v220, 0x3dcccccd, v222
	v_fmac_f32_e32 v221, 0x3dcccccd, v220
	global_store_dword v215, v221, s[30:31] offset:-4096
	global_store_dword v215, v220, s[32:33] offset:-4096
	global_store_dword v215, v221, s[34:35] offset:-4096
	ds_read_b128 v[98:101], v213 offset:1408
	ds_read_b128 v[102:105], v213 offset:34432
	s_waitcnt vmcnt(30) lgkmcnt(2)
	v_mfma_f32_32x32x16_f16 v[34:49], v[106:109], v[190:193], v[34:49]
	v_mfma_f32_32x32x16_f16 v[50:65], v[110:113], v[190:193], v[50:65]
	global_load_dwordx4 v[190:193], v214, s[36:37] offset:3072
	v_add_u32_e32 v214, 0x1000, v214
	v_fma_f32 v222, -v221, v216, v7
	v_fmac_f32_e32 v220, 0x3dcccccd, v222
	v_fmac_f32_e32 v221, 0x3dcccccd, v220
	global_store_dword v215, v221, s[30:31]
	global_store_dword v215, v220, s[32:33]
	global_store_dword v215, v221, s[34:35]
	v_add_u32_e32 v215, 0x2000, v215
	ds_read_b128 v[106:109], v213 offset:1440
	ds_read_b128 v[110:113], v213 offset:34464
	s_waitcnt vmcnt(33) lgkmcnt(2)
	v_mfma_f32_32x32x16_f16 v[34:49], v[98:101], v[194:197], v[34:49]
	v_mfma_f32_32x32x16_f16 v[50:65], v[102:105], v[194:197], v[50:65]
	global_load_dwordx4 v[194:197], v214, s[36:37]
	v_fma_f32 v222, -v221, v216, v8
	v_fmac_f32_e32 v220, 0x3dcccccd, v222
	v_fmac_f32_e32 v221, 0x3dcccccd, v220
	global_store_dword v215, v221, s[30:31] offset:-4096
	global_store_dword v215, v220, s[32:33] offset:-4096
	global_store_dword v215, v221, s[34:35] offset:-4096
	ds_read_b128 v[98:101], v213 offset:1472
	ds_read_b128 v[102:105], v213 offset:34496
	s_waitcnt vmcnt(36) lgkmcnt(2)
	v_mfma_f32_32x32x16_f16 v[34:49], v[106:109], v[198:201], v[34:49]
	v_mfma_f32_32x32x16_f16 v[50:65], v[110:113], v[198:201], v[50:65]
	global_load_dwordx4 v[198:201], v214, s[36:37] offset:1024
	v_fma_f32 v222, -v221, v216, v9
	v_fmac_f32_e32 v220, 0x3dcccccd, v222
	v_fmac_f32_e32 v221, 0x3dcccccd, v220
	global_store_dword v215, v221, s[30:31]
	global_store_dword v215, v220, s[32:33]
	global_store_dword v215, v221, s[34:35]
	v_add_u32_e32 v215, 0x2000, v215
	ds_read_b128 v[106:109], v213 offset:1504
	ds_read_b128 v[110:113], v213 offset:34528
	s_waitcnt vmcnt(39) lgkmcnt(2)
	v_mfma_f32_32x32x16_f16 v[34:49], v[98:101], v[202:205], v[34:49]
	v_mfma_f32_32x32x16_f16 v[50:65], v[102:105], v[202:205], v[50:65]
	global_load_dwordx4 v[202:205], v214, s[36:37] offset:2048
	v_fma_f32 v222, -v221, v216, v10
	v_fmac_f32_e32 v220, 0x3dcccccd, v222
	v_fmac_f32_e32 v221, 0x3dcccccd, v220
	global_store_dword v215, v221, s[30:31] offset:-4096
	global_store_dword v215, v220, s[32:33] offset:-4096
	global_store_dword v215, v221, s[34:35] offset:-4096
	ds_read_b128 v[98:101], v213 offset:1536
	ds_read_b128 v[102:105], v213 offset:34560
	s_waitcnt vmcnt(42) lgkmcnt(2)
	v_mfma_f32_32x32x16_f16 v[34:49], v[106:109], v[206:209], v[34:49]
	v_mfma_f32_32x32x16_f16 v[50:65], v[110:113], v[206:209], v[50:65]
	global_load_dwordx4 v[206:209], v214, s[36:37] offset:3072
	v_add_u32_e32 v214, 0x1000, v214
	v_fma_f32 v222, -v221, v216, v11
	v_fmac_f32_e32 v220, 0x3dcccccd, v222
	v_fmac_f32_e32 v221, 0x3dcccccd, v220
	global_store_dword v215, v221, s[30:31]
	global_store_dword v215, v220, s[32:33]
	global_store_dword v215, v221, s[34:35]
	v_add_u32_e32 v215, 0x2000, v215
	ds_read_b128 v[106:109], v213 offset:1568
	ds_read_b128 v[110:113], v213 offset:34592
	s_waitcnt vmcnt(45) lgkmcnt(2)
	v_mfma_f32_32x32x16_f16 v[34:49], v[98:101], v[146:149], v[34:49]
	v_mfma_f32_32x32x16_f16 v[50:65], v[102:105], v[146:149], v[50:65]
	global_load_dwordx4 v[146:149], v214, s[36:37]
	v_fma_f32 v222, -v221, v216, v12
	v_fmac_f32_e32 v220, 0x3dcccccd, v222
	v_fmac_f32_e32 v221, 0x3dcccccd, v220
	global_store_dword v215, v221, s[30:31] offset:-4096
	global_store_dword v215, v220, s[32:33] offset:-4096
	global_store_dword v215, v221, s[34:35] offset:-4096
	ds_read_b128 v[98:101], v213 offset:1600
	ds_read_b128 v[102:105], v213 offset:34624
	s_waitcnt vmcnt(48) lgkmcnt(2)
	v_mfma_f32_32x32x16_f16 v[34:49], v[106:109], v[150:153], v[34:49]
	v_mfma_f32_32x32x16_f16 v[50:65], v[110:113], v[150:153], v[50:65]
	global_load_dwordx4 v[150:153], v214, s[36:37] offset:1024
	v_fma_f32 v222, -v221, v216, v13
	v_fmac_f32_e32 v220, 0x3dcccccd, v222
	v_fmac_f32_e32 v221, 0x3dcccccd, v220
	global_store_dword v215, v221, s[30:31]
	global_store_dword v215, v220, s[32:33]
	global_store_dword v215, v221, s[34:35]
	v_add_u32_e32 v215, 0x2000, v215
	ds_read_b128 v[106:109], v213 offset:1632
	ds_read_b128 v[110:113], v213 offset:34656
	s_waitcnt vmcnt(51) lgkmcnt(2)
	v_mfma_f32_32x32x16_f16 v[34:49], v[98:101], v[154:157], v[34:49]
	v_mfma_f32_32x32x16_f16 v[50:65], v[102:105], v[154:157], v[50:65]
	global_load_dwordx4 v[154:157], v214, s[36:37] offset:2048
	v_fma_f32 v222, -v221, v216, v14
	v_fmac_f32_e32 v220, 0x3dcccccd, v222
	v_fmac_f32_e32 v221, 0x3dcccccd, v220
	global_store_dword v215, v221, s[30:31] offset:-4096
	global_store_dword v215, v220, s[32:33] offset:-4096
	global_store_dword v215, v221, s[34:35] offset:-4096
	ds_read_b128 v[98:101], v213 offset:1664
	ds_read_b128 v[102:105], v213 offset:34688
	s_waitcnt vmcnt(54) lgkmcnt(2)
	v_mfma_f32_32x32x16_f16 v[34:49], v[106:109], v[158:161], v[34:49]
	v_mfma_f32_32x32x16_f16 v[50:65], v[110:113], v[158:161], v[50:65]
	global_load_dwordx4 v[158:161], v214, s[36:37] offset:3072
	v_add_u32_e32 v214, 0x1000, v214
	v_fma_f32 v222, -v221, v216, v15
	v_fmac_f32_e32 v220, 0x3dcccccd, v222
	v_fmac_f32_e32 v221, 0x3dcccccd, v220
	global_store_dword v215, v221, s[30:31]
	global_store_dword v215, v220, s[32:33]
	global_store_dword v215, v221, s[34:35]
	v_add_u32_e32 v215, 0x2000, v215
	ds_read_b128 v[106:109], v213 offset:1696
	ds_read_b128 v[110:113], v213 offset:34720
	s_waitcnt vmcnt(57) lgkmcnt(2)
	v_mfma_f32_32x32x16_f16 v[34:49], v[98:101], v[162:165], v[34:49]
	v_mfma_f32_32x32x16_f16 v[50:65], v[102:105], v[162:165], v[50:65]
	global_load_dwordx4 v[162:165], v214, s[36:37]
	v_fma_f32 v222, -v221, v216, v16
	v_fmac_f32_e32 v220, 0x3dcccccd, v222
	v_fmac_f32_e32 v221, 0x3dcccccd, v220
	global_store_dword v215, v221, s[30:31] offset:-4096
	global_store_dword v215, v220, s[32:33] offset:-4096
	global_store_dword v215, v221, s[34:35] offset:-4096
	ds_read_b128 v[98:101], v213 offset:1728
	ds_read_b128 v[102:105], v213 offset:34752
	s_waitcnt vmcnt(60) lgkmcnt(2)
	v_mfma_f32_32x32x16_f16 v[34:49], v[106:109], v[166:169], v[34:49]
	v_mfma_f32_32x32x16_f16 v[50:65], v[110:113], v[166:169], v[50:65]
	global_load_dwordx4 v[166:169], v214, s[36:37] offset:1024
	v_fma_f32 v222, -v221, v216, v17
	v_fmac_f32_e32 v220, 0x3dcccccd, v222
	v_fmac_f32_e32 v221, 0x3dcccccd, v220
	global_store_dword v215, v221, s[30:31]
	global_store_dword v215, v220, s[32:33]
	global_store_dword v215, v221, s[34:35]
	v_add_u32_e32 v215, 0x2000, v215
	ds_read_b128 v[106:109], v213 offset:1760
	ds_read_b128 v[110:113], v213 offset:34784
	s_waitcnt vmcnt(63) lgkmcnt(2)
	v_mfma_f32_32x32x16_f16 v[34:49], v[98:101], v[170:173], v[34:49]
	v_mfma_f32_32x32x16_f16 v[50:65], v[102:105], v[170:173], v[50:65]
	global_load_dwordx4 v[170:173], v214, s[36:37] offset:2048
	v_fma_f32 v222, -v221, v216, v18
	v_fmac_f32_e32 v220, 0x3dcccccd, v222
	v_fmac_f32_e32 v221, 0x3dcccccd, v220
	global_store_dword v215, v221, s[30:31] offset:-4096
	global_store_dword v215, v220, s[32:33] offset:-4096
	global_store_dword v215, v221, s[34:35] offset:-4096
	ds_read_b128 v[98:101], v213 offset:1792
	ds_read_b128 v[102:105], v213 offset:34816
	s_waitcnt vmcnt(63) lgkmcnt(2)
	v_mfma_f32_32x32x16_f16 v[34:49], v[106:109], v[174:177], v[34:49]
	v_mfma_f32_32x32x16_f16 v[50:65], v[110:113], v[174:177], v[50:65]
	global_load_dwordx4 v[174:177], v214, s[36:37] offset:3072
	v_add_u32_e32 v214, 0x1000, v214
	v_fma_f32 v222, -v221, v216, v19
	v_fmac_f32_e32 v220, 0x3dcccccd, v222
	v_fmac_f32_e32 v221, 0x3dcccccd, v220
	global_store_dword v215, v221, s[30:31]
	global_store_dword v215, v220, s[32:33]
	global_store_dword v215, v221, s[34:35]
	v_add_u32_e32 v215, 0x2000, v215
	ds_read_b128 v[106:109], v213 offset:1824
	ds_read_b128 v[110:113], v213 offset:34848
	s_waitcnt vmcnt(63) lgkmcnt(2)
	v_mfma_f32_32x32x16_f16 v[34:49], v[98:101], v[178:181], v[34:49]
	v_mfma_f32_32x32x16_f16 v[50:65], v[102:105], v[178:181], v[50:65]
	global_load_dwordx4 v[178:181], v214, s[36:37]
	v_fma_f32 v222, -v221, v216, v20
	v_fmac_f32_e32 v220, 0x3dcccccd, v222
	v_fmac_f32_e32 v221, 0x3dcccccd, v220
	global_store_dword v215, v221, s[30:31] offset:-4096
	global_store_dword v215, v220, s[32:33] offset:-4096
	global_store_dword v215, v221, s[34:35] offset:-4096
	ds_read_b128 v[98:101], v213 offset:1856
	ds_read_b128 v[102:105], v213 offset:34880
	s_waitcnt vmcnt(63) lgkmcnt(2)
	v_mfma_f32_32x32x16_f16 v[34:49], v[106:109], v[182:185], v[34:49]
	v_mfma_f32_32x32x16_f16 v[50:65], v[110:113], v[182:185], v[50:65]
	global_load_dwordx4 v[182:185], v214, s[36:37] offset:1024
	v_fma_f32 v222, -v221, v216, v21
	v_fmac_f32_e32 v220, 0x3dcccccd, v222
	v_fmac_f32_e32 v221, 0x3dcccccd, v220
	global_store_dword v215, v221, s[30:31]
	global_store_dword v215, v220, s[32:33]
	global_store_dword v215, v221, s[34:35]
	v_add_u32_e32 v215, 0x2000, v215
	ds_read_b128 v[106:109], v213 offset:1888
	ds_read_b128 v[110:113], v213 offset:34912
	s_waitcnt vmcnt(63) lgkmcnt(2)
	v_mfma_f32_32x32x16_f16 v[34:49], v[98:101], v[186:189], v[34:49]
	v_mfma_f32_32x32x16_f16 v[50:65], v[102:105], v[186:189], v[50:65]
	global_load_dwordx4 v[186:189], v214, s[36:37] offset:2048
	v_fma_f32 v222, -v221, v216, v22
	v_fmac_f32_e32 v220, 0x3dcccccd, v222
	v_fmac_f32_e32 v221, 0x3dcccccd, v220
	global_store_dword v215, v221, s[30:31] offset:-4096
	global_store_dword v215, v220, s[32:33] offset:-4096
	global_store_dword v215, v221, s[34:35] offset:-4096
	ds_read_b128 v[98:101], v213 offset:1920
	ds_read_b128 v[102:105], v213 offset:34944
	s_waitcnt vmcnt(63) lgkmcnt(2)
	v_mfma_f32_32x32x16_f16 v[34:49], v[106:109], v[190:193], v[34:49]
	v_mfma_f32_32x32x16_f16 v[50:65], v[110:113], v[190:193], v[50:65]
	global_load_dwordx4 v[190:193], v214, s[36:37] offset:3072
	v_add_u32_e32 v214, 0x1000, v214
	v_fma_f32 v222, -v221, v216, v23
	v_fmac_f32_e32 v220, 0x3dcccccd, v222
	v_fmac_f32_e32 v221, 0x3dcccccd, v220
	global_store_dword v215, v221, s[30:31]
	global_store_dword v215, v220, s[32:33]
	global_store_dword v215, v221, s[34:35]
	v_add_u32_e32 v215, 0x2000, v215
	ds_read_b128 v[106:109], v213 offset:1952
	ds_read_b128 v[110:113], v213 offset:34976
	s_waitcnt vmcnt(63) lgkmcnt(2)
	v_mfma_f32_32x32x16_f16 v[34:49], v[98:101], v[194:197], v[34:49]
	v_mfma_f32_32x32x16_f16 v[50:65], v[102:105], v[194:197], v[50:65]
	global_load_dwordx4 v[194:197], v214, s[36:37]
	v_fma_f32 v222, -v221, v216, v24
	v_fmac_f32_e32 v220, 0x3dcccccd, v222
	v_fmac_f32_e32 v221, 0x3dcccccd, v220
	global_store_dword v215, v221, s[30:31] offset:-4096
	global_store_dword v215, v220, s[32:33] offset:-4096
	global_store_dword v215, v221, s[34:35] offset:-4096
	ds_read_b128 v[98:101], v213 offset:1984
	ds_read_b128 v[102:105], v213 offset:35008
	s_waitcnt vmcnt(63) lgkmcnt(2)
	v_mfma_f32_32x32x16_f16 v[34:49], v[106:109], v[198:201], v[34:49]
	v_mfma_f32_32x32x16_f16 v[50:65], v[110:113], v[198:201], v[50:65]
	global_load_dwordx4 v[198:201], v214, s[36:37] offset:1024
	v_fma_f32 v222, -v221, v216, v25
	v_fmac_f32_e32 v220, 0x3dcccccd, v222
	v_fmac_f32_e32 v221, 0x3dcccccd, v220
	global_store_dword v215, v221, s[30:31]
	global_store_dword v215, v220, s[32:33]
	global_store_dword v215, v221, s[34:35]
	v_add_u32_e32 v215, 0x2000, v215
	ds_read_b128 v[106:109], v213 offset:2016
	ds_read_b128 v[110:113], v213 offset:35040
	s_waitcnt vmcnt(63) lgkmcnt(2)
	v_mfma_f32_32x32x16_f16 v[34:49], v[98:101], v[202:205], v[34:49]
	v_mfma_f32_32x32x16_f16 v[50:65], v[102:105], v[202:205], v[50:65]
	global_load_dwordx4 v[202:205], v214, s[36:37] offset:2048
	v_fma_f32 v222, -v221, v216, v26
	v_fmac_f32_e32 v220, 0x3dcccccd, v222
	v_fmac_f32_e32 v221, 0x3dcccccd, v220
	global_store_dword v215, v221, s[30:31] offset:-4096
	global_store_dword v215, v220, s[32:33] offset:-4096
	global_store_dword v215, v221, s[34:35] offset:-4096
	s_waitcnt vmcnt(63) lgkmcnt(0)
	v_mfma_f32_32x32x16_f16 v[34:49], v[106:109], v[206:209], v[34:49]
	v_mfma_f32_32x32x16_f16 v[50:65], v[110:113], v[206:209], v[50:65]
	global_load_dwordx4 v[206:209], v214, s[36:37] offset:3072
	v_add_u32_e32 v214, 0x1000, v214
	v_fma_f32 v222, -v221, v216, v27
	v_fmac_f32_e32 v220, 0x3dcccccd, v222
	v_fmac_f32_e32 v221, 0x3dcccccd, v220
	global_store_dword v215, v221, s[30:31]
	global_store_dword v215, v220, s[32:33]
	global_store_dword v215, v221, s[34:35]
	v_add_u32_e32 v215, 0x2000, v215
	s_nop 15
	v_mov_b32_e32 v254, 0
	v_mov_b32_e32 v255, 0
	v_fma_f32 v241, -v255, v217, v34
	v_fmac_f32_e32 v254, 0x3dcccccd, v241
	v_fmac_f32_e32 v255, 0x3dcccccd, v254
	v_fma_f32 v241, -v255, v217, v35
	v_fmac_f32_e32 v254, 0x3dcccccd, v241
	v_fmac_f32_e32 v255, 0x3dcccccd, v254
	v_fma_f32 v241, -v255, v217, v36
	v_fmac_f32_e32 v254, 0x3dcccccd, v241
	v_fmac_f32_e32 v255, 0x3dcccccd, v254
	v_fma_f32 v241, -v255, v217, v37
	v_fmac_f32_e32 v254, 0x3dcccccd, v241
	v_fmac_f32_e32 v255, 0x3dcccccd, v254
	v_fma_f32 v241, -v255, v217, v38
	v_fmac_f32_e32 v254, 0x3dcccccd, v241
	v_fmac_f32_e32 v255, 0x3dcccccd, v254
	v_fma_f32 v241, -v255, v217, v39
	v_fmac_f32_e32 v254, 0x3dcccccd, v241
	v_fmac_f32_e32 v255, 0x3dcccccd, v254
	v_fma_f32 v241, -v255, v217, v40
	v_fmac_f32_e32 v254, 0x3dcccccd, v241
	v_fmac_f32_e32 v255, 0x3dcccccd, v254
	v_fma_f32 v241, -v255, v217, v41
	v_fmac_f32_e32 v254, 0x3dcccccd, v241
	v_fmac_f32_e32 v255, 0x3dcccccd, v254
	v_fma_f32 v241, -v255, v217, v42
	v_fmac_f32_e32 v254, 0x3dcccccd, v241
	v_fmac_f32_e32 v255, 0x3dcccccd, v254
	v_fma_f32 v241, -v255, v217, v43
	v_fmac_f32_e32 v254, 0x3dcccccd, v241
	v_fmac_f32_e32 v255, 0x3dcccccd, v254
	v_fma_f32 v241, -v255, v217, v44
	v_fmac_f32_e32 v254, 0x3dcccccd, v241
	v_fmac_f32_e32 v255, 0x3dcccccd, v254
	v_fma_f32 v241, -v255, v217, v45
	v_fmac_f32_e32 v254, 0x3dcccccd, v241
	v_fmac_f32_e32 v255, 0x3dcccccd, v254
	v_fma_f32 v241, -v255, v217, v46
	v_fmac_f32_e32 v254, 0x3dcccccd, v241
	v_fmac_f32_e32 v255, 0x3dcccccd, v254
	v_fma_f32 v241, -v255, v217, v47
	v_fmac_f32_e32 v254, 0x3dcccccd, v241
	v_fmac_f32_e32 v255, 0x3dcccccd, v254
	v_fma_f32 v241, -v255, v217, v48
	v_fmac_f32_e32 v254, 0x3dcccccd, v241
	v_fmac_f32_e32 v255, 0x3dcccccd, v254
	v_fma_f32 v241, -v255, v217, v49
	v_fmac_f32_e32 v254, 0x3dcccccd, v241
	v_fmac_f32_e32 v255, 0x3dcccccd, v254
	v_fma_f32 v241, -v255, v217, v50
	v_fmac_f32_e32 v254, 0x3dcccccd, v241
	v_fmac_f32_e32 v255, 0x3dcccccd, v254
	v_fma_f32 v241, -v255, v217, v51
	v_fmac_f32_e32 v254, 0x3dcccccd, v241
	v_fmac_f32_e32 v255, 0x3dcccccd, v254
	v_fma_f32 v241, -v255, v217, v52
	v_fmac_f32_e32 v254, 0x3dcccccd, v241
	v_fmac_f32_e32 v255, 0x3dcccccd, v254
	v_fma_f32 v241, -v255, v217, v53
	v_fmac_f32_e32 v254, 0x3dcccccd, v241
	v_fmac_f32_e32 v255, 0x3dcccccd, v254
	v_fma_f32 v241, -v255, v217, v54
	v_fmac_f32_e32 v254, 0x3dcccccd, v241
	v_fmac_f32_e32 v255, 0x3dcccccd, v254
	v_fma_f32 v241, -v255, v217, v55
	v_fmac_f32_e32 v254, 0x3dcccccd, v241
	v_fmac_f32_e32 v255, 0x3dcccccd, v254
	v_fma_f32 v241, -v255, v217, v56
	v_fmac_f32_e32 v254, 0x3dcccccd, v241
	v_fmac_f32_e32 v255, 0x3dcccccd, v254
	v_fma_f32 v241, -v255, v217, v57
	v_fmac_f32_e32 v254, 0x3dcccccd, v241
	v_fmac_f32_e32 v255, 0x3dcccccd, v254
	v_fma_f32 v241, -v255, v217, v58
	v_fmac_f32_e32 v254, 0x3dcccccd, v241
	v_fmac_f32_e32 v255, 0x3dcccccd, v254
	v_fma_f32 v241, -v255, v217, v59
	v_fmac_f32_e32 v254, 0x3dcccccd, v241
	v_fmac_f32_e32 v255, 0x3dcccccd, v254
	v_fma_f32 v241, -v255, v217, v60
	v_fmac_f32_e32 v254, 0x3dcccccd, v241
	v_fmac_f32_e32 v255, 0x3dcccccd, v254
	v_fma_f32 v241, -v255, v217, v61
	v_fmac_f32_e32 v254, 0x3dcccccd, v241
	v_fmac_f32_e32 v255, 0x3dcccccd, v254
	v_fma_f32 v241, -v255, v217, v62
	v_fmac_f32_e32 v254, 0x3dcccccd, v241
	v_fmac_f32_e32 v255, 0x3dcccccd, v254
	v_fma_f32 v241, -v255, v217, v63
	v_fmac_f32_e32 v254, 0x3dcccccd, v241
	v_fmac_f32_e32 v255, 0x3dcccccd, v254
	v_fma_f32 v241, -v255, v217, v64
	v_fmac_f32_e32 v254, 0x3dcccccd, v241
	v_fmac_f32_e32 v255, 0x3dcccccd, v254
	v_fma_f32 v241, -v255, v217, v65
	v_fmac_f32_e32 v254, 0x3dcccccd, v241
	v_fmac_f32_e32 v255, 0x3dcccccd, v254
	v_mov_b32_e32 v228, 1.0
	v_mul_f32_e32 v229, 0xbdcccccd, v217
	v_mov_b32_e32 v230, 0x3dcccccd
	v_fma_f32 v231, v229, v230, 1.0
	v_mul_f32_e32 v244, v228, v228
	v_fmac_f32_e32 v244, v229, v230
	v_mul_f32_e32 v245, v228, v229
	v_fmac_f32_e32 v245, v229, v231
	v_mul_f32_e32 v246, v230, v228
	v_fmac_f32_e32 v246, v231, v230
	v_mul_f32_e32 v247, v230, v229
	v_fmac_f32_e32 v247, v231, v231
	v_mov_b32_e32 v228, v244
	v_mov_b32_e32 v229, v245
	v_mov_b32_e32 v230, v246
	v_mov_b32_e32 v231, v247
	v_mul_f32_e32 v244, v228, v228
	v_fmac_f32_e32 v244, v229, v230
	v_mul_f32_e32 v245, v228, v229
	v_fmac_f32_e32 v245, v229, v231
	v_mul_f32_e32 v246, v230, v228
	v_fmac_f32_e32 v246, v231, v230
	v_mul_f32_e32 v247, v230, v229
	v_fmac_f32_e32 v247, v231, v231
	v_mov_b32_e32 v228, v244
	v_mov_b32_e32 v229, v245
	v_mov_b32_e32 v230, v246
	v_mov_b32_e32 v231, v247
	v_mul_f32_e32 v244, v228, v228
	v_fmac_f32_e32 v244, v229, v230
	v_mul_f32_e32 v245, v228, v229
	v_fmac_f32_e32 v245, v229, v231
	v_mul_f32_e32 v246, v230, v228
	v_fmac_f32_e32 v246, v231, v230
	v_mul_f32_e32 v247, v230, v229
	v_fmac_f32_e32 v247, v231, v231
	v_mov_b32_e32 v228, v244
	v_mov_b32_e32 v229, v245
	v_mov_b32_e32 v230, v246
	v_mov_b32_e32 v231, v247
	v_mul_f32_e32 v244, v228, v228
	v_fmac_f32_e32 v244, v229, v230
	v_mul_f32_e32 v245, v228, v229
	v_fmac_f32_e32 v245, v229, v231
	v_mul_f32_e32 v246, v230, v228
	v_fmac_f32_e32 v246, v231, v230
	v_mul_f32_e32 v247, v230, v229
	v_fmac_f32_e32 v247, v231, v231
	v_mov_b32_e32 v228, v244
	v_mov_b32_e32 v229, v245
	v_mov_b32_e32 v230, v246
	v_mov_b32_e32 v231, v247
	v_mul_f32_e32 v244, v228, v228
	v_fmac_f32_e32 v244, v229, v230
	v_mul_f32_e32 v245, v228, v229
	v_fmac_f32_e32 v245, v229, v231
	v_mul_f32_e32 v246, v230, v228
	v_fmac_f32_e32 v246, v231, v230
	v_mul_f32_e32 v247, v230, v229
	v_fmac_f32_e32 v247, v231, v231
	v_mov_b32_e32 v228, v244
	v_mov_b32_e32 v229, v245
	v_mov_b32_e32 v230, v246
	v_mov_b32_e32 v231, v247
	v_mul_f32_e32 v232, v228, v228
	v_fmac_f32_e32 v232, v229, v230
	v_mul_f32_e32 v233, v228, v229
	v_fmac_f32_e32 v233, v229, v231
	v_mul_f32_e32 v234, v230, v228
	v_fmac_f32_e32 v234, v231, v230
	v_mul_f32_e32 v235, v230, v229
	v_fmac_f32_e32 v235, v231, v231
	ds_bpermute_b32 v248, v224, v254
	ds_bpermute_b32 v249, v224, v255
	s_waitcnt lgkmcnt(0)
	v_cndmask_b32_e64 v236, v254, v248, s[46:47]
	v_cndmask_b32_e64 v237, v255, v249, s[46:47]
	v_cndmask_b32_e64 v241, v248, v254, s[46:47]
	v_cndmask_b32_e64 v242, v249, v255, s[46:47]
	v_fma_f32 v250, v228, v236, v241
	v_fma_f32 v251, v230, v236, v242
	v_fmac_f32_e32 v250, v229, v237
	v_fmac_f32_e32 v251, v231, v237
	v_or_b32_e32 v250, 1, v250
	v_or_b32_e32 v251, 1, v251
	v_lshlrev_b32_e32 v240, 1, v223
	v_add_u32_e32 v240, 0x100, v240
	s_mov_b64 s[52:53], exec
	s_andn2_b64 exec, exec, s[46:47]
	global_store_dwordx2 v240, v[250:251], s[48:49] sc1
	s_mov_b64 exec, s[52:53]
	v_lshl_add_u32 v240, v212, 18, v240
	ds_read_b128 v[98:101], v213
	ds_read_b128 v[102:105], v213 offset:33024
	ds_read_b128 v[106:109], v213 offset:32
	ds_read_b128 v[110:113], v213 offset:33056
	s_waitcnt vmcnt(63) lgkmcnt(2)
	v_mfma_f32_32x32x16_f16 v[66:81], v[98:101], v[146:149], 0
	v_mfma_f32_32x32x16_f16 v[82:97], v[102:105], v[146:149], 0
	global_load_dwordx4 v[146:149], v214, s[36:37]
	v_fma_f32 v222, -v221, v216, v28
	v_fmac_f32_e32 v220, 0x3dcccccd, v222
	v_fmac_f32_e32 v221, 0x3dcccccd, v220
	global_store_dword v215, v221, s[30:31] offset:-4096
	global_store_dword v215, v220, s[32:33] offset:-4096
	global_store_dword v215, v221, s[34:35] offset:-4096
	ds_read_b128 v[98:101], v213 offset:64
	ds_read_b128 v[102:105], v213 offset:33088
	s_waitcnt vmcnt(63) lgkmcnt(2)
	v_mfma_f32_32x32x16_f16 v[66:81], v[106:109], v[150:153], v[66:81]
	v_mfma_f32_32x32x16_f16 v[82:97], v[110:113], v[150:153], v[82:97]
	global_load_dwordx4 v[150:153], v214, s[36:37] offset:1024
	v_fma_f32 v222, -v221, v216, v29
	v_fmac_f32_e32 v220, 0x3dcccccd, v222
	v_fmac_f32_e32 v221, 0x3dcccccd, v220
	global_store_dword v215, v221, s[30:31]
	global_store_dword v215, v220, s[32:33]
	global_store_dword v215, v221, s[34:35]
	v_add_u32_e32 v215, 0x2000, v215
	ds_read_b128 v[106:109], v213 offset:96
	ds_read_b128 v[110:113], v213 offset:33120
	s_waitcnt vmcnt(63) lgkmcnt(2)
	v_mfma_f32_32x32x16_f16 v[66:81], v[98:101], v[154:157], v[66:81]
	v_mfma_f32_32x32x16_f16 v[82:97], v[102:105], v[154:157], v[82:97]
	global_load_dwordx4 v[154:157], v214, s[36:37] offset:2048
	v_fma_f32 v222, -v221, v216, v30
	v_fmac_f32_e32 v220, 0x3dcccccd, v222
	v_fmac_f32_e32 v221, 0x3dcccccd, v220
	global_store_dword v215, v221, s[30:31] offset:-4096
	global_store_dword v215, v220, s[32:33] offset:-4096
	global_store_dword v215, v221, s[34:35] offset:-4096
	ds_read_b128 v[98:101], v213 offset:128
	ds_read_b128 v[102:105], v213 offset:33152
	s_waitcnt vmcnt(63) lgkmcnt(2)
	v_mfma_f32_32x32x16_f16 v[66:81], v[106:109], v[158:161], v[66:81]
	v_mfma_f32_32x32x16_f16 v[82:97], v[110:113], v[158:161], v[82:97]
	global_load_dwordx4 v[158:161], v214, s[36:37] offset:3072
	v_add_u32_e32 v214, 0x1000, v214
	v_fma_f32 v222, -v221, v216, v31
	v_fmac_f32_e32 v220, 0x3dcccccd, v222
	v_fmac_f32_e32 v221, 0x3dcccccd, v220
	global_store_dword v215, v221, s[30:31]
	global_store_dword v215, v220, s[32:33]
	global_store_dword v215, v221, s[34:35]
	v_add_u32_e32 v215, 0x2000, v215
	ds_read_b128 v[106:109], v213 offset:160
	ds_read_b128 v[110:113], v213 offset:33184
	s_waitcnt vmcnt(63) lgkmcnt(2)
	v_mfma_f32_32x32x16_f16 v[66:81], v[98:101], v[162:165], v[66:81]
	v_mfma_f32_32x32x16_f16 v[82:97], v[102:105], v[162:165], v[82:97]
	global_load_dwordx4 v[162:165], v214, s[36:37]
	v_fma_f32 v222, -v221, v216, v32
	v_fmac_f32_e32 v220, 0x3dcccccd, v222
	v_fmac_f32_e32 v221, 0x3dcccccd, v220
	global_store_dword v215, v221, s[30:31] offset:-4096
	global_store_dword v215, v220, s[32:33] offset:-4096
	global_store_dword v215, v221, s[34:35] offset:-4096
	ds_read_b128 v[98:101], v213 offset:192
	ds_read_b128 v[102:105], v213 offset:33216
	s_waitcnt vmcnt(63) lgkmcnt(2)
	v_mfma_f32_32x32x16_f16 v[66:81], v[106:109], v[166:169], v[66:81]
	v_mfma_f32_32x32x16_f16 v[82:97], v[110:113], v[166:169], v[82:97]
	global_load_dwordx4 v[166:169], v214, s[36:37] offset:1024
	v_fma_f32 v222, -v221, v216, v33
	v_fmac_f32_e32 v220, 0x3dcccccd, v222
	v_fmac_f32_e32 v221, 0x3dcccccd, v220
	global_store_dword v215, v221, s[30:31]
	global_store_dword v215, v220, s[32:33]
	global_store_dword v215, v221, s[34:35]
	v_add_u32_e32 v215, 0x2000, v215
	ds_read_b128 v[106:109], v213 offset:224
	ds_read_b128 v[110:113], v213 offset:33248
	s_waitcnt vmcnt(63) lgkmcnt(2)
	v_mfma_f32_32x32x16_f16 v[66:81], v[98:101], v[170:173], v[66:81]
	v_mfma_f32_32x32x16_f16 v[82:97], v[102:105], v[170:173], v[82:97]
	global_load_dwordx4 v[170:173], v214, s[36:37] offset:2048
	ds_read_b128 v[98:101], v213 offset:256
	ds_read_b128 v[102:105], v213 offset:33280
	s_waitcnt vmcnt(61) lgkmcnt(2)
	v_mfma_f32_32x32x16_f16 v[66:81], v[106:109], v[174:177], v[66:81]
	v_mfma_f32_32x32x16_f16 v[82:97], v[110:113], v[174:177], v[82:97]
	global_load_dwordx4 v[174:177], v214, s[36:37] offset:3072
	v_add_u32_e32 v214, 0x1000, v214
	s_mov_b64 s[40:41], s[38:39]
	global_load_dwordx2 v[114:115], v240, s[40:41] sc1
	s_add_u32 s40, s40, 0x2000
	s_addc_u32 s41, s41, 0
	global_load_dwordx2 v[116:117], v240, s[40:41] sc1
	s_add_u32 s40, s40, 0x2000
	s_addc_u32 s41, s41, 0
	global_load_dwordx2 v[118:119], v240, s[40:41] sc1
	s_add_u32 s40, s40, 0x2000
	s_addc_u32 s41, s41, 0
	global_load_dwordx2 v[120:121], v240, s[40:41] sc1
	s_add_u32 s40, s40, 0x2000
	s_addc_u32 s41, s41, 0
	global_load_dwordx2 v[122:123], v240, s[40:41] sc1
	s_add_u32 s40, s40, 0x2000
	s_addc_u32 s41, s41, 0
	global_load_dwordx2 v[124:125], v240, s[40:41] sc1
	s_add_u32 s40, s40, 0x2000
	s_addc_u32 s41, s41, 0
	global_load_dwordx2 v[126:127], v240, s[40:41] sc1
	s_add_u32 s40, s40, 0x2000
	s_addc_u32 s41, s41, 0
	global_load_dwordx2 v[128:129], v240, s[40:41] sc1
	s_add_u32 s40, s40, 0x2000
	s_addc_u32 s41, s41, 0
	global_load_dwordx2 v[130:131], v240, s[40:41] sc1
	s_add_u32 s40, s40, 0x2000
	s_addc_u32 s41, s41, 0
	global_load_dwordx2 v[132:133], v240, s[40:41] sc1
	s_add_u32 s40, s40, 0x2000
	s_addc_u32 s41, s41, 0
	global_load_dwordx2 v[134:135], v240, s[40:41] sc1
	s_add_u32 s40, s40, 0x2000
	s_addc_u32 s41, s41, 0
	global_load_dwordx2 v[136:137], v240, s[40:41] sc1
	s_add_u32 s40, s40, 0x2000
	s_addc_u32 s41, s41, 0
	global_load_dwordx2 v[138:139], v240, s[40:41] sc1
	s_add_u32 s40, s40, 0x2000
	s_addc_u32 s41, s41, 0
	global_load_dwordx2 v[140:141], v240, s[40:41] sc1
	s_add_u32 s40, s40, 0x2000
	s_addc_u32 s41, s41, 0
	global_load_dwordx2 v[142:143], v240, s[40:41] sc1
	s_add_u32 s40, s40, 0x2000
	s_addc_u32 s41, s41, 0
	global_load_dwordx2 v[144:145], v240, s[40:41] sc1
	ds_read_b128 v[106:109], v213 offset:288
	ds_read_b128 v[110:113], v213 offset:33312
	s_waitcnt vmcnt(63) lgkmcnt(2)
	v_mfma_f32_32x32x16_f16 v[66:81], v[98:101], v[178:181], v[66:81]
	v_mfma_f32_32x32x16_f16 v[82:97], v[102:105], v[178:181], v[82:97]
	global_load_dwordx4 v[178:181], v214, s[36:37]
	ds_read_b128 v[98:101], v213 offset:320
	ds_read_b128 v[102:105], v213 offset:33344
	s_waitcnt vmcnt(63) lgkmcnt(2)
	v_mfma_f32_32x32x16_f16 v[66:81], v[106:109], v[182:185], v[66:81]
	v_mfma_f32_32x32x16_f16 v[82:97], v[110:113], v[182:185], v[82:97]
	global_load_dwordx4 v[182:185], v214, s[36:37] offset:1024
	ds_read_b128 v[106:109], v213 offset:352
	ds_read_b128 v[110:113], v213 offset:33376
	s_waitcnt vmcnt(63) lgkmcnt(2)
	v_mfma_f32_32x32x16_f16 v[66:81], v[98:101], v[186:189], v[66:81]
	v_mfma_f32_32x32x16_f16 v[82:97], v[102:105], v[186:189], v[82:97]
	global_load_dwordx4 v[186:189], v214, s[36:37] offset:2048
	ds_read_b128 v[98:101], v213 offset:384
	ds_read_b128 v[102:105], v213 offset:33408
	s_waitcnt vmcnt(63) lgkmcnt(2)
	v_mfma_f32_32x32x16_f16 v[66:81], v[106:109], v[190:193], v[66:81]
	v_mfma_f32_32x32x16_f16 v[82:97], v[110:113], v[190:193], v[82:97]
	global_load_dwordx4 v[190:193], v214, s[36:37] offset:3072
	v_add_u32_e32 v214, 0x1000, v214
	ds_read_b128 v[106:109], v213 offset:416
	ds_read_b128 v[110:113], v213 offset:33440
	s_waitcnt vmcnt(62) lgkmcnt(2)
	v_mfma_f32_32x32x16_f16 v[66:81], v[98:101], v[194:197], v[66:81]
	v_mfma_f32_32x32x16_f16 v[82:97], v[102:105], v[194:197], v[82:97]
	global_load_dwordx4 v[194:197], v214, s[36:37]
	ds_read_b128 v[98:101], v213 offset:448
	ds_read_b128 v[102:105], v213 offset:33472
	s_waitcnt vmcnt(59) lgkmcnt(2)
	v_mfma_f32_32x32x16_f16 v[66:81], v[106:109], v[198:201], v[66:81]
	v_mfma_f32_32x32x16_f16 v[82:97], v[110:113], v[198:201], v[82:97]
	global_load_dwordx4 v[198:201], v214, s[36:37] offset:1024
	ds_read_b128 v[106:109], v213 offset:480
	ds_read_b128 v[110:113], v213 offset:33504
	s_waitcnt vmcnt(56) lgkmcnt(2)
	v_mfma_f32_32x32x16_f16 v[66:81], v[98:101], v[202:205], v[66:81]
	v_mfma_f32_32x32x16_f16 v[82:97], v[102:105], v[202:205], v[82:97]
	global_load_dwordx4 v[202:205], v214, s[36:37] offset:2048
	ds_read_b128 v[98:101], v213 offset:512
	ds_read_b128 v[102:105], v213 offset:33536
	s_waitcnt vmcnt(53) lgkmcnt(2)
	v_mfma_f32_32x32x16_f16 v[66:81], v[106:109], v[206:209], v[66:81]
	v_mfma_f32_32x32x16_f16 v[82:97], v[110:113], v[206:209], v[82:97]
	global_load_dwordx4 v[206:209], v214, s[36:37] offset:3072
	v_add_u32_e32 v214, 0x1000, v214
	ds_read_b128 v[106:109], v213 offset:544
	ds_read_b128 v[110:113], v213 offset:33568
	s_waitcnt vmcnt(49) lgkmcnt(2)
	v_mfma_f32_32x32x16_f16 v[66:81], v[98:101], v[146:149], v[66:81]
	v_mfma_f32_32x32x16_f16 v[82:97], v[102:105], v[146:149], v[82:97]
	global_load_dwordx4 v[146:149], v214, s[36:37]
	ds_read_b128 v[98:101], v213 offset:576
	ds_read_b128 v[102:105], v213 offset:33600
	s_waitcnt vmcnt(46) lgkmcnt(2)
	v_mfma_f32_32x32x16_f16 v[66:81], v[106:109], v[150:153], v[66:81]
	v_mfma_f32_32x32x16_f16 v[82:97], v[110:113], v[150:153], v[82:97]
	global_load_dwordx4 v[150:153], v214, s[36:37] offset:1024
	v_mov_b32_e32 v238, 0
	v_mov_b32_e32 v239, 0
	s_waitcnt vmcnt(10)
	s_branch .Llb_chk_1_0

.Llb_chk_1_0:
	v_mov_b32_e32 v243, 0
	v_and_b32_e32 v244, v114, v115
	v_alignbit_b32 v243, v244, v243, 1
	v_and_b32_e32 v244, v116, v117
	v_alignbit_b32 v243, v244, v243, 1
	v_and_b32_e32 v244, v118, v119
	v_alignbit_b32 v243, v244, v243, 1
	v_and_b32_e32 v244, v120, v121
	v_alignbit_b32 v243, v244, v243, 1
	v_and_b32_e32 v244, v122, v123
	v_alignbit_b32 v243, v244, v243, 1
	v_and_b32_e32 v244, v124, v125
	v_alignbit_b32 v243, v244, v243, 1
	v_and_b32_e32 v244, v126, v127
	v_alignbit_b32 v243, v244, v243, 1
	v_and_b32_e32 v244, v128, v129
	v_alignbit_b32 v243, v244, v243, 1
	v_and_b32_e32 v244, v130, v131
	v_alignbit_b32 v243, v244, v243, 1
	v_and_b32_e32 v244, v132, v133
	v_alignbit_b32 v243, v244, v243, 1
	v_and_b32_e32 v244, v134, v135
	v_alignbit_b32 v243, v244, v243, 1
	v_and_b32_e32 v244, v136, v137
	v_alignbit_b32 v243, v244, v243, 1
	v_and_b32_e32 v244, v138, v139
	v_alignbit_b32 v243, v244, v243, 1
	v_and_b32_e32 v244, v140, v141
	v_alignbit_b32 v243, v244, v243, 1
	v_and_b32_e32 v244, v142, v143
	v_alignbit_b32 v243, v244, v243, 1
	v_and_b32_e32 v244, v144, v145
	v_alignbit_b32 v243, v244, v243, 1
	v_lshrrev_b32_e32 v243, 16, v243
	v_and_b32_e32 v243, v243, v226
	v_cmp_ne_u32_e32 vcc, v243, v226
	s_nop 1
	s_cmp_eq_u64 vcc, 0
	s_cbranch_scc0 .Llb_retry_1_0
	ds_read_b128 v[106:109], v213 offset:608
	ds_read_b128 v[110:113], v213 offset:33632
	s_waitcnt vmcnt(43) lgkmcnt(2)
	v_mfma_f32_32x32x16_f16 v[66:81], v[98:101], v[154:157], v[66:81]
	v_mfma_f32_32x32x16_f16 v[82:97], v[102:105], v[154:157], v[82:97]
	global_load_dwordx4 v[154:157], v214, s[36:37] offset:2048
	v_cmp_lt_u32_e32 vcc, 0, v225
	v_fma_f32 v241, v232, v238, v114
	v_fma_f32 v242, v234, v238, v115
	v_fmac_f32_e32 v241, v233, v239
	v_fmac_f32_e32 v242, v235, v239
	v_cndmask_b32_e32 v238, v238, v241, vcc
	v_cndmask_b32_e32 v239, v239, v242, vcc
	v_cmp_lt_u32_e32 vcc, 1, v225
	v_fma_f32 v241, v232, v238, v116
	v_fma_f32 v242, v234, v238, v117
	v_fmac_f32_e32 v241, v233, v239
	v_fmac_f32_e32 v242, v235, v239
	v_cndmask_b32_e32 v238, v238, v241, vcc
	v_cndmask_b32_e32 v239, v239, v242, vcc
	v_cmp_lt_u32_e32 vcc, 2, v225
	v_fma_f32 v241, v232, v238, v118
	v_fma_f32 v242, v234, v238, v119
	v_fmac_f32_e32 v241, v233, v239
	v_fmac_f32_e32 v242, v235, v239
	v_cndmask_b32_e32 v238, v238, v241, vcc
	v_cndmask_b32_e32 v239, v239, v242, vcc
	v_cmp_lt_u32_e32 vcc, 3, v225
	v_fma_f32 v241, v232, v238, v120
	v_fma_f32 v242, v234, v238, v121
	v_fmac_f32_e32 v241, v233, v239
	v_fmac_f32_e32 v242, v235, v239
	v_cndmask_b32_e32 v238, v238, v241, vcc
	v_cndmask_b32_e32 v239, v239, v242, vcc
	ds_read_b128 v[98:101], v213 offset:640
	ds_read_b128 v[102:105], v213 offset:33664
	s_waitcnt vmcnt(40) lgkmcnt(2)
	v_mfma_f32_32x32x16_f16 v[66:81], v[106:109], v[158:161], v[66:81]
	v_mfma_f32_32x32x16_f16 v[82:97], v[110:113], v[158:161], v[82:97]
	global_load_dwordx4 v[158:161], v214, s[36:37] offset:3072
	v_add_u32_e32 v214, 0x1000, v214
	v_cmp_lt_u32_e32 vcc, 4, v225
	v_fma_f32 v241, v232, v238, v122
	v_fma_f32 v242, v234, v238, v123
	v_fmac_f32_e32 v241, v233, v239
	v_fmac_f32_e32 v242, v235, v239
	v_cndmask_b32_e32 v238, v238, v241, vcc
	v_cndmask_b32_e32 v239, v239, v242, vcc
	v_cmp_lt_u32_e32 vcc, 5, v225
	v_fma_f32 v241, v232, v238, v124
	v_fma_f32 v242, v234, v238, v125
	v_fmac_f32_e32 v241, v233, v239
	v_fmac_f32_e32 v242, v235, v239
	v_cndmask_b32_e32 v238, v238, v241, vcc
	v_cndmask_b32_e32 v239, v239, v242, vcc
	v_cmp_lt_u32_e32 vcc, 6, v225
	v_fma_f32 v241, v232, v238, v126
	v_fma_f32 v242, v234, v238, v127
	v_fmac_f32_e32 v241, v233, v239
	v_fmac_f32_e32 v242, v235, v239
	v_cndmask_b32_e32 v238, v238, v241, vcc
	v_cndmask_b32_e32 v239, v239, v242, vcc
	v_cmp_lt_u32_e32 vcc, 7, v225
	v_fma_f32 v241, v232, v238, v128
	v_fma_f32 v242, v234, v238, v129
	v_fmac_f32_e32 v241, v233, v239
	v_fmac_f32_e32 v242, v235, v239
	v_cndmask_b32_e32 v238, v238, v241, vcc
	v_cndmask_b32_e32 v239, v239, v242, vcc
	ds_read_b128 v[106:109], v213 offset:672
	ds_read_b128 v[110:113], v213 offset:33696
	s_waitcnt vmcnt(37) lgkmcnt(2)
	v_mfma_f32_32x32x16_f16 v[66:81], v[98:101], v[162:165], v[66:81]
	v_mfma_f32_32x32x16_f16 v[82:97], v[102:105], v[162:165], v[82:97]
	global_load_dwordx4 v[162:165], v214, s[36:37]
	v_cmp_lt_u32_e32 vcc, 8, v225
	v_fma_f32 v241, v232, v238, v130
	v_fma_f32 v242, v234, v238, v131
	v_fmac_f32_e32 v241, v233, v239
	v_fmac_f32_e32 v242, v235, v239
	v_cndmask_b32_e32 v238, v238, v241, vcc
	v_cndmask_b32_e32 v239, v239, v242, vcc
	v_cmp_lt_u32_e32 vcc, 9, v225
	v_fma_f32 v241, v232, v238, v132
	v_fma_f32 v242, v234, v238, v133
	v_fmac_f32_e32 v241, v233, v239
	v_fmac_f32_e32 v242, v235, v239
	v_cndmask_b32_e32 v238, v238, v241, vcc
	v_cndmask_b32_e32 v239, v239, v242, vcc
	v_cmp_lt_u32_e32 vcc, 10, v225
	v_fma_f32 v241, v232, v238, v134
	v_fma_f32 v242, v234, v238, v135
	v_fmac_f32_e32 v241, v233, v239
	v_fmac_f32_e32 v242, v235, v239
	v_cndmask_b32_e32 v238, v238, v241, vcc
	v_cndmask_b32_e32 v239, v239, v242, vcc
	v_cmp_lt_u32_e32 vcc, 11, v225
	v_fma_f32 v241, v232, v238, v136
	v_fma_f32 v242, v234, v238, v137
	v_fmac_f32_e32 v241, v233, v239
	v_fmac_f32_e32 v242, v235, v239
	v_cndmask_b32_e32 v238, v238, v241, vcc
	v_cndmask_b32_e32 v239, v239, v242, vcc
	ds_read_b128 v[98:101], v213 offset:704
	ds_read_b128 v[102:105], v213 offset:33728
	s_waitcnt vmcnt(34) lgkmcnt(2)
	v_mfma_f32_32x32x16_f16 v[66:81], v[106:109], v[166:169], v[66:81]
	v_mfma_f32_32x32x16_f16 v[82:97], v[110:113], v[166:169], v[82:97]
	global_load_dwordx4 v[166:169], v214, s[36:37] offset:1024
	v_cmp_lt_u32_e32 vcc, 12, v225
	v_fma_f32 v241, v232, v238, v138
	v_fma_f32 v242, v234, v238, v139
	v_fmac_f32_e32 v241, v233, v239
	v_fmac_f32_e32 v242, v235, v239
	v_cndmask_b32_e32 v238, v238, v241, vcc
	v_cndmask_b32_e32 v239, v239, v242, vcc
	v_cmp_lt_u32_e32 vcc, 13, v225
	v_fma_f32 v241, v232, v238, v140
	v_fma_f32 v242, v234, v238, v141
	v_fmac_f32_e32 v241, v233, v239
	v_fmac_f32_e32 v242, v235, v239
	v_cndmask_b32_e32 v238, v238, v241, vcc
	v_cndmask_b32_e32 v239, v239, v242, vcc
	v_cmp_lt_u32_e32 vcc, 14, v225
	v_fma_f32 v241, v232, v238, v142
	v_fma_f32 v242, v234, v238, v143
	v_fmac_f32_e32 v241, v233, v239
	v_fmac_f32_e32 v242, v235, v239
	v_cndmask_b32_e32 v238, v238, v241, vcc
	v_cndmask_b32_e32 v239, v239, v242, vcc
	v_cmp_lt_u32_e32 vcc, 15, v225
	v_fma_f32 v241, v232, v238, v144
	v_fma_f32 v242, v234, v238, v145
	v_fmac_f32_e32 v241, v233, v239
	v_fmac_f32_e32 v242, v235, v239
	v_cndmask_b32_e32 v238, v238, v241, vcc
	v_cndmask_b32_e32 v239, v239, v242, vcc
	s_mov_b64 s[40:41], s[50:51]
	global_load_dwordx2 v[114:115], v240, s[40:41] sc1
	s_add_u32 s40, s40, 0x2000
	s_addc_u32 s41, s41, 0
	global_load_dwordx2 v[116:117], v240, s[40:41] sc1
	s_add_u32 s40, s40, 0x2000
	s_addc_u32 s41, s41, 0
	global_load_dwordx2 v[118:119], v240, s[40:41] sc1
	s_add_u32 s40, s40, 0x2000
	s_addc_u32 s41, s41, 0
	global_load_dwordx2 v[120:121], v240, s[40:41] sc1
	s_add_u32 s40, s40, 0x2000
	s_addc_u32 s41, s41, 0
	global_load_dwordx2 v[122:123], v240, s[40:41] sc1
	s_add_u32 s40, s40, 0x2000
	s_addc_u32 s41, s41, 0
	global_load_dwordx2 v[124:125], v240, s[40:41] sc1
	s_add_u32 s40, s40, 0x2000
	s_addc_u32 s41, s41, 0
	global_load_dwordx2 v[126:127], v240, s[40:41] sc1
	s_add_u32 s40, s40, 0x2000
	s_addc_u32 s41, s41, 0
	global_load_dwordx2 v[128:129], v240, s[40:41] sc1
	s_add_u32 s40, s40, 0x2000
	s_addc_u32 s41, s41, 0
	global_load_dwordx2 v[130:131], v240, s[40:41] sc1
	s_add_u32 s40, s40, 0x2000
	s_addc_u32 s41, s41, 0
	global_load_dwordx2 v[132:133], v240, s[40:41] sc1
	s_add_u32 s40, s40, 0x2000
	s_addc_u32 s41, s41, 0
	global_load_dwordx2 v[134:135], v240, s[40:41] sc1
	s_add_u32 s40, s40, 0x2000
	s_addc_u32 s41, s41, 0
	global_load_dwordx2 v[136:137], v240, s[40:41] sc1
	s_add_u32 s40, s40, 0x2000
	s_addc_u32 s41, s41, 0
	global_load_dwordx2 v[138:139], v240, s[40:41] sc1
	s_add_u32 s40, s40, 0x2000
	s_addc_u32 s41, s41, 0
	global_load_dwordx2 v[140:141], v240, s[40:41] sc1
	s_add_u32 s40, s40, 0x2000
	s_addc_u32 s41, s41, 0
	global_load_dwordx2 v[142:143], v240, s[40:41] sc1
	s_add_u32 s40, s40, 0x2000
	s_addc_u32 s41, s41, 0
	global_load_dwordx2 v[144:145], v240, s[40:41] sc1
	ds_read_b128 v[106:109], v213 offset:736
	ds_read_b128 v[110:113], v213 offset:33760
	s_waitcnt vmcnt(47) lgkmcnt(2)
	v_mfma_f32_32x32x16_f16 v[66:81], v[98:101], v[170:173], v[66:81]
	v_mfma_f32_32x32x16_f16 v[82:97], v[102:105], v[170:173], v[82:97]
	global_load_dwordx4 v[170:173], v214, s[36:37] offset:2048
	ds_read_b128 v[98:101], v213 offset:768
	ds_read_b128 v[102:105], v213 offset:33792
	s_waitcnt vmcnt(47) lgkmcnt(2)
	v_mfma_f32_32x32x16_f16 v[66:81], v[106:109], v[174:177], v[66:81]
	v_mfma_f32_32x32x16_f16 v[82:97], v[110:113], v[174:177], v[82:97]
	global_load_dwordx4 v[174:177], v214, s[36:37] offset:3072
	v_add_u32_e32 v214, 0x1000, v214
	ds_read_b128 v[106:109], v213 offset:800
	ds_read_b128 v[110:113], v213 offset:33824
	s_waitcnt vmcnt(31) lgkmcnt(2)
	v_mfma_f32_32x32x16_f16 v[66:81], v[98:101], v[178:181], v[66:81]
	v_mfma_f32_32x32x16_f16 v[82:97], v[102:105], v[178:181], v[82:97]
	global_load_dwordx4 v[178:181], v214, s[36:37]
	ds_read_b128 v[98:101], v213 offset:832
	ds_read_b128 v[102:105], v213 offset:33856
	s_waitcnt vmcnt(31) lgkmcnt(2)
	v_mfma_f32_32x32x16_f16 v[66:81], v[106:109], v[182:185], v[66:81]
	v_mfma_f32_32x32x16_f16 v[82:97], v[110:113], v[182:185], v[82:97]
	global_load_dwordx4 v[182:185], v214, s[36:37] offset:1024
	ds_read_b128 v[106:109], v213 offset:864
	ds_read_b128 v[110:113], v213 offset:33888
	s_waitcnt vmcnt(31) lgkmcnt(2)
	v_mfma_f32_32x32x16_f16 v[66:81], v[98:101], v[186:189], v[66:81]
	v_mfma_f32_32x32x16_f16 v[82:97], v[102:105], v[186:189], v[82:97]
	global_load_dwordx4 v[186:189], v214, s[36:37] offset:2048
	ds_read_b128 v[98:101], v213 offset:896
	ds_read_b128 v[102:105], v213 offset:33920
	s_waitcnt vmcnt(31) lgkmcnt(2)
	v_mfma_f32_32x32x16_f16 v[66:81], v[106:109], v[190:193], v[66:81]
	v_mfma_f32_32x32x16_f16 v[82:97], v[110:113], v[190:193], v[82:97]
	global_load_dwordx4 v[190:193], v214, s[36:37] offset:3072
	v_add_u32_e32 v214, 0x1000, v214
	ds_read_b128 v[106:109], v213 offset:928
	ds_read_b128 v[110:113], v213 offset:33952
	s_waitcnt vmcnt(31) lgkmcnt(2)
	v_mfma_f32_32x32x16_f16 v[66:81], v[98:101], v[194:197], v[66:81]
	v_mfma_f32_32x32x16_f16 v[82:97], v[102:105], v[194:197], v[82:97]
	global_load_dwordx4 v[194:197], v214, s[36:37]
	ds_read_b128 v[98:101], v213 offset:960
	ds_read_b128 v[102:105], v213 offset:33984
	s_waitcnt vmcnt(31) lgkmcnt(2)
	v_mfma_f32_32x32x16_f16 v[66:81], v[106:109], v[198:201], v[66:81]
	v_mfma_f32_32x32x16_f16 v[82:97], v[110:113], v[198:201], v[82:97]
	global_load_dwordx4 v[198:201], v214, s[36:37] offset:1024
	ds_read_b128 v[106:109], v213 offset:992
	ds_read_b128 v[110:113], v213 offset:34016
	s_waitcnt vmcnt(31) lgkmcnt(2)
	v_mfma_f32_32x32x16_f16 v[66:81], v[98:101], v[202:205], v[66:81]
	v_mfma_f32_32x32x16_f16 v[82:97], v[102:105], v[202:205], v[82:97]
	global_load_dwordx4 v[202:205], v214, s[36:37] offset:2048
	ds_read_b128 v[98:101], v213 offset:1024
	ds_read_b128 v[102:105], v213 offset:34048
	s_waitcnt vmcnt(31) lgkmcnt(2)
	v_mfma_f32_32x32x16_f16 v[66:81], v[106:109], v[206:209], v[66:81]
	v_mfma_f32_32x32x16_f16 v[82:97], v[110:113], v[206:209], v[82:97]
	global_load_dwordx4 v[206:209], v214, s[36:37] offset:3072
	v_add_u32_e32 v214, 0x1000, v214
	s_waitcnt vmcnt(10)
	s_branch .Llb_chk_1_1

.Llb_chk_1_1:
	v_mov_b32_e32 v243, 0
	v_and_b32_e32 v244, v114, v115
	v_alignbit_b32 v243, v244, v243, 1
	v_and_b32_e32 v244, v116, v117
	v_alignbit_b32 v243, v244, v243, 1
	v_and_b32_e32 v244, v118, v119
	v_alignbit_b32 v243, v244, v243, 1
	v_and_b32_e32 v244, v120, v121
	v_alignbit_b32 v243, v244, v243, 1
	v_and_b32_e32 v244, v122, v123
	v_alignbit_b32 v243, v244, v243, 1
	v_and_b32_e32 v244, v124, v125
	v_alignbit_b32 v243, v244, v243, 1
	v_and_b32_e32 v244, v126, v127
	v_alignbit_b32 v243, v244, v243, 1
	v_and_b32_e32 v244, v128, v129
	v_alignbit_b32 v243, v244, v243, 1
	v_and_b32_e32 v244, v130, v131
	v_alignbit_b32 v243, v244, v243, 1
	v_and_b32_e32 v244, v132, v133
	v_alignbit_b32 v243, v244, v243, 1
	v_and_b32_e32 v244, v134, v135
	v_alignbit_b32 v243, v244, v243, 1
	v_and_b32_e32 v244, v136, v137
	v_alignbit_b32 v243, v244, v243, 1
	v_and_b32_e32 v244, v138, v139
	v_alignbit_b32 v243, v244, v243, 1
	v_and_b32_e32 v244, v140, v141
	v_alignbit_b32 v243, v244, v243, 1
	v_and_b32_e32 v244, v142, v143
	v_alignbit_b32 v243, v244, v243, 1
	v_and_b32_e32 v244, v144, v145
	v_alignbit_b32 v243, v244, v243, 1
	v_lshrrev_b32_e32 v243, 16, v243
	v_and_b32_e32 v243, v243, v227
	v_cmp_ne_u32_e32 vcc, v243, v227
	s_nop 1
	s_cmp_eq_u64 vcc, 0
	s_cbranch_scc0 .Llb_retry_1_1
	ds_read_b128 v[106:109], v213 offset:1056
	ds_read_b128 v[110:113], v213 offset:34080
	s_waitcnt vmcnt(31) lgkmcnt(2)
	v_mfma_f32_32x32x16_f16 v[66:81], v[98:101], v[146:149], v[66:81]
	v_mfma_f32_32x32x16_f16 v[82:97], v[102:105], v[146:149], v[82:97]
	global_load_dwordx4 v[146:149], v214, s[36:37]
	v_cmp_lt_u32_e32 vcc, 16, v225
	v_fma_f32 v241, v232, v238, v114
	v_fma_f32 v242, v234, v238, v115
	v_fmac_f32_e32 v241, v233, v239
	v_fmac_f32_e32 v242, v235, v239
	v_cndmask_b32_e32 v238, v238, v241, vcc
	v_cndmask_b32_e32 v239, v239, v242, vcc
	v_cmp_lt_u32_e32 vcc, 17, v225
	v_fma_f32 v241, v232, v238, v116
	v_fma_f32 v242, v234, v238, v117
	v_fmac_f32_e32 v241, v233, v239
	v_fmac_f32_e32 v242, v235, v239
	v_cndmask_b32_e32 v238, v238, v241, vcc
	v_cndmask_b32_e32 v239, v239, v242, vcc
	v_cmp_lt_u32_e32 vcc, 18, v225
	v_fma_f32 v241, v232, v238, v118
	v_fma_f32 v242, v234, v238, v119
	v_fmac_f32_e32 v241, v233, v239
	v_fmac_f32_e32 v242, v235, v239
	v_cndmask_b32_e32 v238, v238, v241, vcc
	v_cndmask_b32_e32 v239, v239, v242, vcc
	v_cmp_lt_u32_e32 vcc, 19, v225
	v_fma_f32 v241, v232, v238, v120
	v_fma_f32 v242, v234, v238, v121
	v_fmac_f32_e32 v241, v233, v239
	v_fmac_f32_e32 v242, v235, v239
	v_cndmask_b32_e32 v238, v238, v241, vcc
	v_cndmask_b32_e32 v239, v239, v242, vcc
	ds_read_b128 v[98:101], v213 offset:1088
	ds_read_b128 v[102:105], v213 offset:34112
	s_waitcnt vmcnt(31) lgkmcnt(2)
	v_mfma_f32_32x32x16_f16 v[66:81], v[106:109], v[150:153], v[66:81]
	v_mfma_f32_32x32x16_f16 v[82:97], v[110:113], v[150:153], v[82:97]
	global_load_dwordx4 v[150:153], v214, s[36:37] offset:1024
	v_cmp_lt_u32_e32 vcc, 20, v225
	v_fma_f32 v241, v232, v238, v122
	v_fma_f32 v242, v234, v238, v123
	v_fmac_f32_e32 v241, v233, v239
	v_fmac_f32_e32 v242, v235, v239
	v_cndmask_b32_e32 v238, v238, v241, vcc
	v_cndmask_b32_e32 v239, v239, v242, vcc
	v_cmp_lt_u32_e32 vcc, 21, v225
	v_fma_f32 v241, v232, v238, v124
	v_fma_f32 v242, v234, v238, v125
	v_fmac_f32_e32 v241, v233, v239
	v_fmac_f32_e32 v242, v235, v239
	v_cndmask_b32_e32 v238, v238, v241, vcc
	v_cndmask_b32_e32 v239, v239, v242, vcc
	v_cmp_lt_u32_e32 vcc, 22, v225
	v_fma_f32 v241, v232, v238, v126
	v_fma_f32 v242, v234, v238, v127
	v_fmac_f32_e32 v241, v233, v239
	v_fmac_f32_e32 v242, v235, v239
	v_cndmask_b32_e32 v238, v238, v241, vcc
	v_cndmask_b32_e32 v239, v239, v242, vcc
	v_cmp_lt_u32_e32 vcc, 23, v225
	v_fma_f32 v241, v232, v238, v128
	v_fma_f32 v242, v234, v238, v129
	v_fmac_f32_e32 v241, v233, v239
	v_fmac_f32_e32 v242, v235, v239
	v_cndmask_b32_e32 v238, v238, v241, vcc
	v_cndmask_b32_e32 v239, v239, v242, vcc
	ds_read_b128 v[106:109], v213 offset:1120
	ds_read_b128 v[110:113], v213 offset:34144
	s_waitcnt vmcnt(31) lgkmcnt(2)
	v_mfma_f32_32x32x16_f16 v[66:81], v[98:101], v[154:157], v[66:81]
	v_mfma_f32_32x32x16_f16 v[82:97], v[102:105], v[154:157], v[82:97]
	global_load_dwordx4 v[154:157], v214, s[36:37] offset:2048
	v_cmp_lt_u32_e32 vcc, 24, v225
	v_fma_f32 v241, v232, v238, v130
	v_fma_f32 v242, v234, v238, v131
	v_fmac_f32_e32 v241, v233, v239
	v_fmac_f32_e32 v242, v235, v239
	v_cndmask_b32_e32 v238, v238, v241, vcc
	v_cndmask_b32_e32 v239, v239, v242, vcc
	v_cmp_lt_u32_e32 vcc, 25, v225
	v_fma_f32 v241, v232, v238, v132
	v_fma_f32 v242, v234, v238, v133
	v_fmac_f32_e32 v241, v233, v239
	v_fmac_f32_e32 v242, v235, v239
	v_cndmask_b32_e32 v238, v238, v241, vcc
	v_cndmask_b32_e32 v239, v239, v242, vcc
	v_cmp_lt_u32_e32 vcc, 26, v225
	v_fma_f32 v241, v232, v238, v134
	v_fma_f32 v242, v234, v238, v135
	v_fmac_f32_e32 v241, v233, v239
	v_fmac_f32_e32 v242, v235, v239
	v_cndmask_b32_e32 v238, v238, v241, vcc
	v_cndmask_b32_e32 v239, v239, v242, vcc
	v_cmp_lt_u32_e32 vcc, 27, v225
	v_fma_f32 v241, v232, v238, v136
	v_fma_f32 v242, v234, v238, v137
	v_fmac_f32_e32 v241, v233, v239
	v_fmac_f32_e32 v242, v235, v239
	v_cndmask_b32_e32 v238, v238, v241, vcc
	v_cndmask_b32_e32 v239, v239, v242, vcc
	ds_read_b128 v[98:101], v213 offset:1152
	ds_read_b128 v[102:105], v213 offset:34176
	s_waitcnt vmcnt(31) lgkmcnt(2)
	v_mfma_f32_32x32x16_f16 v[66:81], v[106:109], v[158:161], v[66:81]
	v_mfma_f32_32x32x16_f16 v[82:97], v[110:113], v[158:161], v[82:97]
	global_load_dwordx4 v[158:161], v214, s[36:37] offset:3072
	v_add_u32_e32 v214, 0x1000, v214
	v_cmp_lt_u32_e32 vcc, 28, v225
	v_fma_f32 v241, v232, v238, v138
	v_fma_f32 v242, v234, v238, v139
	v_fmac_f32_e32 v241, v233, v239
	v_fmac_f32_e32 v242, v235, v239
	v_cndmask_b32_e32 v238, v238, v241, vcc
	v_cndmask_b32_e32 v239, v239, v242, vcc
	v_cmp_lt_u32_e32 vcc, 29, v225
	v_fma_f32 v241, v232, v238, v140
	v_fma_f32 v242, v234, v238, v141
	v_fmac_f32_e32 v241, v233, v239
	v_fmac_f32_e32 v242, v235, v239
	v_cndmask_b32_e32 v238, v238, v241, vcc
	v_cndmask_b32_e32 v239, v239, v242, vcc
	v_cmp_lt_u32_e32 vcc, 30, v225
	v_fma_f32 v241, v232, v238, v142
	v_fma_f32 v242, v234, v238, v143
	v_fmac_f32_e32 v241, v233, v239
	v_fmac_f32_e32 v242, v235, v239
	v_cndmask_b32_e32 v238, v238, v241, vcc
	v_cndmask_b32_e32 v239, v239, v242, vcc
	v_cmp_lt_u32_e32 vcc, 31, v225
	v_fma_f32 v241, v232, v238, v144
	v_fma_f32 v242, v234, v238, v145
	v_fmac_f32_e32 v241, v233, v239
	v_fmac_f32_e32 v242, v235, v239
	v_cndmask_b32_e32 v238, v238, v241, vcc
	v_cndmask_b32_e32 v239, v239, v242, vcc
	ds_read_b128 v[106:109], v213 offset:1184
	ds_read_b128 v[110:113], v213 offset:34208
	s_waitcnt vmcnt(31) lgkmcnt(2)
	v_mfma_f32_32x32x16_f16 v[66:81], v[98:101], v[162:165], v[66:81]
	v_mfma_f32_32x32x16_f16 v[82:97], v[102:105], v[162:165], v[82:97]
	global_load_dwordx4 v[162:165], v214, s[36:37]
	ds_bpermute_b32 v247, v224, v238
	ds_bpermute_b32 v248, v224, v239
	s_waitcnt lgkmcnt(0)
	v_cndmask_b32_e64 v249, v238, v247, s[46:47]
	v_cndmask_b32_e64 v250, v239, v248, s[46:47]
	v_cndmask_b32_e64 v251, v247, v238, s[46:47]
	v_cndmask_b32_e64 v252, v248, v239, s[46:47]
	s_sub_i32 s44, s18, 32
	s_cmp_gt_i32 s44, 0
	s_cbranch_scc0 .Llb_np_1

.Llb_np_1:
	v_add_f32_e32 v238, v249, v251
	v_add_f32_e32 v239, v250, v252
	ds_read_b128 v[98:101], v213 offset:1216
	ds_read_b128 v[102:105], v213 offset:34240
	s_waitcnt vmcnt(31) lgkmcnt(2)
	v_mfma_f32_32x32x16_f16 v[66:81], v[106:109], v[166:169], v[66:81]
	v_mfma_f32_32x32x16_f16 v[82:97], v[110:113], v[166:169], v[82:97]
	global_load_dwordx4 v[166:169], v214, s[36:37] offset:1024
	v_fma_f32 v245, v228, v238, v236
	v_fma_f32 v246, v230, v238, v237
	v_fmac_f32_e32 v245, v229, v239
	v_fmac_f32_e32 v246, v231, v239
	v_cndmask_b32_e64 v220, v238, v245, s[46:47]
	v_cndmask_b32_e64 v221, v239, v246, s[46:47]
	v_lshl_add_u32 v215, v212, 17, v223
	v_add_u32_e32 v215, 0x1080, v215
	ds_read_b128 v[106:109], v213 offset:1248
	ds_read_b128 v[110:113], v213 offset:34272
	s_waitcnt vmcnt(15) lgkmcnt(2)
	v_mfma_f32_32x32x16_f16 v[66:81], v[98:101], v[170:173], v[66:81]
	v_mfma_f32_32x32x16_f16 v[82:97], v[102:105], v[170:173], v[82:97]
	global_load_dwordx4 v[170:173], v214, s[36:37] offset:2048
	v_fma_f32 v222, -v221, v217, v34
	v_fmac_f32_e32 v220, 0x3dcccccd, v222
	v_fmac_f32_e32 v221, 0x3dcccccd, v220
	global_store_dword v215, v221, s[30:31] offset:-4096
	global_store_dword v215, v220, s[32:33] offset:-4096
	global_store_dword v215, v221, s[34:35] offset:-4096
	ds_read_b128 v[98:101], v213 offset:1280
	ds_read_b128 v[102:105], v213 offset:34304
	s_waitcnt vmcnt(18) lgkmcnt(2)
	v_mfma_f32_32x32x16_f16 v[66:81], v[106:109], v[174:177], v[66:81]
	v_mfma_f32_32x32x16_f16 v[82:97], v[110:113], v[174:177], v[82:97]
	global_load_dwordx4 v[174:177], v214, s[36:37] offset:3072
	v_add_u32_e32 v214, 0x1000, v214
	v_fma_f32 v222, -v221, v217, v35
	v_fmac_f32_e32 v220, 0x3dcccccd, v222
	v_fmac_f32_e32 v221, 0x3dcccccd, v220
	global_store_dword v215, v221, s[30:31]
	global_store_dword v215, v220, s[32:33]
	global_store_dword v215, v221, s[34:35]
	v_add_u32_e32 v215, 0x2000, v215
	ds_read_b128 v[106:109], v213 offset:1312
	ds_read_b128 v[110:113], v213 offset:34336
	s_waitcnt vmcnt(21) lgkmcnt(2)
	v_mfma_f32_32x32x16_f16 v[66:81], v[98:101], v[178:181], v[66:81]
	v_mfma_f32_32x32x16_f16 v[82:97], v[102:105], v[178:181], v[82:97]
	global_load_dwordx4 v[178:181], v214, s[36:37]
	v_fma_f32 v222, -v221, v217, v36
	v_fmac_f32_e32 v220, 0x3dcccccd, v222
	v_fmac_f32_e32 v221, 0x3dcccccd, v220
	global_store_dword v215, v221, s[30:31] offset:-4096
	global_store_dword v215, v220, s[32:33] offset:-4096
	global_store_dword v215, v221, s[34:35] offset:-4096
	ds_read_b128 v[98:101], v213 offset:1344
	ds_read_b128 v[102:105], v213 offset:34368
	s_waitcnt vmcnt(24) lgkmcnt(2)
	v_mfma_f32_32x32x16_f16 v[66:81], v[106:109], v[182:185], v[66:81]
	v_mfma_f32_32x32x16_f16 v[82:97], v[110:113], v[182:185], v[82:97]
	global_load_dwordx4 v[182:185], v214, s[36:37] offset:1024
	v_fma_f32 v222, -v221, v217, v37
	v_fmac_f32_e32 v220, 0x3dcccccd, v222
	v_fmac_f32_e32 v221, 0x3dcccccd, v220
	global_store_dword v215, v221, s[30:31]
	global_store_dword v215, v220, s[32:33]
	global_store_dword v215, v221, s[34:35]
	v_add_u32_e32 v215, 0x2000, v215
	ds_read_b128 v[106:109], v213 offset:1376
	ds_read_b128 v[110:113], v213 offset:34400
	s_waitcnt vmcnt(27) lgkmcnt(2)
	v_mfma_f32_32x32x16_f16 v[66:81], v[98:101], v[186:189], v[66:81]
	v_mfma_f32_32x32x16_f16 v[82:97], v[102:105], v[186:189], v[82:97]
	global_load_dwordx4 v[186:189], v214, s[36:37] offset:2048
	v_fma_f32 v222, -v221, v217, v38
	v_fmac_f32_e32 v220, 0x3dcccccd, v222
	v_fmac_f32_e32 v221, 0x3dcccccd, v220
	global_store_dword v215, v221, s[30:31] offset:-4096
	global_store_dword v215, v220, s[32:33] offset:-4096
	global_store_dword v215, v221, s[34:35] offset:-4096
	ds_read_b128 v[98:101], v213 offset:1408
	ds_read_b128 v[102:105], v213 offset:34432
	s_waitcnt vmcnt(30) lgkmcnt(2)
	v_mfma_f32_32x32x16_f16 v[66:81], v[106:109], v[190:193], v[66:81]
	v_mfma_f32_32x32x16_f16 v[82:97], v[110:113], v[190:193], v[82:97]
	global_load_dwordx4 v[190:193], v214, s[36:37] offset:3072
	v_add_u32_e32 v214, 0x1000, v214
	v_fma_f32 v222, -v221, v217, v39
	v_fmac_f32_e32 v220, 0x3dcccccd, v222
	v_fmac_f32_e32 v221, 0x3dcccccd, v220
	global_store_dword v215, v221, s[30:31]
	global_store_dword v215, v220, s[32:33]
	global_store_dword v215, v221, s[34:35]
	v_add_u32_e32 v215, 0x2000, v215
	ds_read_b128 v[106:109], v213 offset:1440
	ds_read_b128 v[110:113], v213 offset:34464
	s_waitcnt vmcnt(33) lgkmcnt(2)
	v_mfma_f32_32x32x16_f16 v[66:81], v[98:101], v[194:197], v[66:81]
	v_mfma_f32_32x32x16_f16 v[82:97], v[102:105], v[194:197], v[82:97]
	global_load_dwordx4 v[194:197], v214, s[36:37]
	v_fma_f32 v222, -v221, v217, v40
	v_fmac_f32_e32 v220, 0x3dcccccd, v222
	v_fmac_f32_e32 v221, 0x3dcccccd, v220
	global_store_dword v215, v221, s[30:31] offset:-4096
	global_store_dword v215, v220, s[32:33] offset:-4096
	global_store_dword v215, v221, s[34:35] offset:-4096
	ds_read_b128 v[98:101], v213 offset:1472
	ds_read_b128 v[102:105], v213 offset:34496
	s_waitcnt vmcnt(36) lgkmcnt(2)
	v_mfma_f32_32x32x16_f16 v[66:81], v[106:109], v[198:201], v[66:81]
	v_mfma_f32_32x32x16_f16 v[82:97], v[110:113], v[198:201], v[82:97]
	global_load_dwordx4 v[198:201], v214, s[36:37] offset:1024
	v_fma_f32 v222, -v221, v217, v41
	v_fmac_f32_e32 v220, 0x3dcccccd, v222
	v_fmac_f32_e32 v221, 0x3dcccccd, v220
	global_store_dword v215, v221, s[30:31]
	global_store_dword v215, v220, s[32:33]
	global_store_dword v215, v221, s[34:35]
	v_add_u32_e32 v215, 0x2000, v215
	ds_read_b128 v[106:109], v213 offset:1504
	ds_read_b128 v[110:113], v213 offset:34528
	s_waitcnt vmcnt(39) lgkmcnt(2)
	v_mfma_f32_32x32x16_f16 v[66:81], v[98:101], v[202:205], v[66:81]
	v_mfma_f32_32x32x16_f16 v[82:97], v[102:105], v[202:205], v[82:97]
	global_load_dwordx4 v[202:205], v214, s[36:37] offset:2048
	v_fma_f32 v222, -v221, v217, v42
	v_fmac_f32_e32 v220, 0x3dcccccd, v222
	v_fmac_f32_e32 v221, 0x3dcccccd, v220
	global_store_dword v215, v221, s[30:31] offset:-4096
	global_store_dword v215, v220, s[32:33] offset:-4096
	global_store_dword v215, v221, s[34:35] offset:-4096
	ds_read_b128 v[98:101], v213 offset:1536
	ds_read_b128 v[102:105], v213 offset:34560
	s_waitcnt vmcnt(42) lgkmcnt(2)
	v_mfma_f32_32x32x16_f16 v[66:81], v[106:109], v[206:209], v[66:81]
	v_mfma_f32_32x32x16_f16 v[82:97], v[110:113], v[206:209], v[82:97]
	global_load_dwordx4 v[206:209], v214, s[36:37] offset:3072
	v_add_u32_e32 v214, 0x1000, v214
	v_fma_f32 v222, -v221, v217, v43
	v_fmac_f32_e32 v220, 0x3dcccccd, v222
	v_fmac_f32_e32 v221, 0x3dcccccd, v220
	global_store_dword v215, v221, s[30:31]
	global_store_dword v215, v220, s[32:33]
	global_store_dword v215, v221, s[34:35]
	v_add_u32_e32 v215, 0x2000, v215
	ds_read_b128 v[106:109], v213 offset:1568
	ds_read_b128 v[110:113], v213 offset:34592
	s_waitcnt vmcnt(45) lgkmcnt(2)
	v_mfma_f32_32x32x16_f16 v[66:81], v[98:101], v[146:149], v[66:81]
	v_mfma_f32_32x32x16_f16 v[82:97], v[102:105], v[146:149], v[82:97]
	global_load_dwordx4 v[146:149], v214, s[36:37]
	v_fma_f32 v222, -v221, v217, v44
	v_fmac_f32_e32 v220, 0x3dcccccd, v222
	v_fmac_f32_e32 v221, 0x3dcccccd, v220
	global_store_dword v215, v221, s[30:31] offset:-4096
	global_store_dword v215, v220, s[32:33] offset:-4096
	global_store_dword v215, v221, s[34:35] offset:-4096
	ds_read_b128 v[98:101], v213 offset:1600
	ds_read_b128 v[102:105], v213 offset:34624
	s_waitcnt vmcnt(48) lgkmcnt(2)
	v_mfma_f32_32x32x16_f16 v[66:81], v[106:109], v[150:153], v[66:81]
	v_mfma_f32_32x32x16_f16 v[82:97], v[110:113], v[150:153], v[82:97]
	global_load_dwordx4 v[150:153], v214, s[36:37] offset:1024
	v_fma_f32 v222, -v221, v217, v45
	v_fmac_f32_e32 v220, 0x3dcccccd, v222
	v_fmac_f32_e32 v221, 0x3dcccccd, v220
	global_store_dword v215, v221, s[30:31]
	global_store_dword v215, v220, s[32:33]
	global_store_dword v215, v221, s[34:35]
	v_add_u32_e32 v215, 0x2000, v215
	ds_read_b128 v[106:109], v213 offset:1632
	ds_read_b128 v[110:113], v213 offset:34656
	s_waitcnt vmcnt(51) lgkmcnt(2)
	v_mfma_f32_32x32x16_f16 v[66:81], v[98:101], v[154:157], v[66:81]
	v_mfma_f32_32x32x16_f16 v[82:97], v[102:105], v[154:157], v[82:97]
	global_load_dwordx4 v[154:157], v214, s[36:37] offset:2048
	v_fma_f32 v222, -v221, v217, v46
	v_fmac_f32_e32 v220, 0x3dcccccd, v222
	v_fmac_f32_e32 v221, 0x3dcccccd, v220
	global_store_dword v215, v221, s[30:31] offset:-4096
	global_store_dword v215, v220, s[32:33] offset:-4096
	global_store_dword v215, v221, s[34:35] offset:-4096
	ds_read_b128 v[98:101], v213 offset:1664
	ds_read_b128 v[102:105], v213 offset:34688
	s_waitcnt vmcnt(54) lgkmcnt(2)
	v_mfma_f32_32x32x16_f16 v[66:81], v[106:109], v[158:161], v[66:81]
	v_mfma_f32_32x32x16_f16 v[82:97], v[110:113], v[158:161], v[82:97]
	global_load_dwordx4 v[158:161], v214, s[36:37] offset:3072
	v_add_u32_e32 v214, 0x1000, v214
	v_fma_f32 v222, -v221, v217, v47
	v_fmac_f32_e32 v220, 0x3dcccccd, v222
	v_fmac_f32_e32 v221, 0x3dcccccd, v220
	global_store_dword v215, v221, s[30:31]
	global_store_dword v215, v220, s[32:33]
	global_store_dword v215, v221, s[34:35]
	v_add_u32_e32 v215, 0x2000, v215
	ds_read_b128 v[106:109], v213 offset:1696
	ds_read_b128 v[110:113], v213 offset:34720
	s_waitcnt vmcnt(57) lgkmcnt(2)
	v_mfma_f32_32x32x16_f16 v[66:81], v[98:101], v[162:165], v[66:81]
	v_mfma_f32_32x32x16_f16 v[82:97], v[102:105], v[162:165], v[82:97]
	global_load_dwordx4 v[162:165], v214, s[36:37]
	v_fma_f32 v222, -v221, v217, v48
	v_fmac_f32_e32 v220, 0x3dcccccd, v222
	v_fmac_f32_e32 v221, 0x3dcccccd, v220
	global_store_dword v215, v221, s[30:31] offset:-4096
	global_store_dword v215, v220, s[32:33] offset:-4096
	global_store_dword v215, v221, s[34:35] offset:-4096
	ds_read_b128 v[98:101], v213 offset:1728
	ds_read_b128 v[102:105], v213 offset:34752
	s_waitcnt vmcnt(60) lgkmcnt(2)
	v_mfma_f32_32x32x16_f16 v[66:81], v[106:109], v[166:169], v[66:81]
	v_mfma_f32_32x32x16_f16 v[82:97], v[110:113], v[166:169], v[82:97]
	global_load_dwordx4 v[166:169], v214, s[36:37] offset:1024
	v_fma_f32 v222, -v221, v217, v49
	v_fmac_f32_e32 v220, 0x3dcccccd, v222
	v_fmac_f32_e32 v221, 0x3dcccccd, v220
	global_store_dword v215, v221, s[30:31]
	global_store_dword v215, v220, s[32:33]
	global_store_dword v215, v221, s[34:35]
	v_add_u32_e32 v215, 0x2000, v215
	ds_read_b128 v[106:109], v213 offset:1760
	ds_read_b128 v[110:113], v213 offset:34784
	s_waitcnt vmcnt(63) lgkmcnt(2)
	v_mfma_f32_32x32x16_f16 v[66:81], v[98:101], v[170:173], v[66:81]
	v_mfma_f32_32x32x16_f16 v[82:97], v[102:105], v[170:173], v[82:97]
	global_load_dwordx4 v[170:173], v214, s[36:37] offset:2048
	v_fma_f32 v222, -v221, v217, v50
	v_fmac_f32_e32 v220, 0x3dcccccd, v222
	v_fmac_f32_e32 v221, 0x3dcccccd, v220
	global_store_dword v215, v221, s[30:31] offset:-4096
	global_store_dword v215, v220, s[32:33] offset:-4096
	global_store_dword v215, v221, s[34:35] offset:-4096
	ds_read_b128 v[98:101], v213 offset:1792
	ds_read_b128 v[102:105], v213 offset:34816
	s_waitcnt vmcnt(63) lgkmcnt(2)
	v_mfma_f32_32x32x16_f16 v[66:81], v[106:109], v[174:177], v[66:81]
	v_mfma_f32_32x32x16_f16 v[82:97], v[110:113], v[174:177], v[82:97]
	global_load_dwordx4 v[174:177], v214, s[36:37] offset:3072
	v_add_u32_e32 v214, 0x1000, v214
	v_fma_f32 v222, -v221, v217, v51
	v_fmac_f32_e32 v220, 0x3dcccccd, v222
	v_fmac_f32_e32 v221, 0x3dcccccd, v220
	global_store_dword v215, v221, s[30:31]
	global_store_dword v215, v220, s[32:33]
	global_store_dword v215, v221, s[34:35]
	v_add_u32_e32 v215, 0x2000, v215
	ds_read_b128 v[106:109], v213 offset:1824
	ds_read_b128 v[110:113], v213 offset:34848
	s_waitcnt vmcnt(63) lgkmcnt(2)
	v_mfma_f32_32x32x16_f16 v[66:81], v[98:101], v[178:181], v[66:81]
	v_mfma_f32_32x32x16_f16 v[82:97], v[102:105], v[178:181], v[82:97]
	global_load_dwordx4 v[178:181], v214, s[36:37]
	v_fma_f32 v222, -v221, v217, v52
	v_fmac_f32_e32 v220, 0x3dcccccd, v222
	v_fmac_f32_e32 v221, 0x3dcccccd, v220
	global_store_dword v215, v221, s[30:31] offset:-4096
	global_store_dword v215, v220, s[32:33] offset:-4096
	global_store_dword v215, v221, s[34:35] offset:-4096
	ds_read_b128 v[98:101], v213 offset:1856
	ds_read_b128 v[102:105], v213 offset:34880
	s_waitcnt vmcnt(63) lgkmcnt(2)
	v_mfma_f32_32x32x16_f16 v[66:81], v[106:109], v[182:185], v[66:81]
	v_mfma_f32_32x32x16_f16 v[82:97], v[110:113], v[182:185], v[82:97]
	global_load_dwordx4 v[182:185], v214, s[36:37] offset:1024
	v_fma_f32 v222, -v221, v217, v53
	v_fmac_f32_e32 v220, 0x3dcccccd, v222
	v_fmac_f32_e32 v221, 0x3dcccccd, v220
	global_store_dword v215, v221, s[30:31]
	global_store_dword v215, v220, s[32:33]
	global_store_dword v215, v221, s[34:35]
	v_add_u32_e32 v215, 0x2000, v215
	ds_read_b128 v[106:109], v213 offset:1888
	ds_read_b128 v[110:113], v213 offset:34912
	s_waitcnt vmcnt(63) lgkmcnt(2)
	v_mfma_f32_32x32x16_f16 v[66:81], v[98:101], v[186:189], v[66:81]
	v_mfma_f32_32x32x16_f16 v[82:97], v[102:105], v[186:189], v[82:97]
	global_load_dwordx4 v[186:189], v214, s[36:37] offset:2048
	v_fma_f32 v222, -v221, v217, v54
	v_fmac_f32_e32 v220, 0x3dcccccd, v222
	v_fmac_f32_e32 v221, 0x3dcccccd, v220
	global_store_dword v215, v221, s[30:31] offset:-4096
	global_store_dword v215, v220, s[32:33] offset:-4096
	global_store_dword v215, v221, s[34:35] offset:-4096
	ds_read_b128 v[98:101], v213 offset:1920
	ds_read_b128 v[102:105], v213 offset:34944
	s_waitcnt vmcnt(63) lgkmcnt(2)
	v_mfma_f32_32x32x16_f16 v[66:81], v[106:109], v[190:193], v[66:81]
	v_mfma_f32_32x32x16_f16 v[82:97], v[110:113], v[190:193], v[82:97]
	global_load_dwordx4 v[190:193], v214, s[36:37] offset:3072
	v_add_u32_e32 v214, 0x1000, v214
	v_fma_f32 v222, -v221, v217, v55
	v_fmac_f32_e32 v220, 0x3dcccccd, v222
	v_fmac_f32_e32 v221, 0x3dcccccd, v220
	global_store_dword v215, v221, s[30:31]
	global_store_dword v215, v220, s[32:33]
	global_store_dword v215, v221, s[34:35]
	v_add_u32_e32 v215, 0x2000, v215
	ds_read_b128 v[106:109], v213 offset:1952
	ds_read_b128 v[110:113], v213 offset:34976
	s_waitcnt vmcnt(63) lgkmcnt(2)
	v_mfma_f32_32x32x16_f16 v[66:81], v[98:101], v[194:197], v[66:81]
	v_mfma_f32_32x32x16_f16 v[82:97], v[102:105], v[194:197], v[82:97]
	global_load_dwordx4 v[194:197], v214, s[36:37]
	v_fma_f32 v222, -v221, v217, v56
	v_fmac_f32_e32 v220, 0x3dcccccd, v222
	v_fmac_f32_e32 v221, 0x3dcccccd, v220
	global_store_dword v215, v221, s[30:31] offset:-4096
	global_store_dword v215, v220, s[32:33] offset:-4096
	global_store_dword v215, v221, s[34:35] offset:-4096
	ds_read_b128 v[98:101], v213 offset:1984
	ds_read_b128 v[102:105], v213 offset:35008
	s_waitcnt vmcnt(63) lgkmcnt(2)
	v_mfma_f32_32x32x16_f16 v[66:81], v[106:109], v[198:201], v[66:81]
	v_mfma_f32_32x32x16_f16 v[82:97], v[110:113], v[198:201], v[82:97]
	global_load_dwordx4 v[198:201], v214, s[36:37] offset:1024
	v_fma_f32 v222, -v221, v217, v57
	v_fmac_f32_e32 v220, 0x3dcccccd, v222
	v_fmac_f32_e32 v221, 0x3dcccccd, v220
	global_store_dword v215, v221, s[30:31]
	global_store_dword v215, v220, s[32:33]
	global_store_dword v215, v221, s[34:35]
	v_add_u32_e32 v215, 0x2000, v215
	ds_read_b128 v[106:109], v213 offset:2016
	ds_read_b128 v[110:113], v213 offset:35040
	s_waitcnt vmcnt(63) lgkmcnt(2)
	v_mfma_f32_32x32x16_f16 v[66:81], v[98:101], v[202:205], v[66:81]
	v_mfma_f32_32x32x16_f16 v[82:97], v[102:105], v[202:205], v[82:97]
	global_load_dwordx4 v[202:205], v214, s[36:37] offset:2048
	v_fma_f32 v222, -v221, v217, v58
	v_fmac_f32_e32 v220, 0x3dcccccd, v222
	v_fmac_f32_e32 v221, 0x3dcccccd, v220
	global_store_dword v215, v221, s[30:31] offset:-4096
	global_store_dword v215, v220, s[32:33] offset:-4096
	global_store_dword v215, v221, s[34:35] offset:-4096
	s_waitcnt vmcnt(63) lgkmcnt(0)
	v_mfma_f32_32x32x16_f16 v[66:81], v[106:109], v[206:209], v[66:81]
	v_mfma_f32_32x32x16_f16 v[82:97], v[110:113], v[206:209], v[82:97]
	global_load_dwordx4 v[206:209], v214, s[36:37] offset:3072
	v_add_u32_e32 v214, 0x1000, v214
	v_fma_f32 v222, -v221, v217, v59
	v_fmac_f32_e32 v220, 0x3dcccccd, v222
	v_fmac_f32_e32 v221, 0x3dcccccd, v220
	global_store_dword v215, v221, s[30:31]
	global_store_dword v215, v220, s[32:33]
	global_store_dword v215, v221, s[34:35]
	v_add_u32_e32 v215, 0x2000, v215
	s_nop 15
	v_mov_b32_e32 v254, 0
	v_mov_b32_e32 v255, 0
	v_fma_f32 v241, -v255, v218, v66
	v_fmac_f32_e32 v254, 0x3dcccccd, v241
	v_fmac_f32_e32 v255, 0x3dcccccd, v254
	v_fma_f32 v241, -v255, v218, v67
	v_fmac_f32_e32 v254, 0x3dcccccd, v241
	v_fmac_f32_e32 v255, 0x3dcccccd, v254
	v_fma_f32 v241, -v255, v218, v68
	v_fmac_f32_e32 v254, 0x3dcccccd, v241
	v_fmac_f32_e32 v255, 0x3dcccccd, v254
	v_fma_f32 v241, -v255, v218, v69
	v_fmac_f32_e32 v254, 0x3dcccccd, v241
	v_fmac_f32_e32 v255, 0x3dcccccd, v254
	v_fma_f32 v241, -v255, v218, v70
	v_fmac_f32_e32 v254, 0x3dcccccd, v241
	v_fmac_f32_e32 v255, 0x3dcccccd, v254
	v_fma_f32 v241, -v255, v218, v71
	v_fmac_f32_e32 v254, 0x3dcccccd, v241
	v_fmac_f32_e32 v255, 0x3dcccccd, v254
	v_fma_f32 v241, -v255, v218, v72
	v_fmac_f32_e32 v254, 0x3dcccccd, v241
	v_fmac_f32_e32 v255, 0x3dcccccd, v254
	v_fma_f32 v241, -v255, v218, v73
	v_fmac_f32_e32 v254, 0x3dcccccd, v241
	v_fmac_f32_e32 v255, 0x3dcccccd, v254
	v_fma_f32 v241, -v255, v218, v74
	v_fmac_f32_e32 v254, 0x3dcccccd, v241
	v_fmac_f32_e32 v255, 0x3dcccccd, v254
	v_fma_f32 v241, -v255, v218, v75
	v_fmac_f32_e32 v254, 0x3dcccccd, v241
	v_fmac_f32_e32 v255, 0x3dcccccd, v254
	v_fma_f32 v241, -v255, v218, v76
	v_fmac_f32_e32 v254, 0x3dcccccd, v241
	v_fmac_f32_e32 v255, 0x3dcccccd, v254
	v_fma_f32 v241, -v255, v218, v77
	v_fmac_f32_e32 v254, 0x3dcccccd, v241
	v_fmac_f32_e32 v255, 0x3dcccccd, v254
	v_fma_f32 v241, -v255, v218, v78
	v_fmac_f32_e32 v254, 0x3dcccccd, v241
	v_fmac_f32_e32 v255, 0x3dcccccd, v254
	v_fma_f32 v241, -v255, v218, v79
	v_fmac_f32_e32 v254, 0x3dcccccd, v241
	v_fmac_f32_e32 v255, 0x3dcccccd, v254
	v_fma_f32 v241, -v255, v218, v80
	v_fmac_f32_e32 v254, 0x3dcccccd, v241
	v_fmac_f32_e32 v255, 0x3dcccccd, v254
	v_fma_f32 v241, -v255, v218, v81
	v_fmac_f32_e32 v254, 0x3dcccccd, v241
	v_fmac_f32_e32 v255, 0x3dcccccd, v254
	v_fma_f32 v241, -v255, v218, v82
	v_fmac_f32_e32 v254, 0x3dcccccd, v241
	v_fmac_f32_e32 v255, 0x3dcccccd, v254
	v_fma_f32 v241, -v255, v218, v83
	v_fmac_f32_e32 v254, 0x3dcccccd, v241
	v_fmac_f32_e32 v255, 0x3dcccccd, v254
	v_fma_f32 v241, -v255, v218, v84
	v_fmac_f32_e32 v254, 0x3dcccccd, v241
	v_fmac_f32_e32 v255, 0x3dcccccd, v254
	v_fma_f32 v241, -v255, v218, v85
	v_fmac_f32_e32 v254, 0x3dcccccd, v241
	v_fmac_f32_e32 v255, 0x3dcccccd, v254
	v_fma_f32 v241, -v255, v218, v86
	v_fmac_f32_e32 v254, 0x3dcccccd, v241
	v_fmac_f32_e32 v255, 0x3dcccccd, v254
	v_fma_f32 v241, -v255, v218, v87
	v_fmac_f32_e32 v254, 0x3dcccccd, v241
	v_fmac_f32_e32 v255, 0x3dcccccd, v254
	v_fma_f32 v241, -v255, v218, v88
	v_fmac_f32_e32 v254, 0x3dcccccd, v241
	v_fmac_f32_e32 v255, 0x3dcccccd, v254
	v_fma_f32 v241, -v255, v218, v89
	v_fmac_f32_e32 v254, 0x3dcccccd, v241
	v_fmac_f32_e32 v255, 0x3dcccccd, v254
	v_fma_f32 v241, -v255, v218, v90
	v_fmac_f32_e32 v254, 0x3dcccccd, v241
	v_fmac_f32_e32 v255, 0x3dcccccd, v254
	v_fma_f32 v241, -v255, v218, v91
	v_fmac_f32_e32 v254, 0x3dcccccd, v241
	v_fmac_f32_e32 v255, 0x3dcccccd, v254
	v_fma_f32 v241, -v255, v218, v92
	v_fmac_f32_e32 v254, 0x3dcccccd, v241
	v_fmac_f32_e32 v255, 0x3dcccccd, v254
	v_fma_f32 v241, -v255, v218, v93
	v_fmac_f32_e32 v254, 0x3dcccccd, v241
	v_fmac_f32_e32 v255, 0x3dcccccd, v254
	v_fma_f32 v241, -v255, v218, v94
	v_fmac_f32_e32 v254, 0x3dcccccd, v241
	v_fmac_f32_e32 v255, 0x3dcccccd, v254
	v_fma_f32 v241, -v255, v218, v95
	v_fmac_f32_e32 v254, 0x3dcccccd, v241
	v_fmac_f32_e32 v255, 0x3dcccccd, v254
	v_fma_f32 v241, -v255, v218, v96
	v_fmac_f32_e32 v254, 0x3dcccccd, v241
	v_fmac_f32_e32 v255, 0x3dcccccd, v254
	v_fma_f32 v241, -v255, v218, v97
	v_fmac_f32_e32 v254, 0x3dcccccd, v241
	v_fmac_f32_e32 v255, 0x3dcccccd, v254
	v_mov_b32_e32 v228, 1.0
	v_mul_f32_e32 v229, 0xbdcccccd, v218
	v_mov_b32_e32 v230, 0x3dcccccd
	v_fma_f32 v231, v229, v230, 1.0
	v_mul_f32_e32 v244, v228, v228
	v_fmac_f32_e32 v244, v229, v230
	v_mul_f32_e32 v245, v228, v229
	v_fmac_f32_e32 v245, v229, v231
	v_mul_f32_e32 v246, v230, v228
	v_fmac_f32_e32 v246, v231, v230
	v_mul_f32_e32 v247, v230, v229
	v_fmac_f32_e32 v247, v231, v231
	v_mov_b32_e32 v228, v244
	v_mov_b32_e32 v229, v245
	v_mov_b32_e32 v230, v246
	v_mov_b32_e32 v231, v247
	v_mul_f32_e32 v244, v228, v228
	v_fmac_f32_e32 v244, v229, v230
	v_mul_f32_e32 v245, v228, v229
	v_fmac_f32_e32 v245, v229, v231
	v_mul_f32_e32 v246, v230, v228
	v_fmac_f32_e32 v246, v231, v230
	v_mul_f32_e32 v247, v230, v229
	v_fmac_f32_e32 v247, v231, v231
	v_mov_b32_e32 v228, v244
	v_mov_b32_e32 v229, v245
	v_mov_b32_e32 v230, v246
	v_mov_b32_e32 v231, v247
	v_mul_f32_e32 v244, v228, v228
	v_fmac_f32_e32 v244, v229, v230
	v_mul_f32_e32 v245, v228, v229
	v_fmac_f32_e32 v245, v229, v231
	v_mul_f32_e32 v246, v230, v228
	v_fmac_f32_e32 v246, v231, v230
	v_mul_f32_e32 v247, v230, v229
	v_fmac_f32_e32 v247, v231, v231
	v_mov_b32_e32 v228, v244
	v_mov_b32_e32 v229, v245
	v_mov_b32_e32 v230, v246
	v_mov_b32_e32 v231, v247
	v_mul_f32_e32 v244, v228, v228
	v_fmac_f32_e32 v244, v229, v230
	v_mul_f32_e32 v245, v228, v229
	v_fmac_f32_e32 v245, v229, v231
	v_mul_f32_e32 v246, v230, v228
	v_fmac_f32_e32 v246, v231, v230
	v_mul_f32_e32 v247, v230, v229
	v_fmac_f32_e32 v247, v231, v231
	v_mov_b32_e32 v228, v244
	v_mov_b32_e32 v229, v245
	v_mov_b32_e32 v230, v246
	v_mov_b32_e32 v231, v247
	v_mul_f32_e32 v244, v228, v228
	v_fmac_f32_e32 v244, v229, v230
	v_mul_f32_e32 v245, v228, v229
	v_fmac_f32_e32 v245, v229, v231
	v_mul_f32_e32 v246, v230, v228
	v_fmac_f32_e32 v246, v231, v230
	v_mul_f32_e32 v247, v230, v229
	v_fmac_f32_e32 v247, v231, v231
	v_mov_b32_e32 v228, v244
	v_mov_b32_e32 v229, v245
	v_mov_b32_e32 v230, v246
	v_mov_b32_e32 v231, v247
	v_mul_f32_e32 v232, v228, v228
	v_fmac_f32_e32 v232, v229, v230
	v_mul_f32_e32 v233, v228, v229
	v_fmac_f32_e32 v233, v229, v231
	v_mul_f32_e32 v234, v230, v228
	v_fmac_f32_e32 v234, v231, v230
	v_mul_f32_e32 v235, v230, v229
	v_fmac_f32_e32 v235, v231, v231
	ds_bpermute_b32 v248, v224, v254
	ds_bpermute_b32 v249, v224, v255
	s_waitcnt lgkmcnt(0)
	v_cndmask_b32_e64 v236, v254, v248, s[46:47]
	v_cndmask_b32_e64 v237, v255, v249, s[46:47]
	v_cndmask_b32_e64 v241, v248, v254, s[46:47]
	v_cndmask_b32_e64 v242, v249, v255, s[46:47]
	v_fma_f32 v250, v228, v236, v241
	v_fma_f32 v251, v230, v236, v242
	v_fmac_f32_e32 v250, v229, v237
	v_fmac_f32_e32 v251, v231, v237
	v_or_b32_e32 v250, 1, v250
	v_or_b32_e32 v251, 1, v251
	v_lshlrev_b32_e32 v240, 1, v223
	v_add_u32_e32 v240, 0x200, v240
	s_mov_b64 s[52:53], exec
	s_andn2_b64 exec, exec, s[46:47]
	global_store_dwordx2 v240, v[250:251], s[48:49] sc1
	s_mov_b64 exec, s[52:53]
	v_lshl_add_u32 v240, v212, 18, v240
	ds_read_b128 v[98:101], v213
	ds_read_b128 v[102:105], v213 offset:33024
	ds_read_b128 v[106:109], v213 offset:32
	ds_read_b128 v[110:113], v213 offset:33056
	s_waitcnt vmcnt(63) lgkmcnt(2)
	v_mfma_f32_32x32x16_f16 v[2:17], v[98:101], v[146:149], 0
	v_mfma_f32_32x32x16_f16 v[18:33], v[102:105], v[146:149], 0
	global_load_dwordx4 v[146:149], v214, s[36:37]
	v_fma_f32 v222, -v221, v217, v60
	v_fmac_f32_e32 v220, 0x3dcccccd, v222
	v_fmac_f32_e32 v221, 0x3dcccccd, v220
	global_store_dword v215, v221, s[30:31] offset:-4096
	global_store_dword v215, v220, s[32:33] offset:-4096
	global_store_dword v215, v221, s[34:35] offset:-4096
	ds_read_b128 v[98:101], v213 offset:64
	ds_read_b128 v[102:105], v213 offset:33088
	s_waitcnt vmcnt(63) lgkmcnt(2)
	v_mfma_f32_32x32x16_f16 v[2:17], v[106:109], v[150:153], v[2:17]
	v_mfma_f32_32x32x16_f16 v[18:33], v[110:113], v[150:153], v[18:33]
	global_load_dwordx4 v[150:153], v214, s[36:37] offset:1024
	v_fma_f32 v222, -v221, v217, v61
	v_fmac_f32_e32 v220, 0x3dcccccd, v222
	v_fmac_f32_e32 v221, 0x3dcccccd, v220
	global_store_dword v215, v221, s[30:31]
	global_store_dword v215, v220, s[32:33]
	global_store_dword v215, v221, s[34:35]
	v_add_u32_e32 v215, 0x2000, v215
	ds_read_b128 v[106:109], v213 offset:96
	ds_read_b128 v[110:113], v213 offset:33120
	s_waitcnt vmcnt(63) lgkmcnt(2)
	v_mfma_f32_32x32x16_f16 v[2:17], v[98:101], v[154:157], v[2:17]
	v_mfma_f32_32x32x16_f16 v[18:33], v[102:105], v[154:157], v[18:33]
	global_load_dwordx4 v[154:157], v214, s[36:37] offset:2048
	v_fma_f32 v222, -v221, v217, v62
	v_fmac_f32_e32 v220, 0x3dcccccd, v222
	v_fmac_f32_e32 v221, 0x3dcccccd, v220
	global_store_dword v215, v221, s[30:31] offset:-4096
	global_store_dword v215, v220, s[32:33] offset:-4096
	global_store_dword v215, v221, s[34:35] offset:-4096
	ds_read_b128 v[98:101], v213 offset:128
	ds_read_b128 v[102:105], v213 offset:33152
	s_waitcnt vmcnt(63) lgkmcnt(2)
	v_mfma_f32_32x32x16_f16 v[2:17], v[106:109], v[158:161], v[2:17]
	v_mfma_f32_32x32x16_f16 v[18:33], v[110:113], v[158:161], v[18:33]
	global_load_dwordx4 v[158:161], v214, s[36:37] offset:3072
	v_add_u32_e32 v214, 0x1000, v214
	v_fma_f32 v222, -v221, v217, v63
	v_fmac_f32_e32 v220, 0x3dcccccd, v222
	v_fmac_f32_e32 v221, 0x3dcccccd, v220
	global_store_dword v215, v221, s[30:31]
	global_store_dword v215, v220, s[32:33]
	global_store_dword v215, v221, s[34:35]
	v_add_u32_e32 v215, 0x2000, v215
	ds_read_b128 v[106:109], v213 offset:160
	ds_read_b128 v[110:113], v213 offset:33184
	s_waitcnt vmcnt(63) lgkmcnt(2)
	v_mfma_f32_32x32x16_f16 v[2:17], v[98:101], v[162:165], v[2:17]
	v_mfma_f32_32x32x16_f16 v[18:33], v[102:105], v[162:165], v[18:33]
	global_load_dwordx4 v[162:165], v214, s[36:37]
	v_fma_f32 v222, -v221, v217, v64
	v_fmac_f32_e32 v220, 0x3dcccccd, v222
	v_fmac_f32_e32 v221, 0x3dcccccd, v220
	global_store_dword v215, v221, s[30:31] offset:-4096
	global_store_dword v215, v220, s[32:33] offset:-4096
	global_store_dword v215, v221, s[34:35] offset:-4096
	ds_read_b128 v[98:101], v213 offset:192
	ds_read_b128 v[102:105], v213 offset:33216
	s_waitcnt vmcnt(63) lgkmcnt(2)
	v_mfma_f32_32x32x16_f16 v[2:17], v[106:109], v[166:169], v[2:17]
	v_mfma_f32_32x32x16_f16 v[18:33], v[110:113], v[166:169], v[18:33]
	global_load_dwordx4 v[166:169], v214, s[36:37] offset:1024
	v_fma_f32 v222, -v221, v217, v65
	v_fmac_f32_e32 v220, 0x3dcccccd, v222
	v_fmac_f32_e32 v221, 0x3dcccccd, v220
	global_store_dword v215, v221, s[30:31]
	global_store_dword v215, v220, s[32:33]
	global_store_dword v215, v221, s[34:35]
	v_add_u32_e32 v215, 0x2000, v215
	ds_read_b128 v[106:109], v213 offset:224
	ds_read_b128 v[110:113], v213 offset:33248
	s_waitcnt vmcnt(63) lgkmcnt(2)
	v_mfma_f32_32x32x16_f16 v[2:17], v[98:101], v[170:173], v[2:17]
	v_mfma_f32_32x32x16_f16 v[18:33], v[102:105], v[170:173], v[18:33]
	global_load_dwordx4 v[170:173], v214, s[36:37] offset:2048
	ds_read_b128 v[98:101], v213 offset:256
	ds_read_b128 v[102:105], v213 offset:33280
	s_waitcnt vmcnt(61) lgkmcnt(2)
	v_mfma_f32_32x32x16_f16 v[2:17], v[106:109], v[174:177], v[2:17]
	v_mfma_f32_32x32x16_f16 v[18:33], v[110:113], v[174:177], v[18:33]
	global_load_dwordx4 v[174:177], v214, s[36:37] offset:3072
	v_add_u32_e32 v214, 0x1000, v214
	s_mov_b64 s[40:41], s[38:39]
	global_load_dwordx2 v[114:115], v240, s[40:41] sc1
	s_add_u32 s40, s40, 0x2000
	s_addc_u32 s41, s41, 0
	global_load_dwordx2 v[116:117], v240, s[40:41] sc1
	s_add_u32 s40, s40, 0x2000
	s_addc_u32 s41, s41, 0
	global_load_dwordx2 v[118:119], v240, s[40:41] sc1
	s_add_u32 s40, s40, 0x2000
	s_addc_u32 s41, s41, 0
	global_load_dwordx2 v[120:121], v240, s[40:41] sc1
	s_add_u32 s40, s40, 0x2000
	s_addc_u32 s41, s41, 0
	global_load_dwordx2 v[122:123], v240, s[40:41] sc1
	s_add_u32 s40, s40, 0x2000
	s_addc_u32 s41, s41, 0
	global_load_dwordx2 v[124:125], v240, s[40:41] sc1
	s_add_u32 s40, s40, 0x2000
	s_addc_u32 s41, s41, 0
	global_load_dwordx2 v[126:127], v240, s[40:41] sc1
	s_add_u32 s40, s40, 0x2000
	s_addc_u32 s41, s41, 0
	global_load_dwordx2 v[128:129], v240, s[40:41] sc1
	s_add_u32 s40, s40, 0x2000
	s_addc_u32 s41, s41, 0
	global_load_dwordx2 v[130:131], v240, s[40:41] sc1
	s_add_u32 s40, s40, 0x2000
	s_addc_u32 s41, s41, 0
	global_load_dwordx2 v[132:133], v240, s[40:41] sc1
	s_add_u32 s40, s40, 0x2000
	s_addc_u32 s41, s41, 0
	global_load_dwordx2 v[134:135], v240, s[40:41] sc1
	s_add_u32 s40, s40, 0x2000
	s_addc_u32 s41, s41, 0
	global_load_dwordx2 v[136:137], v240, s[40:41] sc1
	s_add_u32 s40, s40, 0x2000
	s_addc_u32 s41, s41, 0
	global_load_dwordx2 v[138:139], v240, s[40:41] sc1
	s_add_u32 s40, s40, 0x2000
	s_addc_u32 s41, s41, 0
	global_load_dwordx2 v[140:141], v240, s[40:41] sc1
	s_add_u32 s40, s40, 0x2000
	s_addc_u32 s41, s41, 0
	global_load_dwordx2 v[142:143], v240, s[40:41] sc1
	s_add_u32 s40, s40, 0x2000
	s_addc_u32 s41, s41, 0
	global_load_dwordx2 v[144:145], v240, s[40:41] sc1
	ds_read_b128 v[106:109], v213 offset:288
	ds_read_b128 v[110:113], v213 offset:33312
	s_waitcnt vmcnt(63) lgkmcnt(2)
	v_mfma_f32_32x32x16_f16 v[2:17], v[98:101], v[178:181], v[2:17]
	v_mfma_f32_32x32x16_f16 v[18:33], v[102:105], v[178:181], v[18:33]
	global_load_dwordx4 v[178:181], v214, s[36:37]
	ds_read_b128 v[98:101], v213 offset:320
	ds_read_b128 v[102:105], v213 offset:33344
	s_waitcnt vmcnt(63) lgkmcnt(2)
	v_mfma_f32_32x32x16_f16 v[2:17], v[106:109], v[182:185], v[2:17]
	v_mfma_f32_32x32x16_f16 v[18:33], v[110:113], v[182:185], v[18:33]
	global_load_dwordx4 v[182:185], v214, s[36:37] offset:1024
	ds_read_b128 v[106:109], v213 offset:352
	ds_read_b128 v[110:113], v213 offset:33376
	s_waitcnt vmcnt(63) lgkmcnt(2)
	v_mfma_f32_32x32x16_f16 v[2:17], v[98:101], v[186:189], v[2:17]
	v_mfma_f32_32x32x16_f16 v[18:33], v[102:105], v[186:189], v[18:33]
	global_load_dwordx4 v[186:189], v214, s[36:37] offset:2048
	ds_read_b128 v[98:101], v213 offset:384
	ds_read_b128 v[102:105], v213 offset:33408
	s_waitcnt vmcnt(63) lgkmcnt(2)
	v_mfma_f32_32x32x16_f16 v[2:17], v[106:109], v[190:193], v[2:17]
	v_mfma_f32_32x32x16_f16 v[18:33], v[110:113], v[190:193], v[18:33]
	global_load_dwordx4 v[190:193], v214, s[36:37] offset:3072
	v_add_u32_e32 v214, 0x1000, v214
	ds_read_b128 v[106:109], v213 offset:416
	ds_read_b128 v[110:113], v213 offset:33440
	s_waitcnt vmcnt(62) lgkmcnt(2)
	v_mfma_f32_32x32x16_f16 v[2:17], v[98:101], v[194:197], v[2:17]
	v_mfma_f32_32x32x16_f16 v[18:33], v[102:105], v[194:197], v[18:33]
	global_load_dwordx4 v[194:197], v214, s[36:37]
	ds_read_b128 v[98:101], v213 offset:448
	ds_read_b128 v[102:105], v213 offset:33472
	s_waitcnt vmcnt(59) lgkmcnt(2)
	v_mfma_f32_32x32x16_f16 v[2:17], v[106:109], v[198:201], v[2:17]
	v_mfma_f32_32x32x16_f16 v[18:33], v[110:113], v[198:201], v[18:33]
	global_load_dwordx4 v[198:201], v214, s[36:37] offset:1024
	ds_read_b128 v[106:109], v213 offset:480
	ds_read_b128 v[110:113], v213 offset:33504
	s_waitcnt vmcnt(56) lgkmcnt(2)
	v_mfma_f32_32x32x16_f16 v[2:17], v[98:101], v[202:205], v[2:17]
	v_mfma_f32_32x32x16_f16 v[18:33], v[102:105], v[202:205], v[18:33]
	global_load_dwordx4 v[202:205], v214, s[36:37] offset:2048
	ds_read_b128 v[98:101], v213 offset:512
	ds_read_b128 v[102:105], v213 offset:33536
	s_waitcnt vmcnt(53) lgkmcnt(2)
	v_mfma_f32_32x32x16_f16 v[2:17], v[106:109], v[206:209], v[2:17]
	v_mfma_f32_32x32x16_f16 v[18:33], v[110:113], v[206:209], v[18:33]
	global_load_dwordx4 v[206:209], v214, s[36:37] offset:3072
	v_add_u32_e32 v214, 0x1000, v214
	ds_read_b128 v[106:109], v213 offset:544
	ds_read_b128 v[110:113], v213 offset:33568
	s_waitcnt vmcnt(49) lgkmcnt(2)
	v_mfma_f32_32x32x16_f16 v[2:17], v[98:101], v[146:149], v[2:17]
	v_mfma_f32_32x32x16_f16 v[18:33], v[102:105], v[146:149], v[18:33]
	global_load_dwordx4 v[146:149], v214, s[36:37]
	ds_read_b128 v[98:101], v213 offset:576
	ds_read_b128 v[102:105], v213 offset:33600
	s_waitcnt vmcnt(46) lgkmcnt(2)
	v_mfma_f32_32x32x16_f16 v[2:17], v[106:109], v[150:153], v[2:17]
	v_mfma_f32_32x32x16_f16 v[18:33], v[110:113], v[150:153], v[18:33]
	global_load_dwordx4 v[150:153], v214, s[36:37] offset:1024
	v_mov_b32_e32 v238, 0
	v_mov_b32_e32 v239, 0
	s_waitcnt vmcnt(10)
	s_branch .Llb_chk_2_0

.Llb_chk_2_0:
	v_mov_b32_e32 v243, 0
	v_and_b32_e32 v244, v114, v115
	v_alignbit_b32 v243, v244, v243, 1
	v_and_b32_e32 v244, v116, v117
	v_alignbit_b32 v243, v244, v243, 1
	v_and_b32_e32 v244, v118, v119
	v_alignbit_b32 v243, v244, v243, 1
	v_and_b32_e32 v244, v120, v121
	v_alignbit_b32 v243, v244, v243, 1
	v_and_b32_e32 v244, v122, v123
	v_alignbit_b32 v243, v244, v243, 1
	v_and_b32_e32 v244, v124, v125
	v_alignbit_b32 v243, v244, v243, 1
	v_and_b32_e32 v244, v126, v127
	v_alignbit_b32 v243, v244, v243, 1
	v_and_b32_e32 v244, v128, v129
	v_alignbit_b32 v243, v244, v243, 1
	v_and_b32_e32 v244, v130, v131
	v_alignbit_b32 v243, v244, v243, 1
	v_and_b32_e32 v244, v132, v133
	v_alignbit_b32 v243, v244, v243, 1
	v_and_b32_e32 v244, v134, v135
	v_alignbit_b32 v243, v244, v243, 1
	v_and_b32_e32 v244, v136, v137
	v_alignbit_b32 v243, v244, v243, 1
	v_and_b32_e32 v244, v138, v139
	v_alignbit_b32 v243, v244, v243, 1
	v_and_b32_e32 v244, v140, v141
	v_alignbit_b32 v243, v244, v243, 1
	v_and_b32_e32 v244, v142, v143
	v_alignbit_b32 v243, v244, v243, 1
	v_and_b32_e32 v244, v144, v145
	v_alignbit_b32 v243, v244, v243, 1
	v_lshrrev_b32_e32 v243, 16, v243
	v_and_b32_e32 v243, v243, v226
	v_cmp_ne_u32_e32 vcc, v243, v226
	s_nop 1
	s_cmp_eq_u64 vcc, 0
	s_cbranch_scc0 .Llb_retry_2_0
	ds_read_b128 v[106:109], v213 offset:608
	ds_read_b128 v[110:113], v213 offset:33632
	s_waitcnt vmcnt(43) lgkmcnt(2)
	v_mfma_f32_32x32x16_f16 v[2:17], v[98:101], v[154:157], v[2:17]
	v_mfma_f32_32x32x16_f16 v[18:33], v[102:105], v[154:157], v[18:33]
	global_load_dwordx4 v[154:157], v214, s[36:37] offset:2048
	v_cmp_lt_u32_e32 vcc, 0, v225
	v_fma_f32 v241, v232, v238, v114
	v_fma_f32 v242, v234, v238, v115
	v_fmac_f32_e32 v241, v233, v239
	v_fmac_f32_e32 v242, v235, v239
	v_cndmask_b32_e32 v238, v238, v241, vcc
	v_cndmask_b32_e32 v239, v239, v242, vcc
	v_cmp_lt_u32_e32 vcc, 1, v225
	v_fma_f32 v241, v232, v238, v116
	v_fma_f32 v242, v234, v238, v117
	v_fmac_f32_e32 v241, v233, v239
	v_fmac_f32_e32 v242, v235, v239
	v_cndmask_b32_e32 v238, v238, v241, vcc
	v_cndmask_b32_e32 v239, v239, v242, vcc
	v_cmp_lt_u32_e32 vcc, 2, v225
	v_fma_f32 v241, v232, v238, v118
	v_fma_f32 v242, v234, v238, v119
	v_fmac_f32_e32 v241, v233, v239
	v_fmac_f32_e32 v242, v235, v239
	v_cndmask_b32_e32 v238, v238, v241, vcc
	v_cndmask_b32_e32 v239, v239, v242, vcc
	v_cmp_lt_u32_e32 vcc, 3, v225
	v_fma_f32 v241, v232, v238, v120
	v_fma_f32 v242, v234, v238, v121
	v_fmac_f32_e32 v241, v233, v239
	v_fmac_f32_e32 v242, v235, v239
	v_cndmask_b32_e32 v238, v238, v241, vcc
	v_cndmask_b32_e32 v239, v239, v242, vcc
	ds_read_b128 v[98:101], v213 offset:640
	ds_read_b128 v[102:105], v213 offset:33664
	s_waitcnt vmcnt(40) lgkmcnt(2)
	v_mfma_f32_32x32x16_f16 v[2:17], v[106:109], v[158:161], v[2:17]
	v_mfma_f32_32x32x16_f16 v[18:33], v[110:113], v[158:161], v[18:33]
	global_load_dwordx4 v[158:161], v214, s[36:37] offset:3072
	v_add_u32_e32 v214, 0x1000, v214
	v_cmp_lt_u32_e32 vcc, 4, v225
	v_fma_f32 v241, v232, v238, v122
	v_fma_f32 v242, v234, v238, v123
	v_fmac_f32_e32 v241, v233, v239
	v_fmac_f32_e32 v242, v235, v239
	v_cndmask_b32_e32 v238, v238, v241, vcc
	v_cndmask_b32_e32 v239, v239, v242, vcc
	v_cmp_lt_u32_e32 vcc, 5, v225
	v_fma_f32 v241, v232, v238, v124
	v_fma_f32 v242, v234, v238, v125
	v_fmac_f32_e32 v241, v233, v239
	v_fmac_f32_e32 v242, v235, v239
	v_cndmask_b32_e32 v238, v238, v241, vcc
	v_cndmask_b32_e32 v239, v239, v242, vcc
	v_cmp_lt_u32_e32 vcc, 6, v225
	v_fma_f32 v241, v232, v238, v126
	v_fma_f32 v242, v234, v238, v127
	v_fmac_f32_e32 v241, v233, v239
	v_fmac_f32_e32 v242, v235, v239
	v_cndmask_b32_e32 v238, v238, v241, vcc
	v_cndmask_b32_e32 v239, v239, v242, vcc
	v_cmp_lt_u32_e32 vcc, 7, v225
	v_fma_f32 v241, v232, v238, v128
	v_fma_f32 v242, v234, v238, v129
	v_fmac_f32_e32 v241, v233, v239
	v_fmac_f32_e32 v242, v235, v239
	v_cndmask_b32_e32 v238, v238, v241, vcc
	v_cndmask_b32_e32 v239, v239, v242, vcc
	ds_read_b128 v[106:109], v213 offset:672
	ds_read_b128 v[110:113], v213 offset:33696
	s_waitcnt vmcnt(37) lgkmcnt(2)
	v_mfma_f32_32x32x16_f16 v[2:17], v[98:101], v[162:165], v[2:17]
	v_mfma_f32_32x32x16_f16 v[18:33], v[102:105], v[162:165], v[18:33]
	global_load_dwordx4 v[162:165], v214, s[36:37]
	v_cmp_lt_u32_e32 vcc, 8, v225
	v_fma_f32 v241, v232, v238, v130
	v_fma_f32 v242, v234, v238, v131
	v_fmac_f32_e32 v241, v233, v239
	v_fmac_f32_e32 v242, v235, v239
	v_cndmask_b32_e32 v238, v238, v241, vcc
	v_cndmask_b32_e32 v239, v239, v242, vcc
	v_cmp_lt_u32_e32 vcc, 9, v225
	v_fma_f32 v241, v232, v238, v132
	v_fma_f32 v242, v234, v238, v133
	v_fmac_f32_e32 v241, v233, v239
	v_fmac_f32_e32 v242, v235, v239
	v_cndmask_b32_e32 v238, v238, v241, vcc
	v_cndmask_b32_e32 v239, v239, v242, vcc
	v_cmp_lt_u32_e32 vcc, 10, v225
	v_fma_f32 v241, v232, v238, v134
	v_fma_f32 v242, v234, v238, v135
	v_fmac_f32_e32 v241, v233, v239
	v_fmac_f32_e32 v242, v235, v239
	v_cndmask_b32_e32 v238, v238, v241, vcc
	v_cndmask_b32_e32 v239, v239, v242, vcc
	v_cmp_lt_u32_e32 vcc, 11, v225
	v_fma_f32 v241, v232, v238, v136
	v_fma_f32 v242, v234, v238, v137
	v_fmac_f32_e32 v241, v233, v239
	v_fmac_f32_e32 v242, v235, v239
	v_cndmask_b32_e32 v238, v238, v241, vcc
	v_cndmask_b32_e32 v239, v239, v242, vcc
	ds_read_b128 v[98:101], v213 offset:704
	ds_read_b128 v[102:105], v213 offset:33728
	s_waitcnt vmcnt(34) lgkmcnt(2)
	v_mfma_f32_32x32x16_f16 v[2:17], v[106:109], v[166:169], v[2:17]
	v_mfma_f32_32x32x16_f16 v[18:33], v[110:113], v[166:169], v[18:33]
	global_load_dwordx4 v[166:169], v214, s[36:37] offset:1024
	v_cmp_lt_u32_e32 vcc, 12, v225
	v_fma_f32 v241, v232, v238, v138
	v_fma_f32 v242, v234, v238, v139
	v_fmac_f32_e32 v241, v233, v239
	v_fmac_f32_e32 v242, v235, v239
	v_cndmask_b32_e32 v238, v238, v241, vcc
	v_cndmask_b32_e32 v239, v239, v242, vcc
	v_cmp_lt_u32_e32 vcc, 13, v225
	v_fma_f32 v241, v232, v238, v140
	v_fma_f32 v242, v234, v238, v141
	v_fmac_f32_e32 v241, v233, v239
	v_fmac_f32_e32 v242, v235, v239
	v_cndmask_b32_e32 v238, v238, v241, vcc
	v_cndmask_b32_e32 v239, v239, v242, vcc
	v_cmp_lt_u32_e32 vcc, 14, v225
	v_fma_f32 v241, v232, v238, v142
	v_fma_f32 v242, v234, v238, v143
	v_fmac_f32_e32 v241, v233, v239
	v_fmac_f32_e32 v242, v235, v239
	v_cndmask_b32_e32 v238, v238, v241, vcc
	v_cndmask_b32_e32 v239, v239, v242, vcc
	v_cmp_lt_u32_e32 vcc, 15, v225
	v_fma_f32 v241, v232, v238, v144
	v_fma_f32 v242, v234, v238, v145
	v_fmac_f32_e32 v241, v233, v239
	v_fmac_f32_e32 v242, v235, v239
	v_cndmask_b32_e32 v238, v238, v241, vcc
	v_cndmask_b32_e32 v239, v239, v242, vcc
	s_mov_b64 s[40:41], s[50:51]
	global_load_dwordx2 v[114:115], v240, s[40:41] sc1
	s_add_u32 s40, s40, 0x2000
	s_addc_u32 s41, s41, 0
	global_load_dwordx2 v[116:117], v240, s[40:41] sc1
	s_add_u32 s40, s40, 0x2000
	s_addc_u32 s41, s41, 0
	global_load_dwordx2 v[118:119], v240, s[40:41] sc1
	s_add_u32 s40, s40, 0x2000
	s_addc_u32 s41, s41, 0
	global_load_dwordx2 v[120:121], v240, s[40:41] sc1
	s_add_u32 s40, s40, 0x2000
	s_addc_u32 s41, s41, 0
	global_load_dwordx2 v[122:123], v240, s[40:41] sc1
	s_add_u32 s40, s40, 0x2000
	s_addc_u32 s41, s41, 0
	global_load_dwordx2 v[124:125], v240, s[40:41] sc1
	s_add_u32 s40, s40, 0x2000
	s_addc_u32 s41, s41, 0
	global_load_dwordx2 v[126:127], v240, s[40:41] sc1
	s_add_u32 s40, s40, 0x2000
	s_addc_u32 s41, s41, 0
	global_load_dwordx2 v[128:129], v240, s[40:41] sc1
	s_add_u32 s40, s40, 0x2000
	s_addc_u32 s41, s41, 0
	global_load_dwordx2 v[130:131], v240, s[40:41] sc1
	s_add_u32 s40, s40, 0x2000
	s_addc_u32 s41, s41, 0
	global_load_dwordx2 v[132:133], v240, s[40:41] sc1
	s_add_u32 s40, s40, 0x2000
	s_addc_u32 s41, s41, 0
	global_load_dwordx2 v[134:135], v240, s[40:41] sc1
	s_add_u32 s40, s40, 0x2000
	s_addc_u32 s41, s41, 0
	global_load_dwordx2 v[136:137], v240, s[40:41] sc1
	s_add_u32 s40, s40, 0x2000
	s_addc_u32 s41, s41, 0
	global_load_dwordx2 v[138:139], v240, s[40:41] sc1
	s_add_u32 s40, s40, 0x2000
	s_addc_u32 s41, s41, 0
	global_load_dwordx2 v[140:141], v240, s[40:41] sc1
	s_add_u32 s40, s40, 0x2000
	s_addc_u32 s41, s41, 0
	global_load_dwordx2 v[142:143], v240, s[40:41] sc1
	s_add_u32 s40, s40, 0x2000
	s_addc_u32 s41, s41, 0
	global_load_dwordx2 v[144:145], v240, s[40:41] sc1
	ds_read_b128 v[106:109], v213 offset:736
	ds_read_b128 v[110:113], v213 offset:33760
	s_waitcnt vmcnt(47) lgkmcnt(2)
	v_mfma_f32_32x32x16_f16 v[2:17], v[98:101], v[170:173], v[2:17]
	v_mfma_f32_32x32x16_f16 v[18:33], v[102:105], v[170:173], v[18:33]
	global_load_dwordx4 v[170:173], v214, s[36:37] offset:2048
	ds_read_b128 v[98:101], v213 offset:768
	ds_read_b128 v[102:105], v213 offset:33792
	s_waitcnt vmcnt(47) lgkmcnt(2)
	v_mfma_f32_32x32x16_f16 v[2:17], v[106:109], v[174:177], v[2:17]
	v_mfma_f32_32x32x16_f16 v[18:33], v[110:113], v[174:177], v[18:33]
	global_load_dwordx4 v[174:177], v214, s[36:37] offset:3072
	v_add_u32_e32 v214, 0x1000, v214
	ds_read_b128 v[106:109], v213 offset:800
	ds_read_b128 v[110:113], v213 offset:33824
	s_waitcnt vmcnt(31) lgkmcnt(2)
	v_mfma_f32_32x32x16_f16 v[2:17], v[98:101], v[178:181], v[2:17]
	v_mfma_f32_32x32x16_f16 v[18:33], v[102:105], v[178:181], v[18:33]
	global_load_dwordx4 v[178:181], v214, s[36:37]
	ds_read_b128 v[98:101], v213 offset:832
	ds_read_b128 v[102:105], v213 offset:33856
	s_waitcnt vmcnt(31) lgkmcnt(2)
	v_mfma_f32_32x32x16_f16 v[2:17], v[106:109], v[182:185], v[2:17]
	v_mfma_f32_32x32x16_f16 v[18:33], v[110:113], v[182:185], v[18:33]
	global_load_dwordx4 v[182:185], v214, s[36:37] offset:1024
	ds_read_b128 v[106:109], v213 offset:864
	ds_read_b128 v[110:113], v213 offset:33888
	s_waitcnt vmcnt(31) lgkmcnt(2)
	v_mfma_f32_32x32x16_f16 v[2:17], v[98:101], v[186:189], v[2:17]
	v_mfma_f32_32x32x16_f16 v[18:33], v[102:105], v[186:189], v[18:33]
	global_load_dwordx4 v[186:189], v214, s[36:37] offset:2048
	ds_read_b128 v[98:101], v213 offset:896
	ds_read_b128 v[102:105], v213 offset:33920
	s_waitcnt vmcnt(31) lgkmcnt(2)
	v_mfma_f32_32x32x16_f16 v[2:17], v[106:109], v[190:193], v[2:17]
	v_mfma_f32_32x32x16_f16 v[18:33], v[110:113], v[190:193], v[18:33]
	global_load_dwordx4 v[190:193], v214, s[36:37] offset:3072
	v_add_u32_e32 v214, 0x1000, v214
	ds_read_b128 v[106:109], v213 offset:928
	ds_read_b128 v[110:113], v213 offset:33952
	s_waitcnt vmcnt(31) lgkmcnt(2)
	v_mfma_f32_32x32x16_f16 v[2:17], v[98:101], v[194:197], v[2:17]
	v_mfma_f32_32x32x16_f16 v[18:33], v[102:105], v[194:197], v[18:33]
	global_load_dwordx4 v[194:197], v214, s[36:37]
	ds_read_b128 v[98:101], v213 offset:960
	ds_read_b128 v[102:105], v213 offset:33984
	s_waitcnt vmcnt(31) lgkmcnt(2)
	v_mfma_f32_32x32x16_f16 v[2:17], v[106:109], v[198:201], v[2:17]
	v_mfma_f32_32x32x16_f16 v[18:33], v[110:113], v[198:201], v[18:33]
	global_load_dwordx4 v[198:201], v214, s[36:37] offset:1024
	ds_read_b128 v[106:109], v213 offset:992
	ds_read_b128 v[110:113], v213 offset:34016
	s_waitcnt vmcnt(31) lgkmcnt(2)
	v_mfma_f32_32x32x16_f16 v[2:17], v[98:101], v[202:205], v[2:17]
	v_mfma_f32_32x32x16_f16 v[18:33], v[102:105], v[202:205], v[18:33]
	global_load_dwordx4 v[202:205], v214, s[36:37] offset:2048
	ds_read_b128 v[98:101], v213 offset:1024
	ds_read_b128 v[102:105], v213 offset:34048
	s_waitcnt vmcnt(31) lgkmcnt(2)
	v_mfma_f32_32x32x16_f16 v[2:17], v[106:109], v[206:209], v[2:17]
	v_mfma_f32_32x32x16_f16 v[18:33], v[110:113], v[206:209], v[18:33]
	global_load_dwordx4 v[206:209], v214, s[36:37] offset:3072
	v_add_u32_e32 v214, 0x1000, v214
	s_waitcnt vmcnt(10)
	s_branch .Llb_chk_2_1

.Llb_chk_2_1:
	v_mov_b32_e32 v243, 0
	v_and_b32_e32 v244, v114, v115
	v_alignbit_b32 v243, v244, v243, 1
	v_and_b32_e32 v244, v116, v117
	v_alignbit_b32 v243, v244, v243, 1
	v_and_b32_e32 v244, v118, v119
	v_alignbit_b32 v243, v244, v243, 1
	v_and_b32_e32 v244, v120, v121
	v_alignbit_b32 v243, v244, v243, 1
	v_and_b32_e32 v244, v122, v123
	v_alignbit_b32 v243, v244, v243, 1
	v_and_b32_e32 v244, v124, v125
	v_alignbit_b32 v243, v244, v243, 1
	v_and_b32_e32 v244, v126, v127
	v_alignbit_b32 v243, v244, v243, 1
	v_and_b32_e32 v244, v128, v129
	v_alignbit_b32 v243, v244, v243, 1
	v_and_b32_e32 v244, v130, v131
	v_alignbit_b32 v243, v244, v243, 1
	v_and_b32_e32 v244, v132, v133
	v_alignbit_b32 v243, v244, v243, 1
	v_and_b32_e32 v244, v134, v135
	v_alignbit_b32 v243, v244, v243, 1
	v_and_b32_e32 v244, v136, v137
	v_alignbit_b32 v243, v244, v243, 1
	v_and_b32_e32 v244, v138, v139
	v_alignbit_b32 v243, v244, v243, 1
	v_and_b32_e32 v244, v140, v141
	v_alignbit_b32 v243, v244, v243, 1
	v_and_b32_e32 v244, v142, v143
	v_alignbit_b32 v243, v244, v243, 1
	v_and_b32_e32 v244, v144, v145
	v_alignbit_b32 v243, v244, v243, 1
	v_lshrrev_b32_e32 v243, 16, v243
	v_and_b32_e32 v243, v243, v227
	v_cmp_ne_u32_e32 vcc, v243, v227
	s_nop 1
	s_cmp_eq_u64 vcc, 0
	s_cbranch_scc0 .Llb_retry_2_1
	ds_read_b128 v[106:109], v213 offset:1056
	ds_read_b128 v[110:113], v213 offset:34080
	s_waitcnt vmcnt(31) lgkmcnt(2)
	v_mfma_f32_32x32x16_f16 v[2:17], v[98:101], v[146:149], v[2:17]
	v_mfma_f32_32x32x16_f16 v[18:33], v[102:105], v[146:149], v[18:33]
	global_load_dwordx4 v[146:149], v214, s[36:37]
	v_cmp_lt_u32_e32 vcc, 16, v225
	v_fma_f32 v241, v232, v238, v114
	v_fma_f32 v242, v234, v238, v115
	v_fmac_f32_e32 v241, v233, v239
	v_fmac_f32_e32 v242, v235, v239
	v_cndmask_b32_e32 v238, v238, v241, vcc
	v_cndmask_b32_e32 v239, v239, v242, vcc
	v_cmp_lt_u32_e32 vcc, 17, v225
	v_fma_f32 v241, v232, v238, v116
	v_fma_f32 v242, v234, v238, v117
	v_fmac_f32_e32 v241, v233, v239
	v_fmac_f32_e32 v242, v235, v239
	v_cndmask_b32_e32 v238, v238, v241, vcc
	v_cndmask_b32_e32 v239, v239, v242, vcc
	v_cmp_lt_u32_e32 vcc, 18, v225
	v_fma_f32 v241, v232, v238, v118
	v_fma_f32 v242, v234, v238, v119
	v_fmac_f32_e32 v241, v233, v239
	v_fmac_f32_e32 v242, v235, v239
	v_cndmask_b32_e32 v238, v238, v241, vcc
	v_cndmask_b32_e32 v239, v239, v242, vcc
	v_cmp_lt_u32_e32 vcc, 19, v225
	v_fma_f32 v241, v232, v238, v120
	v_fma_f32 v242, v234, v238, v121
	v_fmac_f32_e32 v241, v233, v239
	v_fmac_f32_e32 v242, v235, v239
	v_cndmask_b32_e32 v238, v238, v241, vcc
	v_cndmask_b32_e32 v239, v239, v242, vcc
	ds_read_b128 v[98:101], v213 offset:1088
	ds_read_b128 v[102:105], v213 offset:34112
	s_waitcnt vmcnt(31) lgkmcnt(2)
	v_mfma_f32_32x32x16_f16 v[2:17], v[106:109], v[150:153], v[2:17]
	v_mfma_f32_32x32x16_f16 v[18:33], v[110:113], v[150:153], v[18:33]
	global_load_dwordx4 v[150:153], v214, s[36:37] offset:1024
	v_cmp_lt_u32_e32 vcc, 20, v225
	v_fma_f32 v241, v232, v238, v122
	v_fma_f32 v242, v234, v238, v123
	v_fmac_f32_e32 v241, v233, v239
	v_fmac_f32_e32 v242, v235, v239
	v_cndmask_b32_e32 v238, v238, v241, vcc
	v_cndmask_b32_e32 v239, v239, v242, vcc
	v_cmp_lt_u32_e32 vcc, 21, v225
	v_fma_f32 v241, v232, v238, v124
	v_fma_f32 v242, v234, v238, v125
	v_fmac_f32_e32 v241, v233, v239
	v_fmac_f32_e32 v242, v235, v239
	v_cndmask_b32_e32 v238, v238, v241, vcc
	v_cndmask_b32_e32 v239, v239, v242, vcc
	v_cmp_lt_u32_e32 vcc, 22, v225
	v_fma_f32 v241, v232, v238, v126
	v_fma_f32 v242, v234, v238, v127
	v_fmac_f32_e32 v241, v233, v239
	v_fmac_f32_e32 v242, v235, v239
	v_cndmask_b32_e32 v238, v238, v241, vcc
	v_cndmask_b32_e32 v239, v239, v242, vcc
	v_cmp_lt_u32_e32 vcc, 23, v225
	v_fma_f32 v241, v232, v238, v128
	v_fma_f32 v242, v234, v238, v129
	v_fmac_f32_e32 v241, v233, v239
	v_fmac_f32_e32 v242, v235, v239
	v_cndmask_b32_e32 v238, v238, v241, vcc
	v_cndmask_b32_e32 v239, v239, v242, vcc
	ds_read_b128 v[106:109], v213 offset:1120
	ds_read_b128 v[110:113], v213 offset:34144
	s_waitcnt vmcnt(31) lgkmcnt(2)
	v_mfma_f32_32x32x16_f16 v[2:17], v[98:101], v[154:157], v[2:17]
	v_mfma_f32_32x32x16_f16 v[18:33], v[102:105], v[154:157], v[18:33]
	global_load_dwordx4 v[154:157], v214, s[36:37] offset:2048
	v_cmp_lt_u32_e32 vcc, 24, v225
	v_fma_f32 v241, v232, v238, v130
	v_fma_f32 v242, v234, v238, v131
	v_fmac_f32_e32 v241, v233, v239
	v_fmac_f32_e32 v242, v235, v239
	v_cndmask_b32_e32 v238, v238, v241, vcc
	v_cndmask_b32_e32 v239, v239, v242, vcc
	v_cmp_lt_u32_e32 vcc, 25, v225
	v_fma_f32 v241, v232, v238, v132
	v_fma_f32 v242, v234, v238, v133
	v_fmac_f32_e32 v241, v233, v239
	v_fmac_f32_e32 v242, v235, v239
	v_cndmask_b32_e32 v238, v238, v241, vcc
	v_cndmask_b32_e32 v239, v239, v242, vcc
	v_cmp_lt_u32_e32 vcc, 26, v225
	v_fma_f32 v241, v232, v238, v134
	v_fma_f32 v242, v234, v238, v135
	v_fmac_f32_e32 v241, v233, v239
	v_fmac_f32_e32 v242, v235, v239
	v_cndmask_b32_e32 v238, v238, v241, vcc
	v_cndmask_b32_e32 v239, v239, v242, vcc
	v_cmp_lt_u32_e32 vcc, 27, v225
	v_fma_f32 v241, v232, v238, v136
	v_fma_f32 v242, v234, v238, v137
	v_fmac_f32_e32 v241, v233, v239
	v_fmac_f32_e32 v242, v235, v239
	v_cndmask_b32_e32 v238, v238, v241, vcc
	v_cndmask_b32_e32 v239, v239, v242, vcc
	ds_read_b128 v[98:101], v213 offset:1152
	ds_read_b128 v[102:105], v213 offset:34176
	s_waitcnt vmcnt(31) lgkmcnt(2)
	v_mfma_f32_32x32x16_f16 v[2:17], v[106:109], v[158:161], v[2:17]
	v_mfma_f32_32x32x16_f16 v[18:33], v[110:113], v[158:161], v[18:33]
	global_load_dwordx4 v[158:161], v214, s[36:37] offset:3072
	v_add_u32_e32 v214, 0x1000, v214
	v_cmp_lt_u32_e32 vcc, 28, v225
	v_fma_f32 v241, v232, v238, v138
	v_fma_f32 v242, v234, v238, v139
	v_fmac_f32_e32 v241, v233, v239
	v_fmac_f32_e32 v242, v235, v239
	v_cndmask_b32_e32 v238, v238, v241, vcc
	v_cndmask_b32_e32 v239, v239, v242, vcc
	v_cmp_lt_u32_e32 vcc, 29, v225
	v_fma_f32 v241, v232, v238, v140
	v_fma_f32 v242, v234, v238, v141
	v_fmac_f32_e32 v241, v233, v239
	v_fmac_f32_e32 v242, v235, v239
	v_cndmask_b32_e32 v238, v238, v241, vcc
	v_cndmask_b32_e32 v239, v239, v242, vcc
	v_cmp_lt_u32_e32 vcc, 30, v225
	v_fma_f32 v241, v232, v238, v142
	v_fma_f32 v242, v234, v238, v143
	v_fmac_f32_e32 v241, v233, v239
	v_fmac_f32_e32 v242, v235, v239
	v_cndmask_b32_e32 v238, v238, v241, vcc
	v_cndmask_b32_e32 v239, v239, v242, vcc
	v_cmp_lt_u32_e32 vcc, 31, v225
	v_fma_f32 v241, v232, v238, v144
	v_fma_f32 v242, v234, v238, v145
	v_fmac_f32_e32 v241, v233, v239
	v_fmac_f32_e32 v242, v235, v239
	v_cndmask_b32_e32 v238, v238, v241, vcc
	v_cndmask_b32_e32 v239, v239, v242, vcc
	ds_read_b128 v[106:109], v213 offset:1184
	ds_read_b128 v[110:113], v213 offset:34208
	s_waitcnt vmcnt(31) lgkmcnt(2)
	v_mfma_f32_32x32x16_f16 v[2:17], v[98:101], v[162:165], v[2:17]
	v_mfma_f32_32x32x16_f16 v[18:33], v[102:105], v[162:165], v[18:33]
	global_load_dwordx4 v[162:165], v214, s[36:37]
	ds_bpermute_b32 v247, v224, v238
	ds_bpermute_b32 v248, v224, v239
	s_waitcnt lgkmcnt(0)
	v_cndmask_b32_e64 v249, v238, v247, s[46:47]
	v_cndmask_b32_e64 v250, v239, v248, s[46:47]
	v_cndmask_b32_e64 v251, v247, v238, s[46:47]
	v_cndmask_b32_e64 v252, v248, v239, s[46:47]
	s_sub_i32 s44, s18, 32
	s_cmp_gt_i32 s44, 0
	s_cbranch_scc0 .Llb_np_2

.Llb_np_2:
	v_add_f32_e32 v238, v249, v251
	v_add_f32_e32 v239, v250, v252
	ds_read_b128 v[98:101], v213 offset:1216
	ds_read_b128 v[102:105], v213 offset:34240
	s_waitcnt vmcnt(31) lgkmcnt(2)
	v_mfma_f32_32x32x16_f16 v[2:17], v[106:109], v[166:169], v[2:17]
	v_mfma_f32_32x32x16_f16 v[18:33], v[110:113], v[166:169], v[18:33]
	global_load_dwordx4 v[166:169], v214, s[36:37] offset:1024
	v_fma_f32 v245, v228, v238, v236
	v_fma_f32 v246, v230, v238, v237
	v_fmac_f32_e32 v245, v229, v239
	v_fmac_f32_e32 v246, v231, v239
	v_cndmask_b32_e64 v220, v238, v245, s[46:47]
	v_cndmask_b32_e64 v221, v239, v246, s[46:47]
	v_lshl_add_u32 v215, v212, 17, v223
	v_add_u32_e32 v215, 0x1100, v215
	ds_read_b128 v[106:109], v213 offset:1248
	ds_read_b128 v[110:113], v213 offset:34272
	s_waitcnt vmcnt(15) lgkmcnt(2)
	v_mfma_f32_32x32x16_f16 v[2:17], v[98:101], v[170:173], v[2:17]
	v_mfma_f32_32x32x16_f16 v[18:33], v[102:105], v[170:173], v[18:33]
	global_load_dwordx4 v[170:173], v214, s[36:37] offset:2048
	v_fma_f32 v222, -v221, v218, v66
	v_fmac_f32_e32 v220, 0x3dcccccd, v222
	v_fmac_f32_e32 v221, 0x3dcccccd, v220
	global_store_dword v215, v221, s[30:31] offset:-4096
	global_store_dword v215, v220, s[32:33] offset:-4096
	global_store_dword v215, v221, s[34:35] offset:-4096
	ds_read_b128 v[98:101], v213 offset:1280
	ds_read_b128 v[102:105], v213 offset:34304
	s_waitcnt vmcnt(18) lgkmcnt(2)
	v_mfma_f32_32x32x16_f16 v[2:17], v[106:109], v[174:177], v[2:17]
	v_mfma_f32_32x32x16_f16 v[18:33], v[110:113], v[174:177], v[18:33]
	global_load_dwordx4 v[174:177], v214, s[36:37] offset:3072
	v_add_u32_e32 v214, 0x1000, v214
	v_fma_f32 v222, -v221, v218, v67
	v_fmac_f32_e32 v220, 0x3dcccccd, v222
	v_fmac_f32_e32 v221, 0x3dcccccd, v220
	global_store_dword v215, v221, s[30:31]
	global_store_dword v215, v220, s[32:33]
	global_store_dword v215, v221, s[34:35]
	v_add_u32_e32 v215, 0x2000, v215
	ds_read_b128 v[106:109], v213 offset:1312
	ds_read_b128 v[110:113], v213 offset:34336
	s_waitcnt vmcnt(21) lgkmcnt(2)
	v_mfma_f32_32x32x16_f16 v[2:17], v[98:101], v[178:181], v[2:17]
	v_mfma_f32_32x32x16_f16 v[18:33], v[102:105], v[178:181], v[18:33]
	global_load_dwordx4 v[178:181], v214, s[36:37]
	v_fma_f32 v222, -v221, v218, v68
	v_fmac_f32_e32 v220, 0x3dcccccd, v222
	v_fmac_f32_e32 v221, 0x3dcccccd, v220
	global_store_dword v215, v221, s[30:31] offset:-4096
	global_store_dword v215, v220, s[32:33] offset:-4096
	global_store_dword v215, v221, s[34:35] offset:-4096
	ds_read_b128 v[98:101], v213 offset:1344
	ds_read_b128 v[102:105], v213 offset:34368
	s_waitcnt vmcnt(24) lgkmcnt(2)
	v_mfma_f32_32x32x16_f16 v[2:17], v[106:109], v[182:185], v[2:17]
	v_mfma_f32_32x32x16_f16 v[18:33], v[110:113], v[182:185], v[18:33]
	global_load_dwordx4 v[182:185], v214, s[36:37] offset:1024
	v_fma_f32 v222, -v221, v218, v69
	v_fmac_f32_e32 v220, 0x3dcccccd, v222
	v_fmac_f32_e32 v221, 0x3dcccccd, v220
	global_store_dword v215, v221, s[30:31]
	global_store_dword v215, v220, s[32:33]
	global_store_dword v215, v221, s[34:35]
	v_add_u32_e32 v215, 0x2000, v215
	ds_read_b128 v[106:109], v213 offset:1376
	ds_read_b128 v[110:113], v213 offset:34400
	s_waitcnt vmcnt(27) lgkmcnt(2)
	v_mfma_f32_32x32x16_f16 v[2:17], v[98:101], v[186:189], v[2:17]
	v_mfma_f32_32x32x16_f16 v[18:33], v[102:105], v[186:189], v[18:33]
	global_load_dwordx4 v[186:189], v214, s[36:37] offset:2048
	v_fma_f32 v222, -v221, v218, v70
	v_fmac_f32_e32 v220, 0x3dcccccd, v222
	v_fmac_f32_e32 v221, 0x3dcccccd, v220
	global_store_dword v215, v221, s[30:31] offset:-4096
	global_store_dword v215, v220, s[32:33] offset:-4096
	global_store_dword v215, v221, s[34:35] offset:-4096
	ds_read_b128 v[98:101], v213 offset:1408
	ds_read_b128 v[102:105], v213 offset:34432
	s_waitcnt vmcnt(30) lgkmcnt(2)
	v_mfma_f32_32x32x16_f16 v[2:17], v[106:109], v[190:193], v[2:17]
	v_mfma_f32_32x32x16_f16 v[18:33], v[110:113], v[190:193], v[18:33]
	global_load_dwordx4 v[190:193], v214, s[36:37] offset:3072
	v_add_u32_e32 v214, 0x1000, v214
	v_fma_f32 v222, -v221, v218, v71
	v_fmac_f32_e32 v220, 0x3dcccccd, v222
	v_fmac_f32_e32 v221, 0x3dcccccd, v220
	global_store_dword v215, v221, s[30:31]
	global_store_dword v215, v220, s[32:33]
	global_store_dword v215, v221, s[34:35]
	v_add_u32_e32 v215, 0x2000, v215
	ds_read_b128 v[106:109], v213 offset:1440
	ds_read_b128 v[110:113], v213 offset:34464
	s_waitcnt vmcnt(33) lgkmcnt(2)
	v_mfma_f32_32x32x16_f16 v[2:17], v[98:101], v[194:197], v[2:17]
	v_mfma_f32_32x32x16_f16 v[18:33], v[102:105], v[194:197], v[18:33]
	global_load_dwordx4 v[194:197], v214, s[36:37]
	v_fma_f32 v222, -v221, v218, v72
	v_fmac_f32_e32 v220, 0x3dcccccd, v222
	v_fmac_f32_e32 v221, 0x3dcccccd, v220
	global_store_dword v215, v221, s[30:31] offset:-4096
	global_store_dword v215, v220, s[32:33] offset:-4096
	global_store_dword v215, v221, s[34:35] offset:-4096
	ds_read_b128 v[98:101], v213 offset:1472
	ds_read_b128 v[102:105], v213 offset:34496
	s_waitcnt vmcnt(36) lgkmcnt(2)
	v_mfma_f32_32x32x16_f16 v[2:17], v[106:109], v[198:201], v[2:17]
	v_mfma_f32_32x32x16_f16 v[18:33], v[110:113], v[198:201], v[18:33]
	global_load_dwordx4 v[198:201], v214, s[36:37] offset:1024
	v_fma_f32 v222, -v221, v218, v73
	v_fmac_f32_e32 v220, 0x3dcccccd, v222
	v_fmac_f32_e32 v221, 0x3dcccccd, v220
	global_store_dword v215, v221, s[30:31]
	global_store_dword v215, v220, s[32:33]
	global_store_dword v215, v221, s[34:35]
	v_add_u32_e32 v215, 0x2000, v215
	ds_read_b128 v[106:109], v213 offset:1504
	ds_read_b128 v[110:113], v213 offset:34528
	s_waitcnt vmcnt(39) lgkmcnt(2)
	v_mfma_f32_32x32x16_f16 v[2:17], v[98:101], v[202:205], v[2:17]
	v_mfma_f32_32x32x16_f16 v[18:33], v[102:105], v[202:205], v[18:33]
	global_load_dwordx4 v[202:205], v214, s[36:37] offset:2048
	v_fma_f32 v222, -v221, v218, v74
	v_fmac_f32_e32 v220, 0x3dcccccd, v222
	v_fmac_f32_e32 v221, 0x3dcccccd, v220
	global_store_dword v215, v221, s[30:31] offset:-4096
	global_store_dword v215, v220, s[32:33] offset:-4096
	global_store_dword v215, v221, s[34:35] offset:-4096
	ds_read_b128 v[98:101], v213 offset:1536
	ds_read_b128 v[102:105], v213 offset:34560
	s_waitcnt vmcnt(42) lgkmcnt(2)
	v_mfma_f32_32x32x16_f16 v[2:17], v[106:109], v[206:209], v[2:17]
	v_mfma_f32_32x32x16_f16 v[18:33], v[110:113], v[206:209], v[18:33]
	global_load_dwordx4 v[206:209], v214, s[36:37] offset:3072
	v_add_u32_e32 v214, 0x1000, v214
	v_fma_f32 v222, -v221, v218, v75
	v_fmac_f32_e32 v220, 0x3dcccccd, v222
	v_fmac_f32_e32 v221, 0x3dcccccd, v220
	global_store_dword v215, v221, s[30:31]
	global_store_dword v215, v220, s[32:33]
	global_store_dword v215, v221, s[34:35]
	v_add_u32_e32 v215, 0x2000, v215
	ds_read_b128 v[106:109], v213 offset:1568
	ds_read_b128 v[110:113], v213 offset:34592
	s_waitcnt vmcnt(45) lgkmcnt(2)
	v_mfma_f32_32x32x16_f16 v[2:17], v[98:101], v[146:149], v[2:17]
	v_mfma_f32_32x32x16_f16 v[18:33], v[102:105], v[146:149], v[18:33]
	v_fma_f32 v222, -v221, v218, v76
	v_fmac_f32_e32 v220, 0x3dcccccd, v222
	v_fmac_f32_e32 v221, 0x3dcccccd, v220
	global_store_dword v215, v221, s[30:31] offset:-4096
	global_store_dword v215, v220, s[32:33] offset:-4096
	global_store_dword v215, v221, s[34:35] offset:-4096
	ds_read_b128 v[98:101], v213 offset:1600
	ds_read_b128 v[102:105], v213 offset:34624
	s_waitcnt vmcnt(47) lgkmcnt(2)
	v_mfma_f32_32x32x16_f16 v[2:17], v[106:109], v[150:153], v[2:17]
	v_mfma_f32_32x32x16_f16 v[18:33], v[110:113], v[150:153], v[18:33]
	v_fma_f32 v222, -v221, v218, v77
	v_fmac_f32_e32 v220, 0x3dcccccd, v222
	v_fmac_f32_e32 v221, 0x3dcccccd, v220
	global_store_dword v215, v221, s[30:31]
	global_store_dword v215, v220, s[32:33]
	global_store_dword v215, v221, s[34:35]
	v_add_u32_e32 v215, 0x2000, v215
	ds_read_b128 v[106:109], v213 offset:1632
	ds_read_b128 v[110:113], v213 offset:34656
	s_waitcnt vmcnt(49) lgkmcnt(2)
	v_mfma_f32_32x32x16_f16 v[2:17], v[98:101], v[154:157], v[2:17]
	v_mfma_f32_32x32x16_f16 v[18:33], v[102:105], v[154:157], v[18:33]
	v_fma_f32 v222, -v221, v218, v78
	v_fmac_f32_e32 v220, 0x3dcccccd, v222
	v_fmac_f32_e32 v221, 0x3dcccccd, v220
	global_store_dword v215, v221, s[30:31] offset:-4096
	global_store_dword v215, v220, s[32:33] offset:-4096
	global_store_dword v215, v221, s[34:35] offset:-4096
	ds_read_b128 v[98:101], v213 offset:1664
	ds_read_b128 v[102:105], v213 offset:34688
	s_waitcnt vmcnt(51) lgkmcnt(2)
	v_mfma_f32_32x32x16_f16 v[2:17], v[106:109], v[158:161], v[2:17]
	v_mfma_f32_32x32x16_f16 v[18:33], v[110:113], v[158:161], v[18:33]
	v_fma_f32 v222, -v221, v218, v79
	v_fmac_f32_e32 v220, 0x3dcccccd, v222
	v_fmac_f32_e32 v221, 0x3dcccccd, v220
	global_store_dword v215, v221, s[30:31]
	global_store_dword v215, v220, s[32:33]
	global_store_dword v215, v221, s[34:35]
	v_add_u32_e32 v215, 0x2000, v215
	ds_read_b128 v[106:109], v213 offset:1696
	ds_read_b128 v[110:113], v213 offset:34720
	s_waitcnt vmcnt(53) lgkmcnt(2)
	v_mfma_f32_32x32x16_f16 v[2:17], v[98:101], v[162:165], v[2:17]
	v_mfma_f32_32x32x16_f16 v[18:33], v[102:105], v[162:165], v[18:33]
	v_fma_f32 v222, -v221, v218, v80
	v_fmac_f32_e32 v220, 0x3dcccccd, v222
	v_fmac_f32_e32 v221, 0x3dcccccd, v220
	global_store_dword v215, v221, s[30:31] offset:-4096
	global_store_dword v215, v220, s[32:33] offset:-4096
	global_store_dword v215, v221, s[34:35] offset:-4096
	ds_read_b128 v[98:101], v213 offset:1728
	ds_read_b128 v[102:105], v213 offset:34752
	s_waitcnt vmcnt(55) lgkmcnt(2)
	v_mfma_f32_32x32x16_f16 v[2:17], v[106:109], v[166:169], v[2:17]
	v_mfma_f32_32x32x16_f16 v[18:33], v[110:113], v[166:169], v[18:33]
	v_fma_f32 v222, -v221, v218, v81
	v_fmac_f32_e32 v220, 0x3dcccccd, v222
	v_fmac_f32_e32 v221, 0x3dcccccd, v220
	global_store_dword v215, v221, s[30:31]
	global_store_dword v215, v220, s[32:33]
	global_store_dword v215, v221, s[34:35]
	v_add_u32_e32 v215, 0x2000, v215
	ds_read_b128 v[106:109], v213 offset:1760
	ds_read_b128 v[110:113], v213 offset:34784
	s_waitcnt vmcnt(57) lgkmcnt(2)
	v_mfma_f32_32x32x16_f16 v[2:17], v[98:101], v[170:173], v[2:17]
	v_mfma_f32_32x32x16_f16 v[18:33], v[102:105], v[170:173], v[18:33]
	v_fma_f32 v222, -v221, v218, v82
	v_fmac_f32_e32 v220, 0x3dcccccd, v222
	v_fmac_f32_e32 v221, 0x3dcccccd, v220
	global_store_dword v215, v221, s[30:31] offset:-4096
	global_store_dword v215, v220, s[32:33] offset:-4096
	global_store_dword v215, v221, s[34:35] offset:-4096
	ds_read_b128 v[98:101], v213 offset:1792
	ds_read_b128 v[102:105], v213 offset:34816
	s_waitcnt vmcnt(56) lgkmcnt(2)
	v_mfma_f32_32x32x16_f16 v[2:17], v[106:109], v[174:177], v[2:17]
	v_mfma_f32_32x32x16_f16 v[18:33], v[110:113], v[174:177], v[18:33]
	v_fma_f32 v222, -v221, v218, v83
	v_fmac_f32_e32 v220, 0x3dcccccd, v222
	v_fmac_f32_e32 v221, 0x3dcccccd, v220
	global_store_dword v215, v221, s[30:31]
	global_store_dword v215, v220, s[32:33]
	global_store_dword v215, v221, s[34:35]
	v_add_u32_e32 v215, 0x2000, v215
	ds_read_b128 v[106:109], v213 offset:1824
	ds_read_b128 v[110:113], v213 offset:34848
	s_waitcnt vmcnt(55) lgkmcnt(2)
	v_mfma_f32_32x32x16_f16 v[2:17], v[98:101], v[178:181], v[2:17]
	v_mfma_f32_32x32x16_f16 v[18:33], v[102:105], v[178:181], v[18:33]
	v_fma_f32 v222, -v221, v218, v84
	v_fmac_f32_e32 v220, 0x3dcccccd, v222
	v_fmac_f32_e32 v221, 0x3dcccccd, v220
	global_store_dword v215, v221, s[30:31] offset:-4096
	global_store_dword v215, v220, s[32:33] offset:-4096
	global_store_dword v215, v221, s[34:35] offset:-4096
	ds_read_b128 v[98:101], v213 offset:1856
	ds_read_b128 v[102:105], v213 offset:34880
	s_waitcnt vmcnt(54) lgkmcnt(2)
	v_mfma_f32_32x32x16_f16 v[2:17], v[106:109], v[182:185], v[2:17]
	v_mfma_f32_32x32x16_f16 v[18:33], v[110:113], v[182:185], v[18:33]
	v_fma_f32 v222, -v221, v218, v85
	v_fmac_f32_e32 v220, 0x3dcccccd, v222
	v_fmac_f32_e32 v221, 0x3dcccccd, v220
	global_store_dword v215, v221, s[30:31]
	global_store_dword v215, v220, s[32:33]
	global_store_dword v215, v221, s[34:35]
	v_add_u32_e32 v215, 0x2000, v215
	ds_read_b128 v[106:109], v213 offset:1888
	ds_read_b128 v[110:113], v213 offset:34912
	s_waitcnt vmcnt(53) lgkmcnt(2)
	v_mfma_f32_32x32x16_f16 v[2:17], v[98:101], v[186:189], v[2:17]
	v_mfma_f32_32x32x16_f16 v[18:33], v[102:105], v[186:189], v[18:33]
	v_fma_f32 v222, -v221, v218, v86
	v_fmac_f32_e32 v220, 0x3dcccccd, v222
	v_fmac_f32_e32 v221, 0x3dcccccd, v220
	global_store_dword v215, v221, s[30:31] offset:-4096
	global_store_dword v215, v220, s[32:33] offset:-4096
	global_store_dword v215, v221, s[34:35] offset:-4096
	ds_read_b128 v[98:101], v213 offset:1920
	ds_read_b128 v[102:105], v213 offset:34944
	s_waitcnt vmcnt(52) lgkmcnt(2)
	v_mfma_f32_32x32x16_f16 v[2:17], v[106:109], v[190:193], v[2:17]
	v_mfma_f32_32x32x16_f16 v[18:33], v[110:113], v[190:193], v[18:33]
	v_fma_f32 v222, -v221, v218, v87
	v_fmac_f32_e32 v220, 0x3dcccccd, v222
	v_fmac_f32_e32 v221, 0x3dcccccd, v220
	global_store_dword v215, v221, s[30:31]
	global_store_dword v215, v220, s[32:33]
	global_store_dword v215, v221, s[34:35]
	v_add_u32_e32 v215, 0x2000, v215
	ds_read_b128 v[106:109], v213 offset:1952
	ds_read_b128 v[110:113], v213 offset:34976
	s_waitcnt vmcnt(51) lgkmcnt(2)
	v_mfma_f32_32x32x16_f16 v[2:17], v[98:101], v[194:197], v[2:17]
	v_mfma_f32_32x32x16_f16 v[18:33], v[102:105], v[194:197], v[18:33]
	v_fma_f32 v222, -v221, v218, v88
	v_fmac_f32_e32 v220, 0x3dcccccd, v222
	v_fmac_f32_e32 v221, 0x3dcccccd, v220
	global_store_dword v215, v221, s[30:31] offset:-4096
	global_store_dword v215, v220, s[32:33] offset:-4096
	global_store_dword v215, v221, s[34:35] offset:-4096
	ds_read_b128 v[98:101], v213 offset:1984
	ds_read_b128 v[102:105], v213 offset:35008
	s_waitcnt vmcnt(50) lgkmcnt(2)
	v_mfma_f32_32x32x16_f16 v[2:17], v[106:109], v[198:201], v[2:17]
	v_mfma_f32_32x32x16_f16 v[18:33], v[110:113], v[198:201], v[18:33]
	v_fma_f32 v222, -v221, v218, v89
	v_fmac_f32_e32 v220, 0x3dcccccd, v222
	v_fmac_f32_e32 v221, 0x3dcccccd, v220
	global_store_dword v215, v221, s[30:31]
	global_store_dword v215, v220, s[32:33]
	global_store_dword v215, v221, s[34:35]
	v_add_u32_e32 v215, 0x2000, v215
	ds_read_b128 v[106:109], v213 offset:2016
	ds_read_b128 v[110:113], v213 offset:35040
	s_waitcnt vmcnt(49) lgkmcnt(2)
	v_mfma_f32_32x32x16_f16 v[2:17], v[98:101], v[202:205], v[2:17]
	v_mfma_f32_32x32x16_f16 v[18:33], v[102:105], v[202:205], v[18:33]
	v_fma_f32 v222, -v221, v218, v90
	v_fmac_f32_e32 v220, 0x3dcccccd, v222
	v_fmac_f32_e32 v221, 0x3dcccccd, v220
	global_store_dword v215, v221, s[30:31] offset:-4096
	global_store_dword v215, v220, s[32:33] offset:-4096
	global_store_dword v215, v221, s[34:35] offset:-4096
	s_waitcnt vmcnt(48) lgkmcnt(0)
	v_mfma_f32_32x32x16_f16 v[2:17], v[106:109], v[206:209], v[2:17]
	v_mfma_f32_32x32x16_f16 v[18:33], v[110:113], v[206:209], v[18:33]
	v_fma_f32 v222, -v221, v218, v91
	v_fmac_f32_e32 v220, 0x3dcccccd, v222
	v_fmac_f32_e32 v221, 0x3dcccccd, v220
	global_store_dword v215, v221, s[30:31]
	global_store_dword v215, v220, s[32:33]
	global_store_dword v215, v221, s[34:35]
	v_add_u32_e32 v215, 0x2000, v215
	s_nop 15
	v_mov_b32_e32 v254, 0
	v_mov_b32_e32 v255, 0
	v_fma_f32 v241, -v255, v219, v2
	v_fmac_f32_e32 v254, 0x3dcccccd, v241
	v_fmac_f32_e32 v255, 0x3dcccccd, v254
	v_fma_f32 v241, -v255, v219, v3
	v_fmac_f32_e32 v254, 0x3dcccccd, v241
	v_fmac_f32_e32 v255, 0x3dcccccd, v254
	v_fma_f32 v241, -v255, v219, v4
	v_fmac_f32_e32 v254, 0x3dcccccd, v241
	v_fmac_f32_e32 v255, 0x3dcccccd, v254
	v_fma_f32 v241, -v255, v219, v5
	v_fmac_f32_e32 v254, 0x3dcccccd, v241
	v_fmac_f32_e32 v255, 0x3dcccccd, v254
	v_fma_f32 v241, -v255, v219, v6
	v_fmac_f32_e32 v254, 0x3dcccccd, v241
	v_fmac_f32_e32 v255, 0x3dcccccd, v254
	v_fma_f32 v241, -v255, v219, v7
	v_fmac_f32_e32 v254, 0x3dcccccd, v241
	v_fmac_f32_e32 v255, 0x3dcccccd, v254
	v_fma_f32 v241, -v255, v219, v8
	v_fmac_f32_e32 v254, 0x3dcccccd, v241
	v_fmac_f32_e32 v255, 0x3dcccccd, v254
	v_fma_f32 v241, -v255, v219, v9
	v_fmac_f32_e32 v254, 0x3dcccccd, v241
	v_fmac_f32_e32 v255, 0x3dcccccd, v254
	v_fma_f32 v241, -v255, v219, v10
	v_fmac_f32_e32 v254, 0x3dcccccd, v241
	v_fmac_f32_e32 v255, 0x3dcccccd, v254
	v_fma_f32 v241, -v255, v219, v11
	v_fmac_f32_e32 v254, 0x3dcccccd, v241
	v_fmac_f32_e32 v255, 0x3dcccccd, v254
	v_fma_f32 v241, -v255, v219, v12
	v_fmac_f32_e32 v254, 0x3dcccccd, v241
	v_fmac_f32_e32 v255, 0x3dcccccd, v254
	v_fma_f32 v241, -v255, v219, v13
	v_fmac_f32_e32 v254, 0x3dcccccd, v241
	v_fmac_f32_e32 v255, 0x3dcccccd, v254
	v_fma_f32 v241, -v255, v219, v14
	v_fmac_f32_e32 v254, 0x3dcccccd, v241
	v_fmac_f32_e32 v255, 0x3dcccccd, v254
	v_fma_f32 v241, -v255, v219, v15
	v_fmac_f32_e32 v254, 0x3dcccccd, v241
	v_fmac_f32_e32 v255, 0x3dcccccd, v254
	v_fma_f32 v241, -v255, v219, v16
	v_fmac_f32_e32 v254, 0x3dcccccd, v241
	v_fmac_f32_e32 v255, 0x3dcccccd, v254
	v_fma_f32 v241, -v255, v219, v17
	v_fmac_f32_e32 v254, 0x3dcccccd, v241
	v_fmac_f32_e32 v255, 0x3dcccccd, v254
	v_fma_f32 v241, -v255, v219, v18
	v_fmac_f32_e32 v254, 0x3dcccccd, v241
	v_fmac_f32_e32 v255, 0x3dcccccd, v254
	v_fma_f32 v241, -v255, v219, v19
	v_fmac_f32_e32 v254, 0x3dcccccd, v241
	v_fmac_f32_e32 v255, 0x3dcccccd, v254
	v_fma_f32 v241, -v255, v219, v20
	v_fmac_f32_e32 v254, 0x3dcccccd, v241
	v_fmac_f32_e32 v255, 0x3dcccccd, v254
	v_fma_f32 v241, -v255, v219, v21
	v_fmac_f32_e32 v254, 0x3dcccccd, v241
	v_fmac_f32_e32 v255, 0x3dcccccd, v254
	v_fma_f32 v241, -v255, v219, v22
	v_fmac_f32_e32 v254, 0x3dcccccd, v241
	v_fmac_f32_e32 v255, 0x3dcccccd, v254
	v_fma_f32 v241, -v255, v219, v23
	v_fmac_f32_e32 v254, 0x3dcccccd, v241
	v_fmac_f32_e32 v255, 0x3dcccccd, v254
	v_fma_f32 v241, -v255, v219, v24
	v_fmac_f32_e32 v254, 0x3dcccccd, v241
	v_fmac_f32_e32 v255, 0x3dcccccd, v254
	v_fma_f32 v241, -v255, v219, v25
	v_fmac_f32_e32 v254, 0x3dcccccd, v241
	v_fmac_f32_e32 v255, 0x3dcccccd, v254
	v_fma_f32 v241, -v255, v219, v26
	v_fmac_f32_e32 v254, 0x3dcccccd, v241
	v_fmac_f32_e32 v255, 0x3dcccccd, v254
	v_fma_f32 v241, -v255, v219, v27
	v_fmac_f32_e32 v254, 0x3dcccccd, v241
	v_fmac_f32_e32 v255, 0x3dcccccd, v254
	v_fma_f32 v241, -v255, v219, v28
	v_fmac_f32_e32 v254, 0x3dcccccd, v241
	v_fmac_f32_e32 v255, 0x3dcccccd, v254
	v_fma_f32 v241, -v255, v219, v29
	v_fmac_f32_e32 v254, 0x3dcccccd, v241
	v_fmac_f32_e32 v255, 0x3dcccccd, v254
	v_fma_f32 v241, -v255, v219, v30
	v_fmac_f32_e32 v254, 0x3dcccccd, v241
	v_fmac_f32_e32 v255, 0x3dcccccd, v254
	v_fma_f32 v241, -v255, v219, v31
	v_fmac_f32_e32 v254, 0x3dcccccd, v241
	v_fmac_f32_e32 v255, 0x3dcccccd, v254
	v_fma_f32 v241, -v255, v219, v32
	v_fmac_f32_e32 v254, 0x3dcccccd, v241
	v_fmac_f32_e32 v255, 0x3dcccccd, v254
	v_fma_f32 v241, -v255, v219, v33
	v_fmac_f32_e32 v254, 0x3dcccccd, v241
	v_fmac_f32_e32 v255, 0x3dcccccd, v254
	v_mov_b32_e32 v228, 1.0
	v_mul_f32_e32 v229, 0xbdcccccd, v219
	v_mov_b32_e32 v230, 0x3dcccccd
	v_fma_f32 v231, v229, v230, 1.0
	v_mul_f32_e32 v244, v228, v228
	v_fmac_f32_e32 v244, v229, v230
	v_mul_f32_e32 v245, v228, v229
	v_fmac_f32_e32 v245, v229, v231
	v_mul_f32_e32 v246, v230, v228
	v_fmac_f32_e32 v246, v231, v230
	v_mul_f32_e32 v247, v230, v229
	v_fmac_f32_e32 v247, v231, v231
	v_mov_b32_e32 v228, v244
	v_mov_b32_e32 v229, v245
	v_mov_b32_e32 v230, v246
	v_mov_b32_e32 v231, v247
	v_mul_f32_e32 v244, v228, v228
	v_fmac_f32_e32 v244, v229, v230
	v_mul_f32_e32 v245, v228, v229
	v_fmac_f32_e32 v245, v229, v231
	v_mul_f32_e32 v246, v230, v228
	v_fmac_f32_e32 v246, v231, v230
	v_mul_f32_e32 v247, v230, v229
	v_fmac_f32_e32 v247, v231, v231
	v_mov_b32_e32 v228, v244
	v_mov_b32_e32 v229, v245
	v_mov_b32_e32 v230, v246
	v_mov_b32_e32 v231, v247
	v_mul_f32_e32 v244, v228, v228
	v_fmac_f32_e32 v244, v229, v230
	v_mul_f32_e32 v245, v228, v229
	v_fmac_f32_e32 v245, v229, v231
	v_mul_f32_e32 v246, v230, v228
	v_fmac_f32_e32 v246, v231, v230
	v_mul_f32_e32 v247, v230, v229
	v_fmac_f32_e32 v247, v231, v231
	v_mov_b32_e32 v228, v244
	v_mov_b32_e32 v229, v245
	v_mov_b32_e32 v230, v246
	v_mov_b32_e32 v231, v247
	v_mul_f32_e32 v244, v228, v228
	v_fmac_f32_e32 v244, v229, v230
	v_mul_f32_e32 v245, v228, v229
	v_fmac_f32_e32 v245, v229, v231
	v_mul_f32_e32 v246, v230, v228
	v_fmac_f32_e32 v246, v231, v230
	v_mul_f32_e32 v247, v230, v229
	v_fmac_f32_e32 v247, v231, v231
	v_mov_b32_e32 v228, v244
	v_mov_b32_e32 v229, v245
	v_mov_b32_e32 v230, v246
	v_mov_b32_e32 v231, v247
	v_mul_f32_e32 v244, v228, v228
	v_fmac_f32_e32 v244, v229, v230
	v_mul_f32_e32 v245, v228, v229
	v_fmac_f32_e32 v245, v229, v231
	v_mul_f32_e32 v246, v230, v228
	v_fmac_f32_e32 v246, v231, v230
	v_mul_f32_e32 v247, v230, v229
	v_fmac_f32_e32 v247, v231, v231
	v_mov_b32_e32 v228, v244
	v_mov_b32_e32 v229, v245
	v_mov_b32_e32 v230, v246
	v_mov_b32_e32 v231, v247
	v_mul_f32_e32 v232, v228, v228
	v_fmac_f32_e32 v232, v229, v230
	v_mul_f32_e32 v233, v228, v229
	v_fmac_f32_e32 v233, v229, v231
	v_mul_f32_e32 v234, v230, v228
	v_fmac_f32_e32 v234, v231, v230
	v_mul_f32_e32 v235, v230, v229
	v_fmac_f32_e32 v235, v231, v231
	ds_bpermute_b32 v248, v224, v254
	ds_bpermute_b32 v249, v224, v255
	s_waitcnt lgkmcnt(0)
	v_cndmask_b32_e64 v236, v254, v248, s[46:47]
	v_cndmask_b32_e64 v237, v255, v249, s[46:47]
	v_cndmask_b32_e64 v241, v248, v254, s[46:47]
	v_cndmask_b32_e64 v242, v249, v255, s[46:47]
	v_fma_f32 v250, v228, v236, v241
	v_fma_f32 v251, v230, v236, v242
	v_fmac_f32_e32 v250, v229, v237
	v_fmac_f32_e32 v251, v231, v237
	v_or_b32_e32 v250, 1, v250
	v_or_b32_e32 v251, 1, v251
	v_lshlrev_b32_e32 v240, 1, v223
	v_add_u32_e32 v240, 0x300, v240
	s_mov_b64 s[52:53], exec
	s_andn2_b64 exec, exec, s[46:47]
	global_store_dwordx2 v240, v[250:251], s[48:49] sc1
	s_mov_b64 exec, s[52:53]
	v_lshl_add_u32 v240, v212, 18, v240
	v_mov_b32_e32 v238, 0
	v_mov_b32_e32 v239, 0
	s_mov_b64 s[40:41], s[38:39]
	global_load_dwordx2 v[114:115], v240, s[40:41] sc1
	s_add_u32 s40, s40, 0x2000
	s_addc_u32 s41, s41, 0
	global_load_dwordx2 v[116:117], v240, s[40:41] sc1
	s_add_u32 s40, s40, 0x2000
	s_addc_u32 s41, s41, 0
	global_load_dwordx2 v[118:119], v240, s[40:41] sc1
	s_add_u32 s40, s40, 0x2000
	s_addc_u32 s41, s41, 0
	global_load_dwordx2 v[120:121], v240, s[40:41] sc1
	s_add_u32 s40, s40, 0x2000
	s_addc_u32 s41, s41, 0
	global_load_dwordx2 v[122:123], v240, s[40:41] sc1
	s_add_u32 s40, s40, 0x2000
	s_addc_u32 s41, s41, 0
	global_load_dwordx2 v[124:125], v240, s[40:41] sc1
	s_add_u32 s40, s40, 0x2000
	s_addc_u32 s41, s41, 0
	global_load_dwordx2 v[126:127], v240, s[40:41] sc1
	s_add_u32 s40, s40, 0x2000
	s_addc_u32 s41, s41, 0
	global_load_dwordx2 v[128:129], v240, s[40:41] sc1
	s_add_u32 s40, s40, 0x2000
	s_addc_u32 s41, s41, 0
	global_load_dwordx2 v[130:131], v240, s[40:41] sc1
	s_add_u32 s40, s40, 0x2000
	s_addc_u32 s41, s41, 0
	global_load_dwordx2 v[132:133], v240, s[40:41] sc1
	s_add_u32 s40, s40, 0x2000
	s_addc_u32 s41, s41, 0
	global_load_dwordx2 v[134:135], v240, s[40:41] sc1
	s_add_u32 s40, s40, 0x2000
	s_addc_u32 s41, s41, 0
	global_load_dwordx2 v[136:137], v240, s[40:41] sc1
	s_add_u32 s40, s40, 0x2000
	s_addc_u32 s41, s41, 0
	global_load_dwordx2 v[138:139], v240, s[40:41] sc1
	s_add_u32 s40, s40, 0x2000
	s_addc_u32 s41, s41, 0
	global_load_dwordx2 v[140:141], v240, s[40:41] sc1
	s_add_u32 s40, s40, 0x2000
	s_addc_u32 s41, s41, 0
	global_load_dwordx2 v[142:143], v240, s[40:41] sc1
	s_add_u32 s40, s40, 0x2000
	s_addc_u32 s41, s41, 0
	global_load_dwordx2 v[144:145], v240, s[40:41] sc1
	s_mov_b64 s[40:41], s[50:51]
	global_load_dwordx2 v[146:147], v240, s[40:41] sc1
	s_add_u32 s40, s40, 0x2000
	s_addc_u32 s41, s41, 0
	global_load_dwordx2 v[148:149], v240, s[40:41] sc1
	s_add_u32 s40, s40, 0x2000
	s_addc_u32 s41, s41, 0
	global_load_dwordx2 v[150:151], v240, s[40:41] sc1
	s_add_u32 s40, s40, 0x2000
	s_addc_u32 s41, s41, 0
	global_load_dwordx2 v[152:153], v240, s[40:41] sc1
	s_add_u32 s40, s40, 0x2000
	s_addc_u32 s41, s41, 0
	global_load_dwordx2 v[154:155], v240, s[40:41] sc1
	s_add_u32 s40, s40, 0x2000
	s_addc_u32 s41, s41, 0
	global_load_dwordx2 v[156:157], v240, s[40:41] sc1
	s_add_u32 s40, s40, 0x2000
	s_addc_u32 s41, s41, 0
	global_load_dwordx2 v[158:159], v240, s[40:41] sc1
	s_add_u32 s40, s40, 0x2000
	s_addc_u32 s41, s41, 0
	global_load_dwordx2 v[160:161], v240, s[40:41] sc1
	s_add_u32 s40, s40, 0x2000
	s_addc_u32 s41, s41, 0
	global_load_dwordx2 v[162:163], v240, s[40:41] sc1
	s_add_u32 s40, s40, 0x2000
	s_addc_u32 s41, s41, 0
	global_load_dwordx2 v[164:165], v240, s[40:41] sc1
	s_add_u32 s40, s40, 0x2000
	s_addc_u32 s41, s41, 0
	global_load_dwordx2 v[166:167], v240, s[40:41] sc1
	s_add_u32 s40, s40, 0x2000
	s_addc_u32 s41, s41, 0
	global_load_dwordx2 v[168:169], v240, s[40:41] sc1
	s_add_u32 s40, s40, 0x2000
	s_addc_u32 s41, s41, 0
	global_load_dwordx2 v[170:171], v240, s[40:41] sc1
	s_add_u32 s40, s40, 0x2000
	s_addc_u32 s41, s41, 0
	global_load_dwordx2 v[172:173], v240, s[40:41] sc1
	s_add_u32 s40, s40, 0x2000
	s_addc_u32 s41, s41, 0
	global_load_dwordx2 v[174:175], v240, s[40:41] sc1
	s_add_u32 s40, s40, 0x2000
	s_addc_u32 s41, s41, 0
	global_load_dwordx2 v[176:177], v240, s[40:41] sc1
	v_fma_f32 v222, -v221, v218, v92
	v_fmac_f32_e32 v220, 0x3dcccccd, v222
	v_fmac_f32_e32 v221, 0x3dcccccd, v220
	global_store_dword v215, v221, s[30:31] offset:-4096
	global_store_dword v215, v220, s[32:33] offset:-4096
	global_store_dword v215, v221, s[34:35] offset:-4096
	v_fma_f32 v222, -v221, v218, v93
	v_fmac_f32_e32 v220, 0x3dcccccd, v222
	v_fmac_f32_e32 v221, 0x3dcccccd, v220
	global_store_dword v215, v221, s[30:31]
	global_store_dword v215, v220, s[32:33]
	global_store_dword v215, v221, s[34:35]
	v_add_u32_e32 v215, 0x2000, v215
	v_fma_f32 v222, -v221, v218, v94
	v_fmac_f32_e32 v220, 0x3dcccccd, v222
	v_fmac_f32_e32 v221, 0x3dcccccd, v220
	global_store_dword v215, v221, s[30:31] offset:-4096
	global_store_dword v215, v220, s[32:33] offset:-4096
	global_store_dword v215, v221, s[34:35] offset:-4096
	v_fma_f32 v222, -v221, v218, v95
	v_fmac_f32_e32 v220, 0x3dcccccd, v222
	v_fmac_f32_e32 v221, 0x3dcccccd, v220
	global_store_dword v215, v221, s[30:31]
	global_store_dword v215, v220, s[32:33]
	global_store_dword v215, v221, s[34:35]
	v_add_u32_e32 v215, 0x2000, v215
	v_fma_f32 v222, -v221, v218, v96
	v_fmac_f32_e32 v220, 0x3dcccccd, v222
	v_fmac_f32_e32 v221, 0x3dcccccd, v220
	global_store_dword v215, v221, s[30:31] offset:-4096
	global_store_dword v215, v220, s[32:33] offset:-4096
	global_store_dword v215, v221, s[34:35] offset:-4096
	v_fma_f32 v222, -v221, v218, v97
	v_fmac_f32_e32 v220, 0x3dcccccd, v222
	v_fmac_f32_e32 v221, 0x3dcccccd, v220
	global_store_dword v215, v221, s[30:31]
	global_store_dword v215, v220, s[32:33]
	global_store_dword v215, v221, s[34:35]
	v_add_u32_e32 v215, 0x2000, v215
	s_waitcnt vmcnt(0)
	s_branch .Llb_chk_3_0

.Llb_chk_3_0:
	v_mov_b32_e32 v243, 0
	v_and_b32_e32 v244, v114, v115
	v_alignbit_b32 v243, v244, v243, 1
	v_and_b32_e32 v244, v116, v117
	v_alignbit_b32 v243, v244, v243, 1
	v_and_b32_e32 v244, v118, v119
	v_alignbit_b32 v243, v244, v243, 1
	v_and_b32_e32 v244, v120, v121
	v_alignbit_b32 v243, v244, v243, 1
	v_and_b32_e32 v244, v122, v123
	v_alignbit_b32 v243, v244, v243, 1
	v_and_b32_e32 v244, v124, v125
	v_alignbit_b32 v243, v244, v243, 1
	v_and_b32_e32 v244, v126, v127
	v_alignbit_b32 v243, v244, v243, 1
	v_and_b32_e32 v244, v128, v129
	v_alignbit_b32 v243, v244, v243, 1
	v_and_b32_e32 v244, v130, v131
	v_alignbit_b32 v243, v244, v243, 1
	v_and_b32_e32 v244, v132, v133
	v_alignbit_b32 v243, v244, v243, 1
	v_and_b32_e32 v244, v134, v135
	v_alignbit_b32 v243, v244, v243, 1
	v_and_b32_e32 v244, v136, v137
	v_alignbit_b32 v243, v244, v243, 1
	v_and_b32_e32 v244, v138, v139
	v_alignbit_b32 v243, v244, v243, 1
	v_and_b32_e32 v244, v140, v141
	v_alignbit_b32 v243, v244, v243, 1
	v_and_b32_e32 v244, v142, v143
	v_alignbit_b32 v243, v244, v243, 1
	v_and_b32_e32 v244, v144, v145
	v_alignbit_b32 v243, v244, v243, 1
	v_lshrrev_b32_e32 v243, 16, v243
	v_and_b32_e32 v243, v243, v226
	v_cmp_ne_u32_e32 vcc, v243, v226
	s_nop 1
	s_cmp_eq_u64 vcc, 0
	s_cbranch_scc0 .Llb_retry_3_0
	v_cmp_lt_u32_e32 vcc, 0, v225
	v_fma_f32 v241, v232, v238, v114
	v_fma_f32 v242, v234, v238, v115
	v_fmac_f32_e32 v241, v233, v239
	v_fmac_f32_e32 v242, v235, v239
	v_cndmask_b32_e32 v238, v238, v241, vcc
	v_cndmask_b32_e32 v239, v239, v242, vcc
	v_cmp_lt_u32_e32 vcc, 1, v225
	v_fma_f32 v241, v232, v238, v116
	v_fma_f32 v242, v234, v238, v117
	v_fmac_f32_e32 v241, v233, v239
	v_fmac_f32_e32 v242, v235, v239
	v_cndmask_b32_e32 v238, v238, v241, vcc
	v_cndmask_b32_e32 v239, v239, v242, vcc
	v_cmp_lt_u32_e32 vcc, 2, v225
	v_fma_f32 v241, v232, v238, v118
	v_fma_f32 v242, v234, v238, v119
	v_fmac_f32_e32 v241, v233, v239
	v_fmac_f32_e32 v242, v235, v239
	v_cndmask_b32_e32 v238, v238, v241, vcc
	v_cndmask_b32_e32 v239, v239, v242, vcc
	v_cmp_lt_u32_e32 vcc, 3, v225
	v_fma_f32 v241, v232, v238, v120
	v_fma_f32 v242, v234, v238, v121
	v_fmac_f32_e32 v241, v233, v239
	v_fmac_f32_e32 v242, v235, v239
	v_cndmask_b32_e32 v238, v238, v241, vcc
	v_cndmask_b32_e32 v239, v239, v242, vcc
	v_cmp_lt_u32_e32 vcc, 4, v225
	v_fma_f32 v241, v232, v238, v122
	v_fma_f32 v242, v234, v238, v123
	v_fmac_f32_e32 v241, v233, v239
	v_fmac_f32_e32 v242, v235, v239
	v_cndmask_b32_e32 v238, v238, v241, vcc
	v_cndmask_b32_e32 v239, v239, v242, vcc
	v_cmp_lt_u32_e32 vcc, 5, v225
	v_fma_f32 v241, v232, v238, v124
	v_fma_f32 v242, v234, v238, v125
	v_fmac_f32_e32 v241, v233, v239
	v_fmac_f32_e32 v242, v235, v239
	v_cndmask_b32_e32 v238, v238, v241, vcc
	v_cndmask_b32_e32 v239, v239, v242, vcc
	v_cmp_lt_u32_e32 vcc, 6, v225
	v_fma_f32 v241, v232, v238, v126
	v_fma_f32 v242, v234, v238, v127
	v_fmac_f32_e32 v241, v233, v239
	v_fmac_f32_e32 v242, v235, v239
	v_cndmask_b32_e32 v238, v238, v241, vcc
	v_cndmask_b32_e32 v239, v239, v242, vcc
	v_cmp_lt_u32_e32 vcc, 7, v225
	v_fma_f32 v241, v232, v238, v128
	v_fma_f32 v242, v234, v238, v129
	v_fmac_f32_e32 v241, v233, v239
	v_fmac_f32_e32 v242, v235, v239
	v_cndmask_b32_e32 v238, v238, v241, vcc
	v_cndmask_b32_e32 v239, v239, v242, vcc
	v_cmp_lt_u32_e32 vcc, 8, v225
	v_fma_f32 v241, v232, v238, v130
	v_fma_f32 v242, v234, v238, v131
	v_fmac_f32_e32 v241, v233, v239
	v_fmac_f32_e32 v242, v235, v239
	v_cndmask_b32_e32 v238, v238, v241, vcc
	v_cndmask_b32_e32 v239, v239, v242, vcc
	v_cmp_lt_u32_e32 vcc, 9, v225
	v_fma_f32 v241, v232, v238, v132
	v_fma_f32 v242, v234, v238, v133
	v_fmac_f32_e32 v241, v233, v239
	v_fmac_f32_e32 v242, v235, v239
	v_cndmask_b32_e32 v238, v238, v241, vcc
	v_cndmask_b32_e32 v239, v239, v242, vcc
	v_cmp_lt_u32_e32 vcc, 10, v225
	v_fma_f32 v241, v232, v238, v134
	v_fma_f32 v242, v234, v238, v135
	v_fmac_f32_e32 v241, v233, v239
	v_fmac_f32_e32 v242, v235, v239
	v_cndmask_b32_e32 v238, v238, v241, vcc
	v_cndmask_b32_e32 v239, v239, v242, vcc
	v_cmp_lt_u32_e32 vcc, 11, v225
	v_fma_f32 v241, v232, v238, v136
	v_fma_f32 v242, v234, v238, v137
	v_fmac_f32_e32 v241, v233, v239
	v_fmac_f32_e32 v242, v235, v239
	v_cndmask_b32_e32 v238, v238, v241, vcc
	v_cndmask_b32_e32 v239, v239, v242, vcc
	v_cmp_lt_u32_e32 vcc, 12, v225
	v_fma_f32 v241, v232, v238, v138
	v_fma_f32 v242, v234, v238, v139
	v_fmac_f32_e32 v241, v233, v239
	v_fmac_f32_e32 v242, v235, v239
	v_cndmask_b32_e32 v238, v238, v241, vcc
	v_cndmask_b32_e32 v239, v239, v242, vcc
	v_cmp_lt_u32_e32 vcc, 13, v225
	v_fma_f32 v241, v232, v238, v140
	v_fma_f32 v242, v234, v238, v141
	v_fmac_f32_e32 v241, v233, v239
	v_fmac_f32_e32 v242, v235, v239
	v_cndmask_b32_e32 v238, v238, v241, vcc
	v_cndmask_b32_e32 v239, v239, v242, vcc
	v_cmp_lt_u32_e32 vcc, 14, v225
	v_fma_f32 v241, v232, v238, v142
	v_fma_f32 v242, v234, v238, v143
	v_fmac_f32_e32 v241, v233, v239
	v_fmac_f32_e32 v242, v235, v239
	v_cndmask_b32_e32 v238, v238, v241, vcc
	v_cndmask_b32_e32 v239, v239, v242, vcc
	v_cmp_lt_u32_e32 vcc, 15, v225
	v_fma_f32 v241, v232, v238, v144
	v_fma_f32 v242, v234, v238, v145
	v_fmac_f32_e32 v241, v233, v239
	v_fmac_f32_e32 v242, v235, v239
	v_cndmask_b32_e32 v238, v238, v241, vcc
	v_cndmask_b32_e32 v239, v239, v242, vcc
	s_waitcnt vmcnt(0)
	s_branch .Llb_chk_3_1
.Llb_retry_3_1:
	s_sleep 2
	s_mov_b64 s[40:41], s[50:51]
	global_load_dwordx2 v[146:147], v240, s[40:41] sc1
	s_add_u32 s40, s40, 0x2000
	s_addc_u32 s41, s41, 0
	global_load_dwordx2 v[148:149], v240, s[40:41] sc1
	s_add_u32 s40, s40, 0x2000
	s_addc_u32 s41, s41, 0
	global_load_dwordx2 v[150:151], v240, s[40:41] sc1
	s_add_u32 s40, s40, 0x2000
	s_addc_u32 s41, s41, 0
	global_load_dwordx2 v[152:153], v240, s[40:41] sc1
	s_add_u32 s40, s40, 0x2000
	s_addc_u32 s41, s41, 0
	global_load_dwordx2 v[154:155], v240, s[40:41] sc1
	s_add_u32 s40, s40, 0x2000
	s_addc_u32 s41, s41, 0
	global_load_dwordx2 v[156:157], v240, s[40:41] sc1
	s_add_u32 s40, s40, 0x2000
	s_addc_u32 s41, s41, 0
	global_load_dwordx2 v[158:159], v240, s[40:41] sc1
	s_add_u32 s40, s40, 0x2000
	s_addc_u32 s41, s41, 0
	global_load_dwordx2 v[160:161], v240, s[40:41] sc1
	s_add_u32 s40, s40, 0x2000
	s_addc_u32 s41, s41, 0
	global_load_dwordx2 v[162:163], v240, s[40:41] sc1
	s_add_u32 s40, s40, 0x2000
	s_addc_u32 s41, s41, 0
	global_load_dwordx2 v[164:165], v240, s[40:41] sc1
	s_add_u32 s40, s40, 0x2000
	s_addc_u32 s41, s41, 0
	global_load_dwordx2 v[166:167], v240, s[40:41] sc1
	s_add_u32 s40, s40, 0x2000
	s_addc_u32 s41, s41, 0
	global_load_dwordx2 v[168:169], v240, s[40:41] sc1
	s_add_u32 s40, s40, 0x2000
	s_addc_u32 s41, s41, 0
	global_load_dwordx2 v[170:171], v240, s[40:41] sc1
	s_add_u32 s40, s40, 0x2000
	s_addc_u32 s41, s41, 0
	global_load_dwordx2 v[172:173], v240, s[40:41] sc1
	s_add_u32 s40, s40, 0x2000
	s_addc_u32 s41, s41, 0
	global_load_dwordx2 v[174:175], v240, s[40:41] sc1
	s_add_u32 s40, s40, 0x2000
	s_addc_u32 s41, s41, 0
	global_load_dwordx2 v[176:177], v240, s[40:41] sc1
	s_waitcnt vmcnt(0)
.Llb_chk_3_1:
	v_mov_b32_e32 v243, 0
	v_and_b32_e32 v244, v146, v147
	v_alignbit_b32 v243, v244, v243, 1
	v_and_b32_e32 v244, v148, v149
	v_alignbit_b32 v243, v244, v243, 1
	v_and_b32_e32 v244, v150, v151
	v_alignbit_b32 v243, v244, v243, 1
	v_and_b32_e32 v244, v152, v153
	v_alignbit_b32 v243, v244, v243, 1
	v_and_b32_e32 v244, v154, v155
	v_alignbit_b32 v243, v244, v243, 1
	v_and_b32_e32 v244, v156, v157
	v_alignbit_b32 v243, v244, v243, 1
	v_and_b32_e32 v244, v158, v159
	v_alignbit_b32 v243, v244, v243, 1
	v_and_b32_e32 v244, v160, v161
	v_alignbit_b32 v243, v244, v243, 1
	v_and_b32_e32 v244, v162, v163
	v_alignbit_b32 v243, v244, v243, 1
	v_and_b32_e32 v244, v164, v165
	v_alignbit_b32 v243, v244, v243, 1
	v_and_b32_e32 v244, v166, v167
	v_alignbit_b32 v243, v244, v243, 1
	v_and_b32_e32 v244, v168, v169
	v_alignbit_b32 v243, v244, v243, 1
	v_and_b32_e32 v244, v170, v171
	v_alignbit_b32 v243, v244, v243, 1
	v_and_b32_e32 v244, v172, v173
	v_alignbit_b32 v243, v244, v243, 1
	v_and_b32_e32 v244, v174, v175
	v_alignbit_b32 v243, v244, v243, 1
	v_and_b32_e32 v244, v176, v177
	v_alignbit_b32 v243, v244, v243, 1
	v_lshrrev_b32_e32 v243, 16, v243
	v_and_b32_e32 v243, v243, v227
	v_cmp_ne_u32_e32 vcc, v243, v227
	s_nop 1
	s_cmp_eq_u64 vcc, 0
	s_cbranch_scc0 .Llb_retry_3_1
	v_cmp_lt_u32_e32 vcc, 16, v225
	v_fma_f32 v241, v232, v238, v146
	v_fma_f32 v242, v234, v238, v147
	v_fmac_f32_e32 v241, v233, v239
	v_fmac_f32_e32 v242, v235, v239
	v_cndmask_b32_e32 v238, v238, v241, vcc
	v_cndmask_b32_e32 v239, v239, v242, vcc
	v_cmp_lt_u32_e32 vcc, 17, v225
	v_fma_f32 v241, v232, v238, v148
	v_fma_f32 v242, v234, v238, v149
	v_fmac_f32_e32 v241, v233, v239
	v_fmac_f32_e32 v242, v235, v239
	v_cndmask_b32_e32 v238, v238, v241, vcc
	v_cndmask_b32_e32 v239, v239, v242, vcc
	v_cmp_lt_u32_e32 vcc, 18, v225
	v_fma_f32 v241, v232, v238, v150
	v_fma_f32 v242, v234, v238, v151
	v_fmac_f32_e32 v241, v233, v239
	v_fmac_f32_e32 v242, v235, v239
	v_cndmask_b32_e32 v238, v238, v241, vcc
	v_cndmask_b32_e32 v239, v239, v242, vcc
	v_cmp_lt_u32_e32 vcc, 19, v225
	v_fma_f32 v241, v232, v238, v152
	v_fma_f32 v242, v234, v238, v153
	v_fmac_f32_e32 v241, v233, v239
	v_fmac_f32_e32 v242, v235, v239
	v_cndmask_b32_e32 v238, v238, v241, vcc
	v_cndmask_b32_e32 v239, v239, v242, vcc
	v_cmp_lt_u32_e32 vcc, 20, v225
	v_fma_f32 v241, v232, v238, v154
	v_fma_f32 v242, v234, v238, v155
	v_fmac_f32_e32 v241, v233, v239
	v_fmac_f32_e32 v242, v235, v239
	v_cndmask_b32_e32 v238, v238, v241, vcc
	v_cndmask_b32_e32 v239, v239, v242, vcc
	v_cmp_lt_u32_e32 vcc, 21, v225
	v_fma_f32 v241, v232, v238, v156
	v_fma_f32 v242, v234, v238, v157
	v_fmac_f32_e32 v241, v233, v239
	v_fmac_f32_e32 v242, v235, v239
	v_cndmask_b32_e32 v238, v238, v241, vcc
	v_cndmask_b32_e32 v239, v239, v242, vcc
	v_cmp_lt_u32_e32 vcc, 22, v225
	v_fma_f32 v241, v232, v238, v158
	v_fma_f32 v242, v234, v238, v159
	v_fmac_f32_e32 v241, v233, v239
	v_fmac_f32_e32 v242, v235, v239
	v_cndmask_b32_e32 v238, v238, v241, vcc
	v_cndmask_b32_e32 v239, v239, v242, vcc
	v_cmp_lt_u32_e32 vcc, 23, v225
	v_fma_f32 v241, v232, v238, v160
	v_fma_f32 v242, v234, v238, v161
	v_fmac_f32_e32 v241, v233, v239
	v_fmac_f32_e32 v242, v235, v239
	v_cndmask_b32_e32 v238, v238, v241, vcc
	v_cndmask_b32_e32 v239, v239, v242, vcc
	v_cmp_lt_u32_e32 vcc, 24, v225
	v_fma_f32 v241, v232, v238, v162
	v_fma_f32 v242, v234, v238, v163
	v_fmac_f32_e32 v241, v233, v239
	v_fmac_f32_e32 v242, v235, v239
	v_cndmask_b32_e32 v238, v238, v241, vcc
	v_cndmask_b32_e32 v239, v239, v242, vcc
	v_cmp_lt_u32_e32 vcc, 25, v225
	v_fma_f32 v241, v232, v238, v164
	v_fma_f32 v242, v234, v238, v165
	v_fmac_f32_e32 v241, v233, v239
	v_fmac_f32_e32 v242, v235, v239
	v_cndmask_b32_e32 v238, v238, v241, vcc
	v_cndmask_b32_e32 v239, v239, v242, vcc
	v_cmp_lt_u32_e32 vcc, 26, v225
	v_fma_f32 v241, v232, v238, v166
	v_fma_f32 v242, v234, v238, v167
	v_fmac_f32_e32 v241, v233, v239
	v_fmac_f32_e32 v242, v235, v239
	v_cndmask_b32_e32 v238, v238, v241, vcc
	v_cndmask_b32_e32 v239, v239, v242, vcc
	v_cmp_lt_u32_e32 vcc, 27, v225
	v_fma_f32 v241, v232, v238, v168
	v_fma_f32 v242, v234, v238, v169
	v_fmac_f32_e32 v241, v233, v239
	v_fmac_f32_e32 v242, v235, v239
	v_cndmask_b32_e32 v238, v238, v241, vcc
	v_cndmask_b32_e32 v239, v239, v242, vcc
	v_cmp_lt_u32_e32 vcc, 28, v225
	v_fma_f32 v241, v232, v238, v170
	v_fma_f32 v242, v234, v238, v171
	v_fmac_f32_e32 v241, v233, v239
	v_fmac_f32_e32 v242, v235, v239
	v_cndmask_b32_e32 v238, v238, v241, vcc
	v_cndmask_b32_e32 v239, v239, v242, vcc
	v_cmp_lt_u32_e32 vcc, 29, v225
	v_fma_f32 v241, v232, v238, v172
	v_fma_f32 v242, v234, v238, v173
	v_fmac_f32_e32 v241, v233, v239
	v_fmac_f32_e32 v242, v235, v239
	v_cndmask_b32_e32 v238, v238, v241, vcc
	v_cndmask_b32_e32 v239, v239, v242, vcc
	v_cmp_lt_u32_e32 vcc, 30, v225
	v_fma_f32 v241, v232, v238, v174
	v_fma_f32 v242, v234, v238, v175
	v_fmac_f32_e32 v241, v233, v239
	v_fmac_f32_e32 v242, v235, v239
	v_cndmask_b32_e32 v238, v238, v241, vcc
	v_cndmask_b32_e32 v239, v239, v242, vcc
	v_cmp_lt_u32_e32 vcc, 31, v225
	v_fma_f32 v241, v232, v238, v176
	v_fma_f32 v242, v234, v238, v177
	v_fmac_f32_e32 v241, v233, v239
	v_fmac_f32_e32 v242, v235, v239
	v_cndmask_b32_e32 v238, v238, v241, vcc
	v_cndmask_b32_e32 v239, v239, v242, vcc
	ds_bpermute_b32 v247, v224, v238
	ds_bpermute_b32 v248, v224, v239
	s_waitcnt lgkmcnt(0)
	v_cndmask_b32_e64 v249, v238, v247, s[46:47]
	v_cndmask_b32_e64 v250, v239, v248, s[46:47]
	v_cndmask_b32_e64 v251, v247, v238, s[46:47]
	v_cndmask_b32_e64 v252, v248, v239, s[46:47]
	s_sub_i32 s44, s18, 32
	s_cmp_gt_i32 s44, 0
	s_cbranch_scc0 .Llb_np_3

.Llb_np_3:
	v_add_f32_e32 v238, v249, v251
	v_add_f32_e32 v239, v250, v252
	v_fma_f32 v245, v228, v238, v236
	v_fma_f32 v246, v230, v238, v237
	v_fmac_f32_e32 v245, v229, v239
	v_fmac_f32_e32 v246, v231, v239
	v_cndmask_b32_e64 v220, v238, v245, s[46:47]
	v_cndmask_b32_e64 v221, v239, v246, s[46:47]
	v_lshl_add_u32 v215, v212, 17, v223
	v_add_u32_e32 v215, 0x1180, v215
	v_fma_f32 v222, -v221, v219, v2
	v_fmac_f32_e32 v220, 0x3dcccccd, v222
	v_fmac_f32_e32 v221, 0x3dcccccd, v220
	global_store_dword v215, v221, s[30:31] offset:-4096
	global_store_dword v215, v220, s[32:33] offset:-4096
	global_store_dword v215, v221, s[34:35] offset:-4096
	v_fma_f32 v222, -v221, v219, v3
	v_fmac_f32_e32 v220, 0x3dcccccd, v222
	v_fmac_f32_e32 v221, 0x3dcccccd, v220
	global_store_dword v215, v221, s[30:31]
	global_store_dword v215, v220, s[32:33]
	global_store_dword v215, v221, s[34:35]
	v_add_u32_e32 v215, 0x2000, v215
	v_fma_f32 v222, -v221, v219, v4
	v_fmac_f32_e32 v220, 0x3dcccccd, v222
	v_fmac_f32_e32 v221, 0x3dcccccd, v220
	global_store_dword v215, v221, s[30:31] offset:-4096
	global_store_dword v215, v220, s[32:33] offset:-4096
	global_store_dword v215, v221, s[34:35] offset:-4096
	v_fma_f32 v222, -v221, v219, v5
	v_fmac_f32_e32 v220, 0x3dcccccd, v222
	v_fmac_f32_e32 v221, 0x3dcccccd, v220
	global_store_dword v215, v221, s[30:31]
	global_store_dword v215, v220, s[32:33]
	global_store_dword v215, v221, s[34:35]
	v_add_u32_e32 v215, 0x2000, v215
	v_fma_f32 v222, -v221, v219, v6
	v_fmac_f32_e32 v220, 0x3dcccccd, v222
	v_fmac_f32_e32 v221, 0x3dcccccd, v220
	global_store_dword v215, v221, s[30:31] offset:-4096
	global_store_dword v215, v220, s[32:33] offset:-4096
	global_store_dword v215, v221, s[34:35] offset:-4096
	v_fma_f32 v222, -v221, v219, v7
	v_fmac_f32_e32 v220, 0x3dcccccd, v222
	v_fmac_f32_e32 v221, 0x3dcccccd, v220
	global_store_dword v215, v221, s[30:31]
	global_store_dword v215, v220, s[32:33]
	global_store_dword v215, v221, s[34:35]
	v_add_u32_e32 v215, 0x2000, v215
	v_fma_f32 v222, -v221, v219, v8
	v_fmac_f32_e32 v220, 0x3dcccccd, v222
	v_fmac_f32_e32 v221, 0x3dcccccd, v220
	global_store_dword v215, v221, s[30:31] offset:-4096
	global_store_dword v215, v220, s[32:33] offset:-4096
	global_store_dword v215, v221, s[34:35] offset:-4096
	v_fma_f32 v222, -v221, v219, v9
	v_fmac_f32_e32 v220, 0x3dcccccd, v222
	v_fmac_f32_e32 v221, 0x3dcccccd, v220
	global_store_dword v215, v221, s[30:31]
	global_store_dword v215, v220, s[32:33]
	global_store_dword v215, v221, s[34:35]
	v_add_u32_e32 v215, 0x2000, v215
	v_fma_f32 v222, -v221, v219, v10
	v_fmac_f32_e32 v220, 0x3dcccccd, v222
	v_fmac_f32_e32 v221, 0x3dcccccd, v220
	global_store_dword v215, v221, s[30:31] offset:-4096
	global_store_dword v215, v220, s[32:33] offset:-4096
	global_store_dword v215, v221, s[34:35] offset:-4096
	v_fma_f32 v222, -v221, v219, v11
	v_fmac_f32_e32 v220, 0x3dcccccd, v222
	v_fmac_f32_e32 v221, 0x3dcccccd, v220
	global_store_dword v215, v221, s[30:31]
	global_store_dword v215, v220, s[32:33]
	global_store_dword v215, v221, s[34:35]
	v_add_u32_e32 v215, 0x2000, v215
	v_fma_f32 v222, -v221, v219, v12
	v_fmac_f32_e32 v220, 0x3dcccccd, v222
	v_fmac_f32_e32 v221, 0x3dcccccd, v220
	global_store_dword v215, v221, s[30:31] offset:-4096
	global_store_dword v215, v220, s[32:33] offset:-4096
	global_store_dword v215, v221, s[34:35] offset:-4096
	v_fma_f32 v222, -v221, v219, v13
	v_fmac_f32_e32 v220, 0x3dcccccd, v222
	v_fmac_f32_e32 v221, 0x3dcccccd, v220
	global_store_dword v215, v221, s[30:31]
	global_store_dword v215, v220, s[32:33]
	global_store_dword v215, v221, s[34:35]
	v_add_u32_e32 v215, 0x2000, v215
	v_fma_f32 v222, -v221, v219, v14
	v_fmac_f32_e32 v220, 0x3dcccccd, v222
	v_fmac_f32_e32 v221, 0x3dcccccd, v220
	global_store_dword v215, v221, s[30:31] offset:-4096
	global_store_dword v215, v220, s[32:33] offset:-4096
	global_store_dword v215, v221, s[34:35] offset:-4096
	v_fma_f32 v222, -v221, v219, v15
	v_fmac_f32_e32 v220, 0x3dcccccd, v222
	v_fmac_f32_e32 v221, 0x3dcccccd, v220
	global_store_dword v215, v221, s[30:31]
	global_store_dword v215, v220, s[32:33]
	global_store_dword v215, v221, s[34:35]
	v_add_u32_e32 v215, 0x2000, v215
	v_fma_f32 v222, -v221, v219, v16
	v_fmac_f32_e32 v220, 0x3dcccccd, v222
	v_fmac_f32_e32 v221, 0x3dcccccd, v220
	global_store_dword v215, v221, s[30:31] offset:-4096
	global_store_dword v215, v220, s[32:33] offset:-4096
	global_store_dword v215, v221, s[34:35] offset:-4096
	v_fma_f32 v222, -v221, v219, v17
	v_fmac_f32_e32 v220, 0x3dcccccd, v222
	v_fmac_f32_e32 v221, 0x3dcccccd, v220
	global_store_dword v215, v221, s[30:31]
	global_store_dword v215, v220, s[32:33]
	global_store_dword v215, v221, s[34:35]
	v_add_u32_e32 v215, 0x2000, v215
	v_fma_f32 v222, -v221, v219, v18
	v_fmac_f32_e32 v220, 0x3dcccccd, v222
	v_fmac_f32_e32 v221, 0x3dcccccd, v220
	global_store_dword v215, v221, s[30:31] offset:-4096
	global_store_dword v215, v220, s[32:33] offset:-4096
	global_store_dword v215, v221, s[34:35] offset:-4096
	v_fma_f32 v222, -v221, v219, v19
	v_fmac_f32_e32 v220, 0x3dcccccd, v222
	v_fmac_f32_e32 v221, 0x3dcccccd, v220
	global_store_dword v215, v221, s[30:31]
	global_store_dword v215, v220, s[32:33]
	global_store_dword v215, v221, s[34:35]
	v_add_u32_e32 v215, 0x2000, v215
	v_fma_f32 v222, -v221, v219, v20
	v_fmac_f32_e32 v220, 0x3dcccccd, v222
	v_fmac_f32_e32 v221, 0x3dcccccd, v220
	global_store_dword v215, v221, s[30:31] offset:-4096
	global_store_dword v215, v220, s[32:33] offset:-4096
	global_store_dword v215, v221, s[34:35] offset:-4096
	v_fma_f32 v222, -v221, v219, v21
	v_fmac_f32_e32 v220, 0x3dcccccd, v222
	v_fmac_f32_e32 v221, 0x3dcccccd, v220
	global_store_dword v215, v221, s[30:31]
	global_store_dword v215, v220, s[32:33]
	global_store_dword v215, v221, s[34:35]
	v_add_u32_e32 v215, 0x2000, v215
	v_fma_f32 v222, -v221, v219, v22
	v_fmac_f32_e32 v220, 0x3dcccccd, v222
	v_fmac_f32_e32 v221, 0x3dcccccd, v220
	global_store_dword v215, v221, s[30:31] offset:-4096
	global_store_dword v215, v220, s[32:33] offset:-4096
	global_store_dword v215, v221, s[34:35] offset:-4096
	v_fma_f32 v222, -v221, v219, v23
	v_fmac_f32_e32 v220, 0x3dcccccd, v222
	v_fmac_f32_e32 v221, 0x3dcccccd, v220
	global_store_dword v215, v221, s[30:31]
	global_store_dword v215, v220, s[32:33]
	global_store_dword v215, v221, s[34:35]
	v_add_u32_e32 v215, 0x2000, v215
	v_fma_f32 v222, -v221, v219, v24
	v_fmac_f32_e32 v220, 0x3dcccccd, v222
	v_fmac_f32_e32 v221, 0x3dcccccd, v220
	global_store_dword v215, v221, s[30:31] offset:-4096
	global_store_dword v215, v220, s[32:33] offset:-4096
	global_store_dword v215, v221, s[34:35] offset:-4096
	v_fma_f32 v222, -v221, v219, v25
	v_fmac_f32_e32 v220, 0x3dcccccd, v222
	v_fmac_f32_e32 v221, 0x3dcccccd, v220
	global_store_dword v215, v221, s[30:31]
	global_store_dword v215, v220, s[32:33]
	global_store_dword v215, v221, s[34:35]
	v_add_u32_e32 v215, 0x2000, v215
	v_fma_f32 v222, -v221, v219, v26
	v_fmac_f32_e32 v220, 0x3dcccccd, v222
	v_fmac_f32_e32 v221, 0x3dcccccd, v220
	global_store_dword v215, v221, s[30:31] offset:-4096
	global_store_dword v215, v220, s[32:33] offset:-4096
	global_store_dword v215, v221, s[34:35] offset:-4096
	v_fma_f32 v222, -v221, v219, v27
	v_fmac_f32_e32 v220, 0x3dcccccd, v222
	v_fmac_f32_e32 v221, 0x3dcccccd, v220
	global_store_dword v215, v221, s[30:31]
	global_store_dword v215, v220, s[32:33]
	global_store_dword v215, v221, s[34:35]
	v_add_u32_e32 v215, 0x2000, v215
	v_fma_f32 v222, -v221, v219, v28
	v_fmac_f32_e32 v220, 0x3dcccccd, v222
	v_fmac_f32_e32 v221, 0x3dcccccd, v220
	global_store_dword v215, v221, s[30:31] offset:-4096
	global_store_dword v215, v220, s[32:33] offset:-4096
	global_store_dword v215, v221, s[34:35] offset:-4096
	v_fma_f32 v222, -v221, v219, v29
	v_fmac_f32_e32 v220, 0x3dcccccd, v222
	v_fmac_f32_e32 v221, 0x3dcccccd, v220
	global_store_dword v215, v221, s[30:31]
	global_store_dword v215, v220, s[32:33]
	global_store_dword v215, v221, s[34:35]
	v_add_u32_e32 v215, 0x2000, v215
	v_fma_f32 v222, -v221, v219, v30
	v_fmac_f32_e32 v220, 0x3dcccccd, v222
	v_fmac_f32_e32 v221, 0x3dcccccd, v220
	global_store_dword v215, v221, s[30:31] offset:-4096
	global_store_dword v215, v220, s[32:33] offset:-4096
	global_store_dword v215, v221, s[34:35] offset:-4096
	v_fma_f32 v222, -v221, v219, v31
	v_fmac_f32_e32 v220, 0x3dcccccd, v222
	v_fmac_f32_e32 v221, 0x3dcccccd, v220
	global_store_dword v215, v221, s[30:31]
	global_store_dword v215, v220, s[32:33]
	global_store_dword v215, v221, s[34:35]
	v_add_u32_e32 v215, 0x2000, v215
	v_fma_f32 v222, -v221, v219, v32
	v_fmac_f32_e32 v220, 0x3dcccccd, v222
	v_fmac_f32_e32 v221, 0x3dcccccd, v220
	global_store_dword v215, v221, s[30:31] offset:-4096
	global_store_dword v215, v220, s[32:33] offset:-4096
	global_store_dword v215, v221, s[34:35] offset:-4096
	v_fma_f32 v222, -v221, v219, v33
	v_fmac_f32_e32 v220, 0x3dcccccd, v222
	v_fmac_f32_e32 v221, 0x3dcccccd, v220
	global_store_dword v215, v221, s[30:31]
	global_store_dword v215, v220, s[32:33]
	global_store_dword v215, v221, s[34:35]
	v_add_u32_e32 v215, 0x2000, v215
	s_endpgm

	.amdhsa_kernel _Z9fused_oscPKfS0_PK15HIP_vector_typeIjLj4EEPfPyPj
		.amdhsa_group_segment_fixed_size 0
		.amdhsa_private_segment_fixed_size 0
		.amdhsa_kernarg_size 48
		.amdhsa_user_sgpr_count 2
		.amdhsa_user_sgpr_dispatch_ptr 0
		.amdhsa_user_sgpr_queue_ptr 0
		.amdhsa_user_sgpr_kernarg_segment_ptr 1
		.amdhsa_user_sgpr_dispatch_id 0
		.amdhsa_user_sgpr_kernarg_preload_length 0
		.amdhsa_user_sgpr_kernarg_preload_offset 0
		.amdhsa_user_sgpr_private_segment_size 0
		.amdhsa_uses_dynamic_stack 0
		.amdhsa_enable_private_segment 0
		.amdhsa_system_sgpr_workgroup_id_x 1
		.amdhsa_system_sgpr_workgroup_id_y 0
		.amdhsa_system_sgpr_workgroup_id_z 0
		.amdhsa_system_sgpr_workgroup_info 0
		.amdhsa_system_vgpr_workitem_id 0
		.amdhsa_next_free_vgpr 256
		.amdhsa_next_free_sgpr 64
		.amdhsa_accum_offset 256
		.amdhsa_reserve_vcc 1
		.amdhsa_float_round_mode_32 0
		.amdhsa_float_round_mode_16_64 0
		.amdhsa_float_denorm_mode_32 3
		.amdhsa_float_denorm_mode_16_64 3
		.amdhsa_dx10_clamp 1
		.amdhsa_ieee_mode 1
		.amdhsa_fp16_overflow 0
		.amdhsa_tg_split 0
		.amdhsa_exception_fp_ieee_invalid_op 0
		.amdhsa_exception_fp_denorm_src 0
		.amdhsa_exception_fp_ieee_div_zero 0
		.amdhsa_exception_fp_ieee_overflow 0
		.amdhsa_exception_fp_ieee_underflow 0
		.amdhsa_exception_fp_ieee_inexact 0
		.amdhsa_exception_int_div_zero 0
	.end_amdhsa_kernel

amdhsa.kernels:
  - .agpr_count:     0
    .args:
      - .actual_access:  read_only
        .address_space:  global
        .offset:         0
        .size:           8
        .value_kind:     global_buffer
      - .actual_access:  write_only
        .address_space:  global
        .offset:         8
        .size:           8
        .value_kind:     global_buffer
      - .address_space:  global
        .offset:         16
        .size:           8
        .value_kind:     global_buffer
      - .address_space:  global
        .offset:         24
        .size:           8
        .value_kind:     global_buffer
    .group_segment_fixed_size: 0
    .kernarg_segment_align: 8
    .kernarg_segment_size: 32
    .language:       OpenCL C
    .language_version:
      - 2
      - 0
    .max_flat_workgroup_size: 256
    .name:           _Z9convert_wPKfP15HIP_vector_typeIjLj4EEPjPy
    .private_segment_fixed_size: 0
    .sgpr_count:     18
    .sgpr_spill_count: 0
    .symbol:         _Z9convert_wPKfP15HIP_vector_typeIjLj4EEPjPy.kd
    .uniform_work_group_size: 1
    .uses_dynamic_stack: false
    .vgpr_count:     24
    .vgpr_spill_count: 0
    .wavefront_size: 64
  - .agpr_count:     0
    .args:
      - .actual_access:  read_only
        .address_space:  global
        .offset:         0
        .size:           8
        .value_kind:     global_buffer
      - .actual_access:  read_only
        .address_space:  global
        .offset:         8
        .size:           8
        .value_kind:     global_buffer
      - .address_space:  global
        .offset:         16
        .size:           8
        .value_kind:     global_buffer
      - .actual_access:  write_only
        .address_space:  global
        .offset:         24
        .size:           8
        .value_kind:     global_buffer
      - .address_space:  global
        .offset:         32
        .size:           8
        .value_kind:     global_buffer
      - .address_space:  global
        .offset:         40
        .size:           8
        .value_kind:     global_buffer
    .group_segment_fixed_size: 0
    .kernarg_segment_align: 8
    .kernarg_segment_size: 48
    .language:       OpenCL C
    .language_version:
      - 2
      - 0
    .max_flat_workgroup_size: 512
    .name:           _Z9fused_oscPKfS0_PK15HIP_vector_typeIjLj4EEPfPyPj
    .private_segment_fixed_size: 0
    .sgpr_count:     70
    .sgpr_spill_count: 0
    .symbol:         _Z9fused_oscPKfS0_PK15HIP_vector_typeIjLj4EEPfPyPj.kd
    .uniform_work_group_size: 1
    .uses_dynamic_stack: false
    .vgpr_count:     256
    .vgpr_spill_count: 0
    .wavefront_size: 64
